# v11 with the LDS-DMA stage loads placed after MFMAs 1-4 of each phase instead of 2,3,5,6
# baseline (speedup 1.0000x reference)
.LBB0_249:
	s_add_u32 s31, s26, 0xfffc0080
	s_addc_u32 s33, s27, -1
	s_add_i32 s34, 0, 0x10000
	v_add_u32_e32 v0, s34, v138
	ds_read_b128 v[140:143], v0
	ds_read_b128 v[144:147], v0 offset:1024
	ds_read_b128 v[148:151], v0 offset:2048
	ds_read_b128 v[152:155], v0 offset:3072
	s_cmp_eq_u32 s30, 12
	s_cselect_b32 s49, s3, s33
	s_cselect_b32 s48, s5, s31
	s_cselect_b32 s47, s20, s25
	s_cselect_b32 s46, s21, s22
	v_mov_b32_e32 v0, v136
	ds_read_b128 v[156:159], v139
	ds_read_b128 v[160:163], v139 offset:1024
	ds_read_b128 v[172:175], v139 offset:2048
	ds_read_b128 v[176:179], v139 offset:3072
	ds_read_b128 v[180:183], v139 offset:4096
	ds_read_b128 v[184:187], v139 offset:5120
	ds_read_b128 v[188:191], v139 offset:6144
	ds_read_b128 v[192:195], v139 offset:7168
	s_nop 0
	v_mov_b32_e32 v0, v137
	s_nop 0
	s_waitcnt lgkmcnt(8)
	s_barrier
	s_waitcnt lgkmcnt(0)
	s_setprio 1
	v_mov_b64_e32 v[50:51], v[164:165]
	s_waitcnt lgkmcnt(0)
	v_mfma_scale_f32_16x16x128_f8f6f4 v[98:101], v[156:163], v[148:155], v[98:101], v202, v202 op_sel_hi:[0,0,0]
	s_add_i32 m0, s1, 0xc000
	v_mov_b64_e32 v[52:53], v[166:167]
	v_mfma_scale_f32_16x16x128_f8f6f4 v[164:167], v[172:179], v[140:147], v[118:121], v202, v202 op_sel_hi:[0,0,0]
	global_load_lds_dwordx4 v136, s[26:27]
	v_mfma_scale_f32_16x16x128_f8f6f4 v[90:93], v[180:187], v[148:155], v[90:93], v202, v202 op_sel_hi:[0,0,0]
	s_add_i32 m0, s1, 0xe000
	v_mfma_scale_f32_16x16x128_f8f6f4 v[130:133], v[156:163], v[140:147], v[126:129], v202, v202 op_sel_hi:[0,0,0]
	global_load_lds_dwordx4 v137, s[26:27]
	v_mfma_scale_f32_16x16x128_f8f6f4 v[168:171], v[172:179], v[148:155], v[86:89], v202, v202 op_sel_hi:[0,0,0]
	v_mfma_scale_f32_16x16x128_f8f6f4 v[196:199], v[180:187], v[140:147], v[122:125], v202, v202 op_sel_hi:[0,0,0]
	v_mfma_scale_f32_16x16x128_f8f6f4 v[206:209], v[188:195], v[140:147], v[114:117], v202, v202 op_sel_hi:[0,0,0]
	v_mfma_scale_f32_16x16x128_f8f6f4 v[210:213], v[188:195], v[148:155], v[82:85], v202, v202 op_sel_hi:[0,0,0]
	s_setprio 0
	s_barrier
	s_add_i32 s31, 0, 0x14000
	v_add_u32_e32 v0, s31, v138
	s_nop 2
	ds_read_b128 v[82:85], v0
	ds_read_b128 v[86:89], v0 offset:1024
	ds_read_b128 v[114:117], v0 offset:2048
	ds_read_b128 v[118:121], v0 offset:3072
	v_mov_b32_e32 v0, v136
	s_add_i32 s33, s34, s73
	s_nop 0
	v_mov_b32_e32 v0, v137
	s_nop 0
	s_barrier
	s_waitcnt lgkmcnt(0)
	s_setprio 1
	s_waitcnt lgkmcnt(0)
	v_mfma_scale_f32_16x16x128_f8f6f4 v[66:69], v[156:163], v[82:89], v[66:69], v202, v202 op_sel_hi:[0,0,0]
	s_mov_b32 m0, s33
	v_mfma_scale_f32_16x16x128_f8f6f4 v[38:41], v[156:163], v[114:121], v[38:41], v202, v202 op_sel_hi:[0,0,0]
	global_load_lds_dwordx4 v136, s[46:47]
	v_mfma_scale_f32_16x16x128_f8f6f4 v[58:61], v[180:187], v[82:89], v[58:61], v202, v202 op_sel_hi:[0,0,0]
	s_add_i32 m0, s33, 0x2000
	v_mfma_scale_f32_16x16x128_f8f6f4 v[214:217], v[172:179], v[82:89], v[54:57], v202, v202 op_sel_hi:[0,0,0]
	global_load_lds_dwordx4 v137, s[46:47]
	v_mfma_scale_f32_16x16x128_f8f6f4 v[172:175], v[172:179], v[114:121], v[22:25], v202, v202 op_sel_hi:[0,0,0]
	v_mfma_scale_f32_16x16x128_f8f6f4 v[176:179], v[180:187], v[114:121], v[30:33], v202, v202 op_sel_hi:[0,0,0]
	v_mfma_scale_f32_16x16x128_f8f6f4 v[180:183], v[188:195], v[82:89], v[18:21], v202, v202 op_sel_hi:[0,0,0]
	v_mfma_scale_f32_16x16x128_f8f6f4 v[184:187], v[188:195], v[114:121], v[50:53], v202, v202 op_sel_hi:[0,0,0]
	s_setprio 0
	v_mov_b32_e32 v0, v136
	s_barrier
	s_nop 1
	ds_read_b128 v[18:21], v139 offset:16384
	ds_read_b128 v[22:25], v139 offset:17408
	ds_read_b128 v[50:53], v139 offset:18432
	ds_read_b128 v[54:57], v139 offset:19456
	ds_read_b128 v[122:125], v139 offset:20480
	ds_read_b128 v[126:129], v139 offset:21504
	ds_read_b128 v[156:159], v139 offset:22528
	ds_read_b128 v[160:163], v139 offset:23552
	s_nop 0
	v_mov_b32_e32 v0, v137
	s_nop 0
	s_barrier
	s_waitcnt lgkmcnt(0)
	s_setprio 1
	s_waitcnt lgkmcnt(0)
	v_mfma_scale_f32_16x16x128_f8f6f4 v[110:113], v[18:25], v[140:147], v[110:113], v202, v202 op_sel_hi:[0,0,0]
	s_mov_b32 m0, s1
	v_mfma_scale_f32_16x16x128_f8f6f4 v[78:81], v[18:25], v[148:155], v[78:81], v202, v202 op_sel_hi:[0,0,0]
	global_load_lds_dwordx4 v136, s[48:49]
	v_mfma_scale_f32_16x16x128_f8f6f4 v[102:105], v[50:57], v[140:147], v[102:105], v202, v202 op_sel_hi:[0,0,0]
	s_mov_b32 m0, s13
	v_mfma_scale_f32_16x16x128_f8f6f4 v[106:109], v[122:129], v[140:147], v[106:109], v202, v202 op_sel_hi:[0,0,0]
	global_load_lds_dwordx4 v137, s[48:49]
	v_mfma_scale_f32_16x16x128_f8f6f4 v[94:97], v[156:163], v[140:147], v[94:97], v202, v202 op_sel_hi:[0,0,0]
	v_mfma_scale_f32_16x16x128_f8f6f4 v[62:65], v[156:163], v[148:155], v[62:65], v202, v202 op_sel_hi:[0,0,0]
	v_mfma_scale_f32_16x16x128_f8f6f4 v[218:221], v[50:57], v[148:155], v[70:73], v202, v202 op_sel_hi:[0,0,0]
	v_mfma_scale_f32_16x16x128_f8f6f4 v[222:225], v[122:129], v[148:155], v[74:77], v202, v202 op_sel_hi:[0,0,0]
	s_setprio 0
	s_barrier
	s_add_u32 s34, s46, 0x40000
	s_addc_u32 s35, s47, 0
	v_mov_b32_e32 v0, v136
	s_add_i32 s31, s31, s73
	s_mov_b32 s100, s31
	s_nop 0
	v_mov_b32_e32 v0, v137
	s_add_i32 s101, s31, 0x2000
	s_nop 0
	s_waitcnt vmcnt(4)
	s_barrier
	s_setprio 1
	v_mfma_scale_f32_16x16x128_f8f6f4 v[34:37], v[50:57], v[82:89], v[34:37], v202, v202 op_sel_hi:[0,0,0]
	s_mov_b32 m0, s100
	v_mfma_scale_f32_16x16x128_f8f6f4 v[226:229], v[18:25], v[82:89], v[46:49], v202, v202 op_sel_hi:[0,0,0]
	global_load_lds_dwordx4 v136, s[34:35]
	v_mfma_scale_f32_16x16x128_f8f6f4 v[230:233], v[18:25], v[114:121], v[14:17], v202, v202 op_sel_hi:[0,0,0]
	s_mov_b32 m0, s101
	v_mfma_scale_f32_16x16x128_f8f6f4 v[234:237], v[50:57], v[114:121], v[6:9], v202, v202 op_sel_hi:[0,0,0]
	global_load_lds_dwordx4 v137, s[34:35]
	v_mfma_scale_f32_16x16x128_f8f6f4 v[238:241], v[122:129], v[82:89], v[42:45], v202, v202 op_sel_hi:[0,0,0]
	v_mfma_scale_f32_16x16x128_f8f6f4 v[242:245], v[122:129], v[114:121], v[10:13], v202, v202 op_sel_hi:[0,0,0]
	v_mfma_scale_f32_16x16x128_f8f6f4 v[246:249], v[156:163], v[82:89], v[26:29], v202, v202 op_sel_hi:[0,0,0]
	v_mfma_scale_f32_16x16x128_f8f6f4 v[50:53], v[156:163], v[114:121], v[2:5], v202, v202 op_sel_hi:[0,0,0]
	s_setprio 0
	s_add_i32 s31, 0, 0x18000
	v_add_u32_e32 v0, s31, v138
	s_barrier
	s_nop 2
	ds_read_b128 v[2:5], v0
	ds_read_b128 v[6:9], v0 offset:1024
	ds_read_b128 v[10:13], v0 offset:2048
	ds_read_b128 v[14:17], v0 offset:3072
	s_add_u32 s34, s48, 0x40000
	v_mov_b32_e32 v0, v136
	ds_read_b128 v[18:21], v139 offset:32768
	ds_read_b128 v[22:25], v139 offset:33792
	ds_read_b128 v[26:29], v139 offset:34816
	ds_read_b128 v[30:33], v139 offset:35840
	ds_read_b128 v[42:45], v139 offset:36864
	ds_read_b128 v[46:49], v139 offset:37888
	ds_read_b128 v[70:73], v139 offset:38912
	ds_read_b128 v[74:77], v139 offset:39936
	s_addc_u32 s35, s49, 0
	s_nop 0
	v_mov_b32_e32 v0, v137
	s_nop 0
	s_waitcnt lgkmcnt(8)
	s_barrier
	s_waitcnt lgkmcnt(0)
	s_setprio 1
	s_waitcnt lgkmcnt(0)
	v_mfma_scale_f32_16x16x128_f8f6f4 v[126:129], v[18:25], v[2:9], v[130:133], v202, v202 op_sel_hi:[0,0,0]
	s_mov_b32 m0, s14
	v_mfma_scale_f32_16x16x128_f8f6f4 v[98:101], v[18:25], v[10:17], v[98:101], v202, v202 op_sel_hi:[0,0,0]
	global_load_lds_dwordx4 v136, s[34:35]
	v_mfma_scale_f32_16x16x128_f8f6f4 v[118:121], v[26:33], v[2:9], v[164:167], v202, v202 op_sel_hi:[0,0,0]
	s_mov_b32 m0, s15
	v_mfma_scale_f32_16x16x128_f8f6f4 v[86:89], v[26:33], v[10:17], v[168:171], v202, v202 op_sel_hi:[0,0,0]
	global_load_lds_dwordx4 v137, s[34:35]
	v_mfma_scale_f32_16x16x128_f8f6f4 v[122:125], v[42:49], v[2:9], v[196:199], v202, v202 op_sel_hi:[0,0,0]
	v_mfma_scale_f32_16x16x128_f8f6f4 v[90:93], v[42:49], v[10:17], v[90:93], v202, v202 op_sel_hi:[0,0,0]
	v_mfma_scale_f32_16x16x128_f8f6f4 v[114:117], v[70:77], v[2:9], v[206:209], v202, v202 op_sel_hi:[0,0,0]
	v_mfma_scale_f32_16x16x128_f8f6f4 v[82:85], v[70:77], v[10:17], v[210:213], v202, v202 op_sel_hi:[0,0,0]
	s_setprio 0
	s_barrier
	s_add_i32 s33, 0, 0x1c000
	v_add_u32_e32 v0, s33, v138
	ds_read_b128 v[140:143], v0
	ds_read_b128 v[144:147], v0 offset:1024
	ds_read_b128 v[148:151], v0 offset:2048
	ds_read_b128 v[152:155], v0 offset:3072
	v_mov_b32_e32 v0, v136
	s_add_i32 s31, s31, s73
	v_lshl_add_u64 v[54:55], s[46:47], 0, v[0:1]
	v_lshl_add_u64 v[54:55], v[54:55], 0, s[66:67]
	v_mov_b32_e32 v0, v137
	v_lshl_add_u64 v[54:55], s[46:47], 0, v[0:1]
	v_lshl_add_u64 v[54:55], v[54:55], 0, s[66:67]
	s_barrier
	s_waitcnt lgkmcnt(0)
	s_setprio 1
	s_waitcnt lgkmcnt(0)
	v_mfma_scale_f32_16x16x128_f8f6f4 v[66:69], v[18:25], v[140:147], v[66:69], v202, v202 op_sel_hi:[0,0,0]
	s_add_u32 s98, s46, s66
	s_addc_u32 s99, s47, s67
	s_mov_b32 m0, s31
	v_mfma_scale_f32_16x16x128_f8f6f4 v[38:41], v[18:25], v[148:155], v[38:41], v202, v202 op_sel_hi:[0,0,0]
	global_load_lds_dwordx4 v136, s[98:99]
	v_mfma_scale_f32_16x16x128_f8f6f4 v[54:57], v[26:33], v[140:147], v[214:217], v202, v202 op_sel_hi:[0,0,0]
	s_add_i32 m0, s31, 0x2000
	v_mfma_scale_f32_16x16x128_f8f6f4 v[22:25], v[26:33], v[148:155], v[172:175], v202, v202 op_sel_hi:[0,0,0]
	global_load_lds_dwordx4 v137, s[98:99]
	v_mfma_scale_f32_16x16x128_f8f6f4 v[58:61], v[42:49], v[140:147], v[58:61], v202, v202 op_sel_hi:[0,0,0]
	v_mfma_scale_f32_16x16x128_f8f6f4 v[30:33], v[42:49], v[148:155], v[176:179], v202, v202 op_sel_hi:[0,0,0]
	v_mfma_scale_f32_16x16x128_f8f6f4 v[18:21], v[70:77], v[140:147], v[180:183], v202, v202 op_sel_hi:[0,0,0]
	v_mfma_scale_f32_16x16x128_f8f6f4 v[164:167], v[70:77], v[148:155], v[184:187], v202, v202 op_sel_hi:[0,0,0]
	s_setprio 0
	v_mov_b32_e32 v0, v136
	s_barrier
	ds_read_b128 v[156:159], v139 offset:49152
	ds_read_b128 v[160:163], v139 offset:50176
	ds_read_b128 v[172:175], v139 offset:51200
	ds_read_b128 v[176:179], v139 offset:52224
	ds_read_b128 v[180:183], v139 offset:53248
	ds_read_b128 v[184:187], v139 offset:54272
	ds_read_b128 v[188:191], v139 offset:55296
	ds_read_b128 v[192:195], v139 offset:56320
	v_lshl_add_u64 v[26:27], s[48:49], 0, v[0:1]
	v_lshl_add_u64 v[26:27], v[26:27], 0, s[66:67]
	v_mov_b32_e32 v0, v137
	v_lshl_add_u64 v[26:27], s[48:49], 0, v[0:1]
	v_lshl_add_u64 v[26:27], v[26:27], 0, s[66:67]
	s_barrier
	s_waitcnt lgkmcnt(0)
	s_setprio 1
	s_waitcnt lgkmcnt(0)
	v_mfma_scale_f32_16x16x128_f8f6f4 v[110:113], v[156:163], v[2:9], v[110:113], v202, v202 op_sel_hi:[0,0,0]
	s_add_u32 s98, s48, s66
	s_addc_u32 s99, s49, s67
	s_mov_b32 m0, s17
	v_mfma_scale_f32_16x16x128_f8f6f4 v[78:81], v[156:163], v[10:17], v[78:81], v202, v202 op_sel_hi:[0,0,0]
	global_load_lds_dwordx4 v136, s[98:99]
	v_mfma_scale_f32_16x16x128_f8f6f4 v[102:105], v[172:179], v[2:9], v[102:105], v202, v202 op_sel_hi:[0,0,0]
	s_mov_b32 m0, s18
	v_mfma_scale_f32_16x16x128_f8f6f4 v[70:73], v[172:179], v[10:17], v[218:221], v202, v202 op_sel_hi:[0,0,0]
	global_load_lds_dwordx4 v137, s[98:99]
	v_mfma_scale_f32_16x16x128_f8f6f4 v[106:109], v[180:187], v[2:9], v[106:109], v202, v202 op_sel_hi:[0,0,0]
	v_mfma_scale_f32_16x16x128_f8f6f4 v[74:77], v[180:187], v[10:17], v[222:225], v202, v202 op_sel_hi:[0,0,0]
	v_mfma_scale_f32_16x16x128_f8f6f4 v[94:97], v[188:195], v[2:9], v[94:97], v202, v202 op_sel_hi:[0,0,0]
	v_mfma_scale_f32_16x16x128_f8f6f4 v[62:65], v[188:195], v[10:17], v[62:65], v202, v202 op_sel_hi:[0,0,0]
	s_setprio 0
	s_barrier
	s_add_u32 s34, s46, 0x40080
	s_addc_u32 s35, s47, 0
	v_mov_b32_e32 v0, v136
	s_add_i32 s31, s33, s73
	s_nop 0
	v_mov_b32_e32 v0, v137
	s_nop 0
	s_waitcnt vmcnt(4)
	s_barrier
	s_setprio 1
	v_mfma_scale_f32_16x16x128_f8f6f4 v[46:49], v[156:163], v[140:147], v[226:229], v202, v202 op_sel_hi:[0,0,0]
	s_mov_b32 m0, s31
	v_mfma_scale_f32_16x16x128_f8f6f4 v[14:17], v[156:163], v[148:155], v[230:233], v202, v202 op_sel_hi:[0,0,0]
	global_load_lds_dwordx4 v136, s[34:35]
	v_mfma_scale_f32_16x16x128_f8f6f4 v[34:37], v[172:179], v[140:147], v[34:37], v202, v202 op_sel_hi:[0,0,0]
	s_add_i32 m0, s31, 0x2000
	v_mfma_scale_f32_16x16x128_f8f6f4 v[6:9], v[172:179], v[148:155], v[234:237], v202, v202 op_sel_hi:[0,0,0]
	global_load_lds_dwordx4 v137, s[34:35]
	v_mfma_scale_f32_16x16x128_f8f6f4 v[42:45], v[180:187], v[140:147], v[238:241], v202, v202 op_sel_hi:[0,0,0]
	v_mfma_scale_f32_16x16x128_f8f6f4 v[10:13], v[180:187], v[148:155], v[242:245], v202, v202 op_sel_hi:[0,0,0]
	v_mfma_scale_f32_16x16x128_f8f6f4 v[26:29], v[188:195], v[140:147], v[246:249], v202, v202 op_sel_hi:[0,0,0]
	v_mfma_scale_f32_16x16x128_f8f6f4 v[2:5], v[188:195], v[148:155], v[50:53], v202, v202 op_sel_hi:[0,0,0]
	s_setprio 0
	s_add_i32 s30, s30, 2
	s_add_u32 s26, s26, 0x100
	s_addc_u32 s27, s27, 0
	s_add_u32 s22, s22, 0x100
	s_addc_u32 s25, s25, 0
	s_cmp_gt_u32 s30, 13
	s_barrier
	s_cbranch_scc0 .LBB0_249
	s_mul_hi_i32 s3, s24, 0x2aaaaaab
	s_lshr_b32 s5, s3, 31
	s_lshr_b32 s3, s3, 1
	s_add_i32 s3, s3, s5
	s_lshl_b32 s5, s24, 1
	s_and_b32 s5, s5, 6
	s_and_b32 s20, s12, -16
	s_lshl_b32 s3, s3, 3
	s_or_b32 s5, s5, s20
	s_add_i32 s24, s5, s3
	v_readlane_b32 s3, v252, 41
	v_mbcnt_lo_u32_b32 v0, -1, 0
	v_mbcnt_hi_u32_b32 v0, -1, v0
	s_ashr_i32 s25, s24, 31
	s_lshl_b64 s[20:21], s[24:25], 19
	v_and_or_b32 v51, v0, 15, s3
	s_lshl_b32 s3, s12, 8
	s_and_b32 s22, s3, 0xf00
	v_ashrrev_i32_e32 v50, 4, v0
	s_add_u32 s20, s87, s20
	v_readlane_b32 s3, v252, 59
	v_lshlrev_b32_e32 v0, 5, v50
	v_lshlrev_b32_e32 v50, 3, v50
	v_lshlrev_b32_e32 v132, 12, v51
	v_mov_b32_e32 v133, v1
	s_addc_u32 s21, s3, s21
	v_and_b32_e32 v130, -16, v50
	v_lshl_add_u64 v[50:51], s[20:21], 0, v[132:133]
	v_lshl_add_u64 v[50:51], v[50:51], 0, s[22:23]
	v_and_b32_e32 v0, 32, v0
	v_lshl_add_u64 v[50:51], v[50:51], 0, s[28:29]
	v_pk_mul_f32 v[52:53], v[126:127], s[68:69] op_sel_hi:[1,0]
	v_mov_b32_e32 v126, v1
	v_ashrrev_i32_e32 v131, 31, v130
	v_lshl_add_u64 v[50:51], v[50:51], 0, v[0:1]
	v_cvt_pk_fp8_f32 v126, v52, v53
	v_pk_mul_f32 v[52:53], v[122:123], s[68:69] op_sel_hi:[1,0]
	v_mov_b32_e32 v127, v1
	v_lshl_add_u64 v[134:135], v[50:51], 0, v[130:131]
	v_pk_mul_f32 v[50:51], v[128:129], s[68:69] op_sel_hi:[1,0]
	v_cvt_pk_fp8_f32 v127, v52, v53
	v_pk_mul_f32 v[52:53], v[118:119], s[68:69] op_sel_hi:[1,0]
	v_mov_b32_e32 v128, v1
	v_cvt_pk_fp8_f32 v128, v52, v53
	v_pk_mul_f32 v[52:53], v[114:115], s[68:69] op_sel_hi:[1,0]
	v_mov_b32_e32 v129, v1
	v_cvt_pk_fp8_f32 v129, v52, v53
	v_cvt_pk_fp8_f32 v126, v50, v51 op_sel:[0,0,1]
	v_pk_mul_f32 v[50:51], v[124:125], s[68:69] op_sel_hi:[1,0]
	v_pk_mul_f32 v[52:53], v[110:111], s[68:69] op_sel_hi:[1,0]
	v_cvt_pk_fp8_f32 v127, v50, v51 op_sel:[0,0,1]
	v_pk_mul_f32 v[50:51], v[120:121], s[68:69] op_sel_hi:[1,0]
	v_mov_b32_e32 v110, v1
	v_cvt_pk_fp8_f32 v128, v50, v51 op_sel:[0,0,1]
	v_pk_mul_f32 v[50:51], v[116:117], s[68:69] op_sel_hi:[1,0]
	v_cvt_pk_fp8_f32 v110, v52, v53
	v_pk_mul_f32 v[52:53], v[106:107], s[68:69] op_sel_hi:[1,0]
	v_mov_b32_e32 v111, v1
	v_cvt_pk_fp8_f32 v129, v50, v51 op_sel:[0,0,1]
	v_pk_mul_f32 v[50:51], v[112:113], s[68:69] op_sel_hi:[1,0]
	v_cvt_pk_fp8_f32 v111, v52, v53
	v_pk_mul_f32 v[52:53], v[102:103], s[68:69] op_sel_hi:[1,0]
	v_mov_b32_e32 v112, v1
	v_cvt_pk_fp8_f32 v112, v52, v53
	v_cvt_pk_fp8_f32 v110, v50, v51 op_sel:[0,0,1]
	v_pk_mul_f32 v[50:51], v[108:109], s[68:69] op_sel_hi:[1,0]
	v_pk_mul_f32 v[52:53], v[94:95], s[68:69] op_sel_hi:[1,0]
	v_cvt_pk_fp8_f32 v111, v50, v51 op_sel:[0,0,1]
	v_pk_mul_f32 v[50:51], v[104:105], s[68:69] op_sel_hi:[1,0]
	v_mov_b32_e32 v94, v1
	v_cvt_pk_fp8_f32 v112, v50, v51 op_sel:[0,0,1]
	v_pk_mul_f32 v[50:51], v[96:97], s[68:69] op_sel_hi:[1,0]
	v_pk_mul_f32 v[96:97], v[98:99], s[68:69] op_sel_hi:[1,0]
	v_pk_mul_f32 v[90:91], v[90:91], s[68:69] op_sel_hi:[1,0]
	v_cvt_pk_fp8_f32 v94, v96, v97
	v_mov_b32_e32 v95, v1
	v_cvt_pk_fp8_f32 v95, v90, v91
	v_pk_mul_f32 v[86:87], v[86:87], s[68:69] op_sel_hi:[1,0]
	v_mov_b32_e32 v96, v1
	v_mov_b32_e32 v113, v1
	v_cvt_pk_fp8_f32 v96, v86, v87
	v_pk_mul_f32 v[82:83], v[82:83], s[68:69] op_sel_hi:[1,0]
	v_mov_b32_e32 v97, v1
	v_cvt_pk_fp8_f32 v113, v52, v53
	v_pk_mul_f32 v[52:53], v[100:101], s[68:69] op_sel_hi:[1,0]
	v_cvt_pk_fp8_f32 v97, v82, v83
	v_cvt_pk_fp8_f32 v94, v52, v53 op_sel:[0,0,1]
	v_pk_mul_f32 v[52:53], v[92:93], s[68:69] op_sel_hi:[1,0]
	s_mov_b32 s5, 0x10000
	v_cvt_pk_fp8_f32 v95, v52, v53 op_sel:[0,0,1]
	v_pk_mul_f32 v[52:53], v[88:89], s[68:69] op_sel_hi:[1,0]
	v_pk_mul_f32 v[74:75], v[74:75], s[68:69] op_sel_hi:[1,0]
	v_cvt_pk_fp8_f32 v96, v52, v53 op_sel:[0,0,1]
	v_pk_mul_f32 v[52:53], v[84:85], s[68:69] op_sel_hi:[1,0]
	v_permlane32_swap_b32_e32 v94, v95
	v_cvt_pk_fp8_f32 v97, v52, v53 op_sel:[0,0,1]
	v_add_co_u32_e32 v52, vcc, s5, v134
	v_pk_mul_f32 v[70:71], v[70:71], s[68:69] op_sel_hi:[1,0]
	v_permlane32_swap_b32_e32 v96, v97
	v_addc_co_u32_e32 v53, vcc, 0, v135, vcc
	global_store_dwordx4 v[52:53], v[94:97], off
	v_pk_mul_f32 v[52:53], v[80:81], s[68:69] op_sel_hi:[1,0]
	v_pk_mul_f32 v[80:81], v[78:79], s[68:69] op_sel_hi:[1,0]
	v_mov_b32_e32 v78, v1
	v_cvt_pk_fp8_f32 v78, v80, v81
	v_mov_b32_e32 v79, v1
	v_cvt_pk_fp8_f32 v79, v74, v75
	v_mov_b32_e32 v80, v1
	v_cvt_pk_fp8_f32 v80, v70, v71
	v_pk_mul_f32 v[62:63], v[62:63], s[68:69] op_sel_hi:[1,0]
	v_mov_b32_e32 v81, v1
	v_cvt_pk_fp8_f32 v81, v62, v63
	v_cvt_pk_fp8_f32 v78, v52, v53 op_sel:[0,0,1]
	v_pk_mul_f32 v[52:53], v[76:77], s[68:69] op_sel_hi:[1,0]
	v_pk_mul_f32 v[18:19], v[18:19], s[68:69] op_sel_hi:[1,0]
	v_cvt_pk_fp8_f32 v79, v52, v53 op_sel:[0,0,1]
	v_pk_mul_f32 v[52:53], v[72:73], s[68:69] op_sel_hi:[1,0]
	v_pk_mul_f32 v[20:21], v[20:21], s[68:69] op_sel_hi:[1,0]
	v_cvt_pk_fp8_f32 v80, v52, v53 op_sel:[0,0,1]
	v_pk_mul_f32 v[52:53], v[64:65], s[68:69] op_sel_hi:[1,0]
	s_or_b32 s20, s24, 1
	v_cvt_pk_fp8_f32 v81, v52, v53 op_sel:[0,0,1]
	v_pk_mul_f32 v[52:53], v[66:67], s[68:69] op_sel_hi:[1,0]
	v_mov_b32_e32 v67, v1
	v_cvt_pk_fp8_f32 v67, v18, v19
	v_pk_mul_f32 v[18:19], v[48:49], s[68:69] op_sel_hi:[1,0]
	v_mov_b32_e32 v48, v1
	s_ashr_i32 s21, s20, 31
	v_cvt_pk_fp8_f32 v67, v20, v21 op_sel:[0,0,1]
	v_pk_mul_f32 v[20:21], v[46:47], s[68:69] op_sel_hi:[1,0]
	v_mov_b32_e32 v46, v1
	v_cvt_pk_fp8_f32 v46, v20, v21
	v_pk_mul_f32 v[20:21], v[42:43], s[68:69] op_sel_hi:[1,0]
	v_mov_b32_e32 v47, v1
	v_cvt_pk_fp8_f32 v47, v20, v21
	v_pk_mul_f32 v[20:21], v[34:35], s[68:69] op_sel_hi:[1,0]
	v_cvt_pk_fp8_f32 v46, v18, v19 op_sel:[0,0,1]
	v_cvt_pk_fp8_f32 v48, v20, v21
	v_pk_mul_f32 v[18:19], v[44:45], s[68:69] op_sel_hi:[1,0]
	v_pk_mul_f32 v[20:21], v[26:27], s[68:69] op_sel_hi:[1,0]
	v_cvt_pk_fp8_f32 v47, v18, v19 op_sel:[0,0,1]
	v_pk_mul_f32 v[18:19], v[36:37], s[68:69] op_sel_hi:[1,0]
	v_mov_b32_e32 v26, v1
	v_cvt_pk_fp8_f32 v48, v18, v19 op_sel:[0,0,1]
	v_pk_mul_f32 v[18:19], v[28:29], s[68:69] op_sel_hi:[1,0]
	v_pk_mul_f32 v[28:29], v[38:39], s[68:69] op_sel_hi:[1,0]
	v_mov_b32_e32 v27, v1
	v_cvt_pk_fp8_f32 v26, v28, v29
	v_pk_mul_f32 v[28:29], v[30:31], s[68:69] op_sel_hi:[1,0]
	v_pk_mul_f32 v[22:23], v[22:23], s[68:69] op_sel_hi:[1,0]
	v_cvt_pk_fp8_f32 v27, v28, v29
	v_mov_b32_e32 v28, v1
	s_lshl_b64 s[20:21], s[20:21], 19
	v_mov_b32_e32 v49, v1
	v_cvt_pk_fp8_f32 v28, v22, v23
	v_pk_mul_f32 v[22:23], v[164:165], s[68:69] op_sel_hi:[1,0]
	v_mov_b32_e32 v29, v1
	s_mov_b64 s[26:27], 0x10000
	s_add_u32 s20, s87, s20
	v_cvt_pk_fp8_f32 v49, v20, v21
	v_pk_mul_f32 v[20:21], v[40:41], s[68:69] op_sel_hi:[1,0]
	v_cvt_pk_fp8_f32 v29, v22, v23
	v_cvt_pk_fp8_f32 v113, v50, v51 op_sel:[0,0,1]
	v_lshl_add_u64 v[50:51], v[134:135], 0, s[26:27]
	v_permlane32_swap_b32_e32 v78, v79
	v_permlane32_swap_b32_e32 v80, v81
	s_addc_u32 s21, s3, s21
	v_cvt_pk_fp8_f32 v26, v20, v21 op_sel:[0,0,1]
	v_pk_mul_f32 v[20:21], v[32:33], s[68:69] op_sel_hi:[1,0]
	global_store_dwordx4 v[50:51], v[78:81], off offset:128
	v_lshl_add_u64 v[50:51], s[20:21], 0, v[132:133]
	v_cvt_pk_fp8_f32 v27, v20, v21 op_sel:[0,0,1]
	v_pk_mul_f32 v[20:21], v[24:25], s[68:69] op_sel_hi:[1,0]
	v_lshl_add_u64 v[50:51], v[50:51], 0, s[22:23]
	v_cvt_pk_fp8_f32 v28, v20, v21 op_sel:[0,0,1]
	v_pk_mul_f32 v[20:21], v[166:167], s[68:69] op_sel_hi:[1,0]
	v_lshl_add_u64 v[50:51], v[50:51], 0, s[28:29]
	v_cvt_pk_fp8_f32 v29, v20, v21 op_sel:[0,0,1]
	v_lshl_add_u64 v[50:51], v[50:51], 0, v[0:1]
	v_lshl_add_u64 v[62:63], v[50:51], 0, v[130:131]
	v_add_co_u32_e32 v20, vcc, s5, v62
	v_permlane32_swap_b32_e32 v26, v27
	v_permlane32_swap_b32_e32 v28, v29
	v_addc_co_u32_e32 v21, vcc, 0, v63, vcc
	global_store_dwordx4 v[20:21], v[26:29], off
	v_pk_mul_f32 v[20:21], v[14:15], s[68:69] op_sel_hi:[1,0]
	v_mov_b32_e32 v14, v1
	v_cvt_pk_fp8_f32 v14, v20, v21
	v_mov_b32_e32 v64, v1
	v_cvt_pk_fp8_f32 v64, v52, v53
	v_pk_mul_f32 v[52:53], v[58:59], s[68:69] op_sel_hi:[1,0]
	v_mov_b32_e32 v65, v1
	v_pk_mul_f32 v[16:17], v[16:17], s[68:69] op_sel_hi:[1,0]
	v_cvt_pk_fp8_f32 v65, v52, v53
	v_pk_mul_f32 v[52:53], v[54:55], s[68:69] op_sel_hi:[1,0]
	v_mov_b32_e32 v66, v1
	v_cvt_pk_fp8_f32 v14, v16, v17 op_sel:[0,0,1]
	v_pk_mul_f32 v[10:11], v[10:11], s[68:69] op_sel_hi:[1,0]
	v_mov_b32_e32 v15, v1
	v_pk_mul_f32 v[6:7], v[6:7], s[68:69] op_sel_hi:[1,0]
	v_mov_b32_e32 v16, v1
	v_pk_mul_f32 v[2:3], v[2:3], s[68:69] op_sel_hi:[1,0]
	v_mov_b32_e32 v17, v1
	v_cvt_pk_fp8_f32 v66, v52, v53
	v_cvt_pk_fp8_f32 v15, v10, v11
	v_cvt_pk_fp8_f32 v16, v6, v7
	v_cvt_pk_fp8_f32 v17, v2, v3
	v_pk_mul_f32 v[50:51], v[68:69], s[68:69] op_sel_hi:[1,0]
	v_pk_mul_f32 v[12:13], v[12:13], s[68:69] op_sel_hi:[1,0]
	v_cvt_pk_fp8_f32 v64, v50, v51 op_sel:[0,0,1]
	v_pk_mul_f32 v[50:51], v[60:61], s[68:69] op_sel_hi:[1,0]
	v_pk_mul_f32 v[8:9], v[8:9], s[68:69] op_sel_hi:[1,0]
	v_cvt_pk_fp8_f32 v65, v50, v51 op_sel:[0,0,1]
	v_pk_mul_f32 v[50:51], v[56:57], s[68:69] op_sel_hi:[1,0]
	v_pk_mul_f32 v[4:5], v[4:5], s[68:69] op_sel_hi:[1,0]
	v_cvt_pk_fp8_f32 v66, v50, v51 op_sel:[0,0,1]
	v_cvt_pk_fp8_f32 v49, v18, v19 op_sel:[0,0,1]
	v_cvt_pk_fp8_f32 v15, v12, v13 op_sel:[0,0,1]
	v_cvt_pk_fp8_f32 v16, v8, v9 op_sel:[0,0,1]
	v_cvt_pk_fp8_f32 v17, v4, v5 op_sel:[0,0,1]
	v_permlane32_swap_b32_e32 v126, v127
	v_permlane32_swap_b32_e32 v128, v129
	v_permlane32_swap_b32_e32 v110, v111
	v_permlane32_swap_b32_e32 v112, v113
	v_permlane32_swap_b32_e32 v64, v65
	v_permlane32_swap_b32_e32 v66, v67
	v_permlane32_swap_b32_e32 v46, v47
	v_permlane32_swap_b32_e32 v48, v49
	v_lshl_add_u64 v[18:19], v[62:63], 0, s[26:27]
	v_permlane32_swap_b32_e32 v14, v15
	v_permlane32_swap_b32_e32 v16, v17
	s_and_b64 vcc, exec, s[10:11]
	s_mov_b32 s12, s2
	s_mov_b32 s24, s4
	s_mov_b64 s[46:47], s[8:9]
	s_mov_b64 s[26:27], s[6:7]
	global_store_dwordx4 v[134:135], v[126:129], off
	global_store_dwordx4 v[134:135], v[110:113], off offset:128
	global_store_dwordx4 v[62:63], v[64:67], off
	global_store_dwordx4 v[62:63], v[46:49], off offset:128
	global_store_dwordx4 v[18:19], v[14:17], off offset:128
	s_cbranch_vccz .LBB0_241
	v_readlane_b32 s0, v252, 50
	s_waitcnt vmcnt(0)
	v_readlane_b32 s1, v252, 51
	s_andn2_b64 vcc, exec, s[0:1]
	s_cbranch_vccnz .LBB0_253
	s_barrier

.LBB0_278:
	s_add_u32 s6, s4, 0xfffc0080
	s_addc_u32 s7, s5, -1
	s_add_i32 s25, 0, 0x10000
	v_add_u32_e32 v0, s25, v207
	ds_read_b128 v[52:55], v0
	ds_read_b128 v[56:59], v0 offset:1024
	ds_read_b128 v[68:71], v0 offset:2048
	ds_read_b128 v[72:75], v0 offset:3072
	s_cmp_eq_u32 s17, 12
	s_cselect_b32 s11, s3, s7
	s_cselect_b32 s10, s9, s6
	s_cselect_b32 s7, s12, s16
	s_cselect_b32 s6, s13, s15
	v_mov_b32_e32 v0, v205
	ds_read_b128 v[84:87], v208
	ds_read_b128 v[88:91], v208 offset:1024
	ds_read_b128 v[92:95], v208 offset:2048
	ds_read_b128 v[96:99], v208 offset:3072
	ds_read_b128 v[172:175], v208 offset:4096
	ds_read_b128 v[176:179], v208 offset:5120
	ds_read_b128 v[180:183], v208 offset:6144
	ds_read_b128 v[184:187], v208 offset:7168
	s_nop 0
	v_mov_b32_e32 v0, v206
	s_nop 0
	s_waitcnt lgkmcnt(8)
	s_barrier
	s_waitcnt lgkmcnt(0)
	s_setprio 1
	s_waitcnt lgkmcnt(0)
	v_mfma_scale_f32_16x16x128_f8f6f4 v[164:167], v[52:59], v[84:91], v[164:167], v202, v202 op_sel_hi:[0,0,0]
	s_add_i32 m0, s18, 0xc000
	v_mfma_scale_f32_16x16x128_f8f6f4 v[160:163], v[68:75], v[84:91], v[160:163], v202, v202 op_sel_hi:[0,0,0]
	global_load_lds_dwordx4 v205, s[4:5]
	v_mfma_scale_f32_16x16x128_f8f6f4 v[156:159], v[52:59], v[92:99], v[156:159], v202, v202 op_sel_hi:[0,0,0]
	s_add_i32 m0, s18, 0xe000
	v_mfma_scale_f32_16x16x128_f8f6f4 v[152:155], v[68:75], v[92:99], v[152:155], v202, v202 op_sel_hi:[0,0,0]
	global_load_lds_dwordx4 v206, s[4:5]
	v_mfma_scale_f32_16x16x128_f8f6f4 v[148:151], v[52:59], v[172:179], v[148:151], v202, v202 op_sel_hi:[0,0,0]
	v_mfma_scale_f32_16x16x128_f8f6f4 v[188:191], v[68:75], v[172:179], v[144:147], v202, v202 op_sel_hi:[0,0,0]
	v_mfma_scale_f32_16x16x128_f8f6f4 v[192:195], v[52:59], v[180:187], v[136:139], v202, v202 op_sel_hi:[0,0,0]
	v_mfma_scale_f32_16x16x128_f8f6f4 v[196:199], v[68:75], v[180:187], v[132:135], v202, v202 op_sel_hi:[0,0,0]
	s_setprio 0
	s_barrier
	s_add_i32 s30, 0, 0x14000
	v_add_u32_e32 v0, s30, v207
	s_nop 2
	ds_read_b128 v[132:135], v0
	ds_read_b128 v[136:139], v0 offset:1024
	ds_read_b128 v[140:143], v0 offset:2048
	ds_read_b128 v[144:147], v0 offset:3072
	v_mov_b32_e32 v0, v205
	s_add_i32 s25, s25, s73
	s_nop 0
	v_mov_b32_e32 v0, v206
	s_nop 0
	s_barrier
	s_waitcnt lgkmcnt(0)
	s_setprio 1
	s_waitcnt lgkmcnt(0)
	v_mfma_scale_f32_16x16x128_f8f6f4 v[128:131], v[132:139], v[84:91], v[128:131], v202, v202 op_sel_hi:[0,0,0]
	s_mov_b32 m0, s25
	v_mfma_scale_f32_16x16x128_f8f6f4 v[124:127], v[140:147], v[84:91], v[124:127], v202, v202 op_sel_hi:[0,0,0]
	global_load_lds_dwordx4 v205, s[6:7]
	v_mfma_scale_f32_16x16x128_f8f6f4 v[120:123], v[132:139], v[92:99], v[120:123], v202, v202 op_sel_hi:[0,0,0]
	s_add_i32 m0, s25, 0x2000
	v_mfma_scale_f32_16x16x128_f8f6f4 v[116:119], v[140:147], v[92:99], v[116:119], v202, v202 op_sel_hi:[0,0,0]
	global_load_lds_dwordx4 v206, s[6:7]
	v_mfma_scale_f32_16x16x128_f8f6f4 v[210:213], v[132:139], v[172:179], v[112:115], v202, v202 op_sel_hi:[0,0,0]
	v_mfma_scale_f32_16x16x128_f8f6f4 v[172:175], v[140:147], v[172:179], v[108:111], v202, v202 op_sel_hi:[0,0,0]
	v_mfma_scale_f32_16x16x128_f8f6f4 v[176:179], v[132:139], v[180:187], v[104:107], v202, v202 op_sel_hi:[0,0,0]
	v_mfma_scale_f32_16x16x128_f8f6f4 v[180:183], v[140:147], v[180:187], v[100:103], v202, v202 op_sel_hi:[0,0,0]
	s_setprio 0
	v_mov_b32_e32 v0, v205
	s_barrier
	ds_read_b128 v[84:87], v208 offset:16384
	ds_read_b128 v[88:91], v208 offset:17408
	ds_read_b128 v[92:95], v208 offset:18432
	ds_read_b128 v[96:99], v208 offset:19456
	ds_read_b128 v[100:103], v208 offset:20480
	ds_read_b128 v[104:107], v208 offset:21504
	ds_read_b128 v[108:111], v208 offset:22528
	ds_read_b128 v[112:115], v208 offset:23552
	s_nop 0
	v_mov_b32_e32 v0, v206
	s_nop 0
	s_barrier
	s_waitcnt lgkmcnt(0)
	s_setprio 1
	s_waitcnt lgkmcnt(0)
	v_mfma_scale_f32_16x16x128_f8f6f4 v[80:83], v[52:59], v[84:91], v[80:83], v202, v202 op_sel_hi:[0,0,0]
	s_mov_b32 m0, s18
	v_mfma_scale_f32_16x16x128_f8f6f4 v[76:79], v[68:75], v[84:91], v[76:79], v202, v202 op_sel_hi:[0,0,0]
	global_load_lds_dwordx4 v205, s[10:11]
	v_mfma_scale_f32_16x16x128_f8f6f4 v[64:67], v[52:59], v[92:99], v[64:67], v202, v202 op_sel_hi:[0,0,0]
	s_mov_b32 m0, s19
	v_mfma_scale_f32_16x16x128_f8f6f4 v[60:63], v[68:75], v[92:99], v[60:63], v202, v202 op_sel_hi:[0,0,0]
	global_load_lds_dwordx4 v206, s[10:11]
	v_mfma_scale_f32_16x16x128_f8f6f4 v[184:187], v[52:59], v[100:107], v[48:51], v202, v202 op_sel_hi:[0,0,0]
	v_mfma_scale_f32_16x16x128_f8f6f4 v[214:217], v[68:75], v[100:107], v[44:47], v202, v202 op_sel_hi:[0,0,0]
	v_mfma_scale_f32_16x16x128_f8f6f4 v[218:221], v[52:59], v[108:115], v[40:43], v202, v202 op_sel_hi:[0,0,0]
	v_mfma_scale_f32_16x16x128_f8f6f4 v[222:225], v[68:75], v[108:115], v[36:39], v202, v202 op_sel_hi:[0,0,0]
	s_setprio 0
	s_barrier
	s_add_u32 s26, s6, 0x40000
	s_addc_u32 s27, s7, 0
	v_mov_b32_e32 v0, v205
	s_add_i32 s25, s30, s73
	s_mov_b32 s100, s25
	s_nop 0
	v_mov_b32_e32 v0, v206
	s_add_i32 s101, s25, 0x2000
	s_nop 0
	s_waitcnt vmcnt(4)
	s_barrier
	s_setprio 1
	v_mfma_scale_f32_16x16x128_f8f6f4 v[226:229], v[132:139], v[84:91], v[32:35], v202, v202 op_sel_hi:[0,0,0]
	s_mov_b32 m0, s100
	v_mfma_scale_f32_16x16x128_f8f6f4 v[230:233], v[140:147], v[84:91], v[28:31], v202, v202 op_sel_hi:[0,0,0]
	global_load_lds_dwordx4 v205, s[26:27]
	v_mfma_scale_f32_16x16x128_f8f6f4 v[234:237], v[132:139], v[92:99], v[24:27], v202, v202 op_sel_hi:[0,0,0]
	s_mov_b32 m0, s101
	v_mfma_scale_f32_16x16x128_f8f6f4 v[238:241], v[140:147], v[92:99], v[20:23], v202, v202 op_sel_hi:[0,0,0]
	global_load_lds_dwordx4 v206, s[26:27]
	v_mfma_scale_f32_16x16x128_f8f6f4 v[242:245], v[132:139], v[100:107], v[16:19], v202, v202 op_sel_hi:[0,0,0]
	v_mfma_scale_f32_16x16x128_f8f6f4 v[246:249], v[140:147], v[100:107], v[12:15], v202, v202 op_sel_hi:[0,0,0]
	v_mfma_scale_f32_16x16x128_f8f6f4 v[168:171], v[132:139], v[108:115], v[8:11], v202, v202 op_sel_hi:[0,0,0]
	v_mfma_scale_f32_16x16x128_f8f6f4 v[140:143], v[140:147], v[108:115], v[4:7], v202, v202 op_sel_hi:[0,0,0]
	s_setprio 0
	s_add_i32 s25, 0, 0x18000
	v_add_u32_e32 v0, s25, v207
	s_barrier
	s_nop 2
	ds_read_b128 v[2:5], v0
	ds_read_b128 v[6:9], v0 offset:1024
	ds_read_b128 v[10:13], v0 offset:2048
	ds_read_b128 v[14:17], v0 offset:3072
	s_add_u32 s26, s10, 0x40000
	v_mov_b32_e32 v0, v205
	ds_read_b128 v[18:21], v208 offset:32768
	ds_read_b128 v[22:25], v208 offset:33792
	ds_read_b128 v[26:29], v208 offset:34816
	ds_read_b128 v[30:33], v208 offset:35840
	ds_read_b128 v[34:37], v208 offset:36864
	ds_read_b128 v[38:41], v208 offset:37888
	ds_read_b128 v[42:45], v208 offset:38912
	ds_read_b128 v[46:49], v208 offset:39936
	s_addc_u32 s27, s11, 0
	s_nop 0
	v_mov_b32_e32 v0, v206
	s_nop 0
	s_waitcnt lgkmcnt(8)
	s_barrier
	s_waitcnt lgkmcnt(0)
	s_setprio 1
	s_waitcnt lgkmcnt(0)
	v_mfma_scale_f32_16x16x128_f8f6f4 v[164:167], v[2:9], v[18:25], v[164:167], v202, v202 op_sel_hi:[0,0,0]
	s_mov_b32 m0, s20
	v_mfma_scale_f32_16x16x128_f8f6f4 v[160:163], v[10:17], v[18:25], v[160:163], v202, v202 op_sel_hi:[0,0,0]
	global_load_lds_dwordx4 v205, s[26:27]
	v_mfma_scale_f32_16x16x128_f8f6f4 v[156:159], v[2:9], v[26:33], v[156:159], v202, v202 op_sel_hi:[0,0,0]
	s_mov_b32 m0, s21
	v_mfma_scale_f32_16x16x128_f8f6f4 v[152:155], v[10:17], v[26:33], v[152:155], v202, v202 op_sel_hi:[0,0,0]
	global_load_lds_dwordx4 v206, s[26:27]
	v_mfma_scale_f32_16x16x128_f8f6f4 v[148:151], v[2:9], v[34:41], v[148:151], v202, v202 op_sel_hi:[0,0,0]
	v_mfma_scale_f32_16x16x128_f8f6f4 v[144:147], v[10:17], v[34:41], v[188:191], v202, v202 op_sel_hi:[0,0,0]
	v_mfma_scale_f32_16x16x128_f8f6f4 v[136:139], v[2:9], v[42:49], v[192:195], v202, v202 op_sel_hi:[0,0,0]
	v_mfma_scale_f32_16x16x128_f8f6f4 v[132:135], v[10:17], v[42:49], v[196:199], v202, v202 op_sel_hi:[0,0,0]
	s_setprio 0
	s_barrier
	s_add_i32 s26, 0, 0x1c000
	v_add_u32_e32 v0, s26, v207
	ds_read_b128 v[52:55], v0
	ds_read_b128 v[56:59], v0 offset:1024
	ds_read_b128 v[68:71], v0 offset:2048
	ds_read_b128 v[72:75], v0 offset:3072
	v_mov_b32_e32 v0, v205
	s_add_i32 s25, s25, s73
	v_lshl_add_u64 v[50:51], s[6:7], 0, v[0:1]
	v_lshl_add_u64 v[50:51], v[50:51], 0, s[66:67]
	v_mov_b32_e32 v0, v206
	v_lshl_add_u64 v[50:51], s[6:7], 0, v[0:1]
	v_lshl_add_u64 v[50:51], v[50:51], 0, s[66:67]
	s_barrier
	s_waitcnt lgkmcnt(0)
	s_setprio 1
	s_waitcnt lgkmcnt(0)
	v_mfma_scale_f32_16x16x128_f8f6f4 v[128:131], v[52:59], v[18:25], v[128:131], v202, v202 op_sel_hi:[0,0,0]
	s_add_u32 s98, s6, s66
	s_addc_u32 s99, s7, s67
	s_mov_b32 m0, s25
	v_mfma_scale_f32_16x16x128_f8f6f4 v[124:127], v[68:75], v[18:25], v[124:127], v202, v202 op_sel_hi:[0,0,0]
	global_load_lds_dwordx4 v205, s[98:99]
	v_mfma_scale_f32_16x16x128_f8f6f4 v[120:123], v[52:59], v[26:33], v[120:123], v202, v202 op_sel_hi:[0,0,0]
	s_add_i32 m0, s25, 0x2000
	v_mfma_scale_f32_16x16x128_f8f6f4 v[116:119], v[68:75], v[26:33], v[116:119], v202, v202 op_sel_hi:[0,0,0]
	global_load_lds_dwordx4 v206, s[98:99]
	v_mfma_scale_f32_16x16x128_f8f6f4 v[112:115], v[52:59], v[34:41], v[210:213], v202, v202 op_sel_hi:[0,0,0]
	v_mfma_scale_f32_16x16x128_f8f6f4 v[108:111], v[68:75], v[34:41], v[172:175], v202, v202 op_sel_hi:[0,0,0]
	v_mfma_scale_f32_16x16x128_f8f6f4 v[104:107], v[52:59], v[42:49], v[176:179], v202, v202 op_sel_hi:[0,0,0]
	v_mfma_scale_f32_16x16x128_f8f6f4 v[100:103], v[68:75], v[42:49], v[180:183], v202, v202 op_sel_hi:[0,0,0]
	s_setprio 0
	v_mov_b32_e32 v0, v205
	s_barrier
	ds_read_b128 v[18:21], v208 offset:49152
	ds_read_b128 v[22:25], v208 offset:50176
	ds_read_b128 v[84:87], v208 offset:51200
	ds_read_b128 v[88:91], v208 offset:52224
	ds_read_b128 v[92:95], v208 offset:53248
	ds_read_b128 v[96:99], v208 offset:54272
	ds_read_b128 v[172:175], v208 offset:55296
	ds_read_b128 v[176:179], v208 offset:56320
	v_lshl_add_u64 v[26:27], s[10:11], 0, v[0:1]
	v_lshl_add_u64 v[26:27], v[26:27], 0, s[66:67]
	v_mov_b32_e32 v0, v206
	v_lshl_add_u64 v[26:27], s[10:11], 0, v[0:1]
	v_lshl_add_u64 v[26:27], v[26:27], 0, s[66:67]
	s_barrier
	s_waitcnt lgkmcnt(0)
	s_setprio 1
	s_waitcnt lgkmcnt(0)
	v_mfma_scale_f32_16x16x128_f8f6f4 v[80:83], v[2:9], v[18:25], v[80:83], v202, v202 op_sel_hi:[0,0,0]
	s_add_u32 s98, s10, s66
	s_addc_u32 s99, s11, s67
	s_mov_b32 m0, s22
	v_mfma_scale_f32_16x16x128_f8f6f4 v[76:79], v[10:17], v[18:25], v[76:79], v202, v202 op_sel_hi:[0,0,0]
	global_load_lds_dwordx4 v205, s[98:99]
	v_mfma_scale_f32_16x16x128_f8f6f4 v[64:67], v[2:9], v[84:91], v[64:67], v202, v202 op_sel_hi:[0,0,0]
	s_mov_b32 m0, s34
	v_mfma_scale_f32_16x16x128_f8f6f4 v[60:63], v[10:17], v[84:91], v[60:63], v202, v202 op_sel_hi:[0,0,0]
	global_load_lds_dwordx4 v206, s[98:99]
	v_mfma_scale_f32_16x16x128_f8f6f4 v[48:51], v[2:9], v[92:99], v[184:187], v202, v202 op_sel_hi:[0,0,0]
	v_mfma_scale_f32_16x16x128_f8f6f4 v[44:47], v[10:17], v[92:99], v[214:217], v202, v202 op_sel_hi:[0,0,0]
	v_mfma_scale_f32_16x16x128_f8f6f4 v[40:43], v[2:9], v[172:179], v[218:221], v202, v202 op_sel_hi:[0,0,0]
	v_mfma_scale_f32_16x16x128_f8f6f4 v[36:39], v[10:17], v[172:179], v[222:225], v202, v202 op_sel_hi:[0,0,0]
	s_setprio 0
	s_barrier
	s_add_u32 s6, s6, 0x40080
	s_addc_u32 s7, s7, 0
	v_mov_b32_e32 v0, v205
	s_add_i32 s10, s26, s73
	s_nop 0
	v_mov_b32_e32 v0, v206
	s_nop 0
	s_waitcnt vmcnt(4)
	s_barrier
	s_setprio 1
	v_mfma_scale_f32_16x16x128_f8f6f4 v[32:35], v[52:59], v[18:25], v[226:229], v202, v202 op_sel_hi:[0,0,0]
	s_mov_b32 m0, s10
	v_mfma_scale_f32_16x16x128_f8f6f4 v[28:31], v[68:75], v[18:25], v[230:233], v202, v202 op_sel_hi:[0,0,0]
	global_load_lds_dwordx4 v205, s[6:7]
	v_mfma_scale_f32_16x16x128_f8f6f4 v[24:27], v[52:59], v[84:91], v[234:237], v202, v202 op_sel_hi:[0,0,0]
	s_add_i32 m0, s10, 0x2000
	v_mfma_scale_f32_16x16x128_f8f6f4 v[20:23], v[68:75], v[84:91], v[238:241], v202, v202 op_sel_hi:[0,0,0]
	global_load_lds_dwordx4 v206, s[6:7]
	v_mfma_scale_f32_16x16x128_f8f6f4 v[16:19], v[52:59], v[92:99], v[242:245], v202, v202 op_sel_hi:[0,0,0]
	v_mfma_scale_f32_16x16x128_f8f6f4 v[12:15], v[68:75], v[92:99], v[246:249], v202, v202 op_sel_hi:[0,0,0]
	v_mfma_scale_f32_16x16x128_f8f6f4 v[8:11], v[52:59], v[172:179], v[168:171], v202, v202 op_sel_hi:[0,0,0]
	v_mfma_scale_f32_16x16x128_f8f6f4 v[4:7], v[68:75], v[172:179], v[140:143], v202, v202 op_sel_hi:[0,0,0]
	s_setprio 0
	s_add_i32 s17, s17, 2
	s_add_u32 s4, s4, 0x100
	s_addc_u32 s5, s5, 0
	s_add_u32 s15, s15, 0x100
	s_addc_u32 s16, s16, 0
	s_cmp_gt_u32 s17, 13
	s_barrier
	s_cbranch_scc0 .LBB0_278
	s_ashr_i32 s3, s8, 2
	s_mul_hi_i32 s4, s3, 0x55555556
	s_lshr_b32 s5, s4, 31
	s_add_i32 s4, s4, s5
	s_mul_i32 s4, s4, 3
	s_sub_i32 s15, s3, s4
	s_add_i32 s3, s8, 11
	s_cmp_lt_u32 s3, 23
	s_cselect_b64 s[12:13], -1, 0
	s_cmp_lt_i32 s15, 2
	v_readlane_b32 s6, v252, 53
	s_cselect_b64 s[4:5], -1, 0
	v_readlane_b32 s7, v252, 54
	s_and_b64 s[4:5], s[6:7], s[4:5]
	v_mbcnt_lo_u32_b32 v211, -1, 0
	v_mbcnt_hi_u32_b32 v211, -1, v211
	s_and_b64 s[6:7], s[12:13], s[4:5]
	v_ashrrev_i32_e32 v210, 4, v211
	s_lshl_b32 s3, s74, 8
	v_lshlrev_b32_e32 v172, 2, v210
	v_mov_b32_e32 v140, 0
	v_cndmask_b32_e64 v0, 0, 1, s[6:7]
	v_and_b32_e32 v209, 15, v211
	s_add_i32 s46, s3, s28
	v_ashrrev_i32_e32 v173, 31, v172
	v_cmp_ne_u32_e64 s[10:11], 1, v0
	s_andn2_b64 vcc, exec, s[6:7]
	v_mov_b32_e32 v141, v140
	v_mov_b32_e32 v142, v140
	v_mov_b32_e32 v143, v140
	v_mov_b32_e32 v92, v140
	v_mov_b32_e32 v93, v140
	v_mov_b32_e32 v94, v140
	v_mov_b32_e32 v95, v140
	v_mov_b32_e32 v88, v140
	v_mov_b32_e32 v89, v140
	v_mov_b32_e32 v90, v140
	v_mov_b32_e32 v91, v140
	v_mov_b32_e32 v72, v140
	v_mov_b32_e32 v73, v140
	v_mov_b32_e32 v74, v140
	v_mov_b32_e32 v75, v140
	v_mov_b32_e32 v56, v140
	v_mov_b32_e32 v57, v140
	v_mov_b32_e32 v58, v140
	v_mov_b32_e32 v59, v140
	s_cbranch_vccnz .LBB0_281
	s_and_b32 s3, s46, 0xfc0
	v_readlane_b32 s4, v252, 31
	v_or_b32_e32 v0, s3, v209
	v_readlane_b32 s5, v252, 32
	v_lshlrev_b32_e32 v0, 7, v0
	s_movk_i32 s3, 0x1000
	v_lshl_add_u64 v[2:3], v[172:173], 2, s[4:5]
	v_lshl_add_u64 v[2:3], v[2:3], 0, v[0:1]
	global_load_dwordx4 v[92:95], v[2:3], off
	global_load_dwordx4 v[96:99], v[2:3], off offset:64
	v_add_co_u32_e32 v52, vcc, s3, v2
	s_nop 1
	v_addc_co_u32_e32 v53, vcc, 0, v3, vcc
	global_load_dwordx4 v[140:143], v[52:53], off offset:2048
	global_load_dwordx4 v[88:91], v[2:3], off offset:2048
	global_load_dwordx4 v[84:87], v[2:3], off offset:2112
	global_load_dwordx4 v[72:75], v[52:53], off
	global_load_dwordx4 v[68:71], v[52:53], off offset:64
	s_nop 0
	global_load_dwordx4 v[52:55], v[52:53], off offset:2112
	s_waitcnt vmcnt(0)
	v_mov_b32_e32 v56, v140
	v_mov_b32_e32 v57, v141
	v_mov_b32_e32 v58, v142
	v_mov_b32_e32 v59, v143

.LBB0_1503:
	s_add_u32 s24, s2, 0xfffc0080
	s_addc_u32 s25, s3, -1
	s_add_i32 s28, 0, 0x10000
	v_add_u32_e32 v128, s28, v150
	ds_read_b128 v[136:139], v128
	ds_read_b128 v[140:143], v128 offset:1024
	ds_read_b128 v[152:155], v128 offset:2048
	ds_read_b128 v[156:159], v128 offset:3072
	s_cmp_eq_u32 s22, 12
	s_cselect_b32 s41, s49, s25
	s_cselect_b32 s40, s48, s24
	s_cselect_b32 s39, s59, s20
	s_cselect_b32 s38, s58, s7
	v_mov_b32_e32 v128, v148
	ds_read_b128 v[160:163], v151
	ds_read_b128 v[164:167], v151 offset:1024
	ds_read_b128 v[168:171], v151 offset:2048
	ds_read_b128 v[172:175], v151 offset:3072
	ds_read_b128 v[176:179], v151 offset:4096
	ds_read_b128 v[180:183], v151 offset:5120
	ds_read_b128 v[184:187], v151 offset:6144
	ds_read_b128 v[188:191], v151 offset:7168
	s_nop 0
	v_mov_b32_e32 v128, v149
	s_nop 0
	s_waitcnt lgkmcnt(8)
	s_barrier
	s_waitcnt lgkmcnt(0)
	s_setprio 1
	s_waitcnt lgkmcnt(0)
	v_mfma_scale_f32_16x16x128_f8f6f4 v[124:127], v[136:143], v[160:167], v[124:127], v146, v146 op_sel_hi:[0,0,0]
	s_add_i32 m0, s0, 0xc000
	v_mfma_scale_f32_16x16x128_f8f6f4 v[120:123], v[152:159], v[160:167], v[120:123], v146, v146 op_sel_hi:[0,0,0]
	global_load_lds_dwordx4 v148, s[2:3]
	v_mfma_scale_f32_16x16x128_f8f6f4 v[116:119], v[136:143], v[168:175], v[116:119], v146, v146 op_sel_hi:[0,0,0]
	s_add_i32 m0, s0, 0xe000
	v_mfma_scale_f32_16x16x128_f8f6f4 v[112:115], v[152:159], v[168:175], v[112:115], v146, v146 op_sel_hi:[0,0,0]
	global_load_lds_dwordx4 v149, s[2:3]
	v_mfma_scale_f32_16x16x128_f8f6f4 v[128:131], v[136:143], v[176:183], v[108:111], v146, v146 op_sel_hi:[0,0,0]
	v_mfma_scale_f32_16x16x128_f8f6f4 v[192:195], v[152:159], v[176:183], v[104:107], v146, v146 op_sel_hi:[0,0,0]
	v_mfma_scale_f32_16x16x128_f8f6f4 v[196:199], v[136:143], v[184:191], v[100:103], v146, v146 op_sel_hi:[0,0,0]
	v_mfma_scale_f32_16x16x128_f8f6f4 v[200:203], v[152:159], v[184:191], v[96:99], v146, v146 op_sel_hi:[0,0,0]
	s_setprio 0
	s_barrier
	s_add_i32 s29, 0, 0x14000
	s_nop 0
	v_add_u32_e32 v108, s29, v150
	v_mov_b32_e32 v132, v148
	s_add_i32 s24, s28, s21
	ds_read_b128 v[96:99], v108
	ds_read_b128 v[100:103], v108 offset:1024
	ds_read_b128 v[104:107], v108 offset:2048
	ds_read_b128 v[108:111], v108 offset:3072
	s_nop 0
	v_mov_b32_e32 v132, v149
	s_nop 0
	s_barrier
	s_waitcnt lgkmcnt(0)
	s_setprio 1
	s_waitcnt lgkmcnt(0)
	v_mfma_scale_f32_16x16x128_f8f6f4 v[204:207], v[96:103], v[160:167], v[60:63], v146, v146 op_sel_hi:[0,0,0]
	s_mov_b32 m0, s24
	v_mfma_scale_f32_16x16x128_f8f6f4 v[160:163], v[104:111], v[160:167], v[56:59], v146, v146 op_sel_hi:[0,0,0]
	global_load_lds_dwordx4 v148, s[38:39]
	v_mfma_scale_f32_16x16x128_f8f6f4 v[164:167], v[96:103], v[168:175], v[52:55], v146, v146 op_sel_hi:[0,0,0]
	s_add_i32 m0, s24, 0x2000
	v_mfma_scale_f32_16x16x128_f8f6f4 v[168:171], v[104:111], v[168:175], v[48:51], v146, v146 op_sel_hi:[0,0,0]
	global_load_lds_dwordx4 v149, s[38:39]
	v_mfma_scale_f32_16x16x128_f8f6f4 v[172:175], v[96:103], v[176:183], v[44:47], v146, v146 op_sel_hi:[0,0,0]
	v_mfma_scale_f32_16x16x128_f8f6f4 v[176:179], v[104:111], v[176:183], v[40:43], v146, v146 op_sel_hi:[0,0,0]
	v_mfma_scale_f32_16x16x128_f8f6f4 v[180:183], v[96:103], v[184:191], v[36:39], v146, v146 op_sel_hi:[0,0,0]
	v_mfma_scale_f32_16x16x128_f8f6f4 v[184:187], v[104:111], v[184:191], v[32:35], v146, v146 op_sel_hi:[0,0,0]
	s_setprio 0
	v_mov_b32_e32 v132, v148
	s_barrier
	s_nop 2
	ds_read_b128 v[32:35], v151 offset:16384
	ds_read_b128 v[36:39], v151 offset:17408
	ds_read_b128 v[40:43], v151 offset:18432
	ds_read_b128 v[44:47], v151 offset:19456
	ds_read_b128 v[48:51], v151 offset:20480
	ds_read_b128 v[52:55], v151 offset:21504
	ds_read_b128 v[56:59], v151 offset:22528
	ds_read_b128 v[60:63], v151 offset:23552
	s_nop 0
	v_mov_b32_e32 v132, v149
	s_nop 0
	s_barrier
	s_waitcnt lgkmcnt(0)
	s_setprio 1
	s_waitcnt lgkmcnt(0)
	v_mfma_scale_f32_16x16x128_f8f6f4 v[92:95], v[136:143], v[32:39], v[92:95], v146, v146 op_sel_hi:[0,0,0]
	s_mov_b32 m0, s0
	v_mfma_scale_f32_16x16x128_f8f6f4 v[88:91], v[152:159], v[32:39], v[88:91], v146, v146 op_sel_hi:[0,0,0]
	global_load_lds_dwordx4 v148, s[40:41]
	v_mfma_scale_f32_16x16x128_f8f6f4 v[84:87], v[136:143], v[40:47], v[84:87], v146, v146 op_sel_hi:[0,0,0]
	s_mov_b32 m0, s1
	v_mfma_scale_f32_16x16x128_f8f6f4 v[80:83], v[152:159], v[40:47], v[80:83], v146, v146 op_sel_hi:[0,0,0]
	global_load_lds_dwordx4 v149, s[40:41]
	v_mfma_scale_f32_16x16x128_f8f6f4 v[76:79], v[136:143], v[48:55], v[76:79], v146, v146 op_sel_hi:[0,0,0]
	v_mfma_scale_f32_16x16x128_f8f6f4 v[72:75], v[152:159], v[48:55], v[72:75], v146, v146 op_sel_hi:[0,0,0]
	v_mfma_scale_f32_16x16x128_f8f6f4 v[188:191], v[136:143], v[56:63], v[68:71], v146, v146 op_sel_hi:[0,0,0]
	v_mfma_scale_f32_16x16x128_f8f6f4 v[208:211], v[152:159], v[56:63], v[64:67], v146, v146 op_sel_hi:[0,0,0]
	s_setprio 0
	s_barrier
	s_add_u32 s24, s38, 0x40000
	s_addc_u32 s25, s39, 0
	s_nop 2
	v_mov_b32_e32 v64, v148
	s_add_i32 s28, s29, s21
	s_mov_b32 s100, s28
	s_nop 0
	v_mov_b32_e32 v64, v149
	s_add_i32 s101, s28, 0x2000
	s_nop 0
	s_waitcnt vmcnt(4)
	s_barrier
	s_setprio 1
	v_mfma_scale_f32_16x16x128_f8f6f4 v[212:215], v[96:103], v[32:39], v[28:31], v146, v146 op_sel_hi:[0,0,0]
	s_mov_b32 m0, s100
	v_mfma_scale_f32_16x16x128_f8f6f4 v[216:219], v[104:111], v[32:39], v[24:27], v146, v146 op_sel_hi:[0,0,0]
	global_load_lds_dwordx4 v148, s[24:25]
	v_mfma_scale_f32_16x16x128_f8f6f4 v[220:223], v[96:103], v[40:47], v[20:23], v146, v146 op_sel_hi:[0,0,0]
	s_mov_b32 m0, s101
	v_mfma_scale_f32_16x16x128_f8f6f4 v[224:227], v[104:111], v[40:47], v[16:19], v146, v146 op_sel_hi:[0,0,0]
	global_load_lds_dwordx4 v149, s[24:25]
	v_mfma_scale_f32_16x16x128_f8f6f4 v[228:231], v[96:103], v[48:55], v[12:15], v146, v146 op_sel_hi:[0,0,0]
	v_mfma_scale_f32_16x16x128_f8f6f4 v[232:235], v[104:111], v[48:55], v[8:11], v146, v146 op_sel_hi:[0,0,0]
	v_mfma_scale_f32_16x16x128_f8f6f4 v[236:239], v[96:103], v[56:63], v[4:7], v146, v146 op_sel_hi:[0,0,0]
	v_mfma_scale_f32_16x16x128_f8f6f4 v[240:243], v[104:111], v[56:63], v[0:3], v146, v146 op_sel_hi:[0,0,0]
	s_setprio 0
	s_add_i32 s28, 0, 0x18000
	s_nop 1
	v_add_u32_e32 v12, s28, v150
	s_barrier
	s_nop 0
	ds_read_b128 v[0:3], v12
	ds_read_b128 v[4:7], v12 offset:1024
	ds_read_b128 v[8:11], v12 offset:2048
	ds_read_b128 v[12:15], v12 offset:3072
	s_add_u32 s24, s40, 0x40000
	v_mov_b32_e32 v40, v148
	ds_read_b128 v[16:19], v151 offset:32768
	ds_read_b128 v[20:23], v151 offset:33792
	ds_read_b128 v[24:27], v151 offset:34816
	ds_read_b128 v[28:31], v151 offset:35840
	ds_read_b128 v[32:35], v151 offset:36864
	ds_read_b128 v[36:39], v151 offset:37888
	ds_read_b128 v[64:67], v151 offset:38912
	ds_read_b128 v[68:71], v151 offset:39936
	s_addc_u32 s25, s41, 0
	s_nop 0
	v_mov_b32_e32 v40, v149
	s_nop 0
	s_waitcnt lgkmcnt(8)
	s_barrier
	s_waitcnt lgkmcnt(0)
	s_setprio 1
	s_waitcnt lgkmcnt(0)
	v_mfma_scale_f32_16x16x128_f8f6f4 v[124:127], v[0:7], v[16:23], v[124:127], v146, v146 op_sel_hi:[0,0,0]
	s_mov_b32 m0, s8
	v_mfma_scale_f32_16x16x128_f8f6f4 v[120:123], v[8:15], v[16:23], v[120:123], v146, v146 op_sel_hi:[0,0,0]
	global_load_lds_dwordx4 v148, s[24:25]
	v_mfma_scale_f32_16x16x128_f8f6f4 v[116:119], v[0:7], v[24:31], v[116:119], v146, v146 op_sel_hi:[0,0,0]
	s_mov_b32 m0, s9
	v_mfma_scale_f32_16x16x128_f8f6f4 v[112:115], v[8:15], v[24:31], v[112:115], v146, v146 op_sel_hi:[0,0,0]
	global_load_lds_dwordx4 v149, s[24:25]
	v_mfma_scale_f32_16x16x128_f8f6f4 v[108:111], v[0:7], v[32:39], v[128:131], v146, v146 op_sel_hi:[0,0,0]
	v_mfma_scale_f32_16x16x128_f8f6f4 v[104:107], v[8:15], v[32:39], v[192:195], v146, v146 op_sel_hi:[0,0,0]
	v_mfma_scale_f32_16x16x128_f8f6f4 v[100:103], v[0:7], v[64:71], v[196:199], v146, v146 op_sel_hi:[0,0,0]
	v_mfma_scale_f32_16x16x128_f8f6f4 v[96:99], v[8:15], v[64:71], v[200:203], v146, v146 op_sel_hi:[0,0,0]
	s_setprio 0
	s_barrier
	s_add_i32 s29, 0, 0x1c000
	v_add_u32_e32 v40, s29, v150
	v_mov_b32_e32 v132, v148
	ds_read_b128 v[136:139], v40
	ds_read_b128 v[140:143], v40 offset:1024
	ds_read_b128 v[152:155], v40 offset:2048
	ds_read_b128 v[156:159], v40 offset:3072
	s_add_i32 s24, s28, s21
	v_lshl_add_u64 v[40:41], s[38:39], 0, v[132:133]
	v_lshl_add_u64 v[40:41], v[40:41], 0, s[52:53]
	v_mov_b32_e32 v132, v149
	v_lshl_add_u64 v[40:41], s[38:39], 0, v[132:133]
	v_lshl_add_u64 v[40:41], v[40:41], 0, s[52:53]
	s_barrier
	s_waitcnt lgkmcnt(0)
	s_setprio 1
	s_waitcnt lgkmcnt(0)
	v_mfma_scale_f32_16x16x128_f8f6f4 v[60:63], v[136:143], v[16:23], v[204:207], v146, v146 op_sel_hi:[0,0,0]
	s_add_u32 s98, s38, s52
	s_addc_u32 s99, s39, s53
	s_mov_b32 m0, s24
	v_mfma_scale_f32_16x16x128_f8f6f4 v[56:59], v[152:159], v[16:23], v[160:163], v146, v146 op_sel_hi:[0,0,0]
	global_load_lds_dwordx4 v148, s[98:99]
	v_mfma_scale_f32_16x16x128_f8f6f4 v[52:55], v[136:143], v[24:31], v[164:167], v146, v146 op_sel_hi:[0,0,0]
	s_add_i32 m0, s24, 0x2000
	v_mfma_scale_f32_16x16x128_f8f6f4 v[48:51], v[152:159], v[24:31], v[168:171], v146, v146 op_sel_hi:[0,0,0]
	global_load_lds_dwordx4 v149, s[98:99]
	v_mfma_scale_f32_16x16x128_f8f6f4 v[44:47], v[136:143], v[32:39], v[172:175], v146, v146 op_sel_hi:[0,0,0]
	v_mfma_scale_f32_16x16x128_f8f6f4 v[40:43], v[152:159], v[32:39], v[176:179], v146, v146 op_sel_hi:[0,0,0]
	v_mfma_scale_f32_16x16x128_f8f6f4 v[36:39], v[136:143], v[64:71], v[180:183], v146, v146 op_sel_hi:[0,0,0]
	v_mfma_scale_f32_16x16x128_f8f6f4 v[32:35], v[152:159], v[64:71], v[184:187], v146, v146 op_sel_hi:[0,0,0]
	s_setprio 0
	v_mov_b32_e32 v132, v148
	s_barrier
	ds_read_b128 v[16:19], v151 offset:49152
	ds_read_b128 v[20:23], v151 offset:50176
	ds_read_b128 v[160:163], v151 offset:51200
	ds_read_b128 v[164:167], v151 offset:52224
	ds_read_b128 v[168:171], v151 offset:53248
	ds_read_b128 v[172:175], v151 offset:54272
	ds_read_b128 v[176:179], v151 offset:55296
	ds_read_b128 v[180:183], v151 offset:56320
	v_lshl_add_u64 v[24:25], s[40:41], 0, v[132:133]
	v_lshl_add_u64 v[24:25], v[24:25], 0, s[52:53]
	v_mov_b32_e32 v132, v149
	v_lshl_add_u64 v[24:25], s[40:41], 0, v[132:133]
	v_lshl_add_u64 v[24:25], v[24:25], 0, s[52:53]
	s_barrier
	s_waitcnt lgkmcnt(0)
	s_setprio 1
	s_waitcnt lgkmcnt(0)
	v_mfma_scale_f32_16x16x128_f8f6f4 v[92:95], v[0:7], v[16:23], v[92:95], v146, v146 op_sel_hi:[0,0,0]
	s_add_u32 s98, s40, s52
	s_addc_u32 s99, s41, s53
	s_mov_b32 m0, s10
	v_mfma_scale_f32_16x16x128_f8f6f4 v[88:91], v[8:15], v[16:23], v[88:91], v146, v146 op_sel_hi:[0,0,0]
	global_load_lds_dwordx4 v148, s[98:99]
	v_mfma_scale_f32_16x16x128_f8f6f4 v[84:87], v[0:7], v[160:167], v[84:87], v146, v146 op_sel_hi:[0,0,0]
	s_mov_b32 m0, s11
	v_mfma_scale_f32_16x16x128_f8f6f4 v[80:83], v[8:15], v[160:167], v[80:83], v146, v146 op_sel_hi:[0,0,0]
	global_load_lds_dwordx4 v149, s[98:99]
	v_mfma_scale_f32_16x16x128_f8f6f4 v[76:79], v[0:7], v[168:175], v[76:79], v146, v146 op_sel_hi:[0,0,0]
	v_mfma_scale_f32_16x16x128_f8f6f4 v[72:75], v[8:15], v[168:175], v[72:75], v146, v146 op_sel_hi:[0,0,0]
	v_mfma_scale_f32_16x16x128_f8f6f4 v[68:71], v[0:7], v[176:183], v[188:191], v146, v146 op_sel_hi:[0,0,0]
	v_mfma_scale_f32_16x16x128_f8f6f4 v[64:67], v[8:15], v[176:183], v[208:211], v146, v146 op_sel_hi:[0,0,0]
	s_setprio 0
	s_barrier
	s_add_u32 s24, s38, 0x40080
	s_addc_u32 s25, s39, 0
	v_mov_b32_e32 v0, v148
	s_add_i32 s28, s29, s21
	s_nop 0
	v_mov_b32_e32 v0, v149
	s_nop 0
	s_waitcnt vmcnt(4)
	s_barrier
	s_setprio 1
	v_mfma_scale_f32_16x16x128_f8f6f4 v[28:31], v[136:143], v[16:23], v[212:215], v146, v146 op_sel_hi:[0,0,0]
	s_mov_b32 m0, s28
	v_mfma_scale_f32_16x16x128_f8f6f4 v[24:27], v[152:159], v[16:23], v[216:219], v146, v146 op_sel_hi:[0,0,0]
	global_load_lds_dwordx4 v148, s[24:25]
	v_mfma_scale_f32_16x16x128_f8f6f4 v[20:23], v[136:143], v[160:167], v[220:223], v146, v146 op_sel_hi:[0,0,0]
	s_add_i32 m0, s28, 0x2000
	v_mfma_scale_f32_16x16x128_f8f6f4 v[16:19], v[152:159], v[160:167], v[224:227], v146, v146 op_sel_hi:[0,0,0]
	global_load_lds_dwordx4 v149, s[24:25]
	v_mfma_scale_f32_16x16x128_f8f6f4 v[12:15], v[136:143], v[168:175], v[228:231], v146, v146 op_sel_hi:[0,0,0]
	v_mfma_scale_f32_16x16x128_f8f6f4 v[8:11], v[152:159], v[168:175], v[232:235], v146, v146 op_sel_hi:[0,0,0]
	v_mfma_scale_f32_16x16x128_f8f6f4 v[4:7], v[136:143], v[176:183], v[236:239], v146, v146 op_sel_hi:[0,0,0]
	v_mfma_scale_f32_16x16x128_f8f6f4 v[0:3], v[152:159], v[176:183], v[240:243], v146, v146 op_sel_hi:[0,0,0]
	s_setprio 0
	s_add_i32 s22, s22, 2
	s_add_u32 s2, s2, 0x100
	s_addc_u32 s3, s3, 0
	s_add_u32 s7, s7, 0x100
	s_addc_u32 s20, s20, 0
	s_cmp_gt_u32 s22, 13
	s_barrier
	s_cbranch_scc0 .LBB0_1503
	s_ashr_i32 s2, s13, 4
	s_mul_hi_i32 s3, s2, 0xc000
	s_mul_i32 s2, s2, 0xc000
	s_add_u32 s7, s69, s2
	s_addc_u32 s20, s71, s3
	s_lshl_b32 s2, s15, 8
	s_ashr_i32 s3, s2, 31
	s_lshl_b64 s[24:25], s[2:3], 2
	s_add_u32 s7, s7, s24
	v_mbcnt_lo_u32_b32 v132, -1, 0
	v_mbcnt_hi_u32_b32 v132, -1, v132
	s_addc_u32 s15, s20, s25
	v_ashrrev_i32_e32 v136, 4, v132
	s_lshl_b32 s20, s23, 2
	s_add_u32 s24, s7, s20
	v_lshlrev_b32_e32 v128, 2, v136
	s_addc_u32 s25, s15, 0
	v_ashrrev_i32_e32 v129, 31, v128
	v_lshl_add_u64 v[130:131], v[128:129], 2, s[24:25]
	v_lshlrev_b32_e32 v128, 3, v136
	global_load_dwordx4 v[136:139], v[130:131], off
	global_load_dwordx4 v[152:155], v[130:131], off offset:64
	s_lshl_b32 s7, s13, 8
	s_add_i32 s24, s7, s16
	s_ashr_i32 s25, s24, 31
	s_lshl_b64 s[24:25], s[24:25], 11
	s_add_u32 s7, s61, s24
	s_addc_u32 s13, s65, s25
	s_add_u32 s2, s7, s2
	s_addc_u32 s3, s13, s3
	v_bfi_b32 v128, -16, v128, v132
	s_add_u32 s2, s2, s23
	v_ashrrev_i32_e32 v129, 31, v128
	s_addc_u32 s3, s3, 0
	v_lshlrev_b64 v[128:129], 11, v[128:129]
	v_lshl_add_u64 v[128:129], s[2:3], 0, v[128:129]
	v_and_b32_e32 v132, 16, v132
	v_lshl_add_u64 v[128:129], v[128:129], 0, v[132:133]
	s_mov_b32 s2, 0x10000
	s_mov_b32 s13, s36
	s_mov_b32 s15, s6
	s_mov_b64 s[34:35], s[58:59]
	s_waitcnt vmcnt(0)
	v_pk_mul_f32 v[140:141], v[138:139], s[54:55] op_sel_hi:[1,0]
	v_pk_mul_f32 v[138:139], v[136:137], s[54:55] op_sel_hi:[1,0]
	v_pk_mul_f32 v[136:137], v[152:153], s[54:55] op_sel_hi:[1,0]
	v_pk_mul_f32 v[152:153], v[124:125], v[138:139]
	v_mov_b32_e32 v124, v133
	v_cvt_pk_fp8_f32 v124, v152, v153
	v_pk_mul_f32 v[126:127], v[126:127], v[140:141]
	v_pk_mul_f32 v[112:113], v[112:113], v[136:137]
	v_pk_mul_f32 v[110:111], v[110:111], v[140:141]
	v_cvt_pk_fp8_f32 v124, v126, v127 op_sel:[0,0,1]
	v_mov_b32_e32 v127, v133
	v_cvt_pk_fp8_f32 v127, v112, v113
	v_pk_mul_f32 v[112:113], v[108:109], v[138:139]
	v_mov_b32_e32 v108, v133
	v_cvt_pk_fp8_f32 v108, v112, v113
	v_pk_mul_f32 v[96:97], v[96:97], v[136:137]
	v_pk_mul_f32 v[142:143], v[154:155], s[54:55] op_sel_hi:[1,0]
	v_pk_mul_f32 v[94:95], v[94:95], v[140:141]
	v_cvt_pk_fp8_f32 v108, v110, v111 op_sel:[0,0,1]
	v_mov_b32_e32 v111, v133
	v_cvt_pk_fp8_f32 v111, v96, v97
	v_pk_mul_f32 v[98:99], v[98:99], v[142:143]
	v_pk_mul_f32 v[80:81], v[80:81], v[136:137]
	v_pk_mul_f32 v[78:79], v[78:79], v[140:141]
	v_cvt_pk_fp8_f32 v111, v98, v99 op_sel:[0,0,1]
	v_pk_mul_f32 v[98:99], v[92:93], v[138:139]
	v_mov_b32_e32 v92, v133
	v_cvt_pk_fp8_f32 v92, v98, v99
	v_pk_mul_f32 v[120:121], v[120:121], v[136:137]
	v_mov_b32_e32 v125, v133
	v_pk_mul_f32 v[116:117], v[116:117], v[138:139]
	v_cvt_pk_fp8_f32 v92, v94, v95 op_sel:[0,0,1]
	v_mov_b32_e32 v95, v133
	v_cvt_pk_fp8_f32 v95, v80, v81
	v_pk_mul_f32 v[80:81], v[76:77], v[138:139]
	v_mov_b32_e32 v76, v133
	v_cvt_pk_fp8_f32 v76, v80, v81
	v_mov_b32_e32 v126, v133
	v_pk_mul_f32 v[104:105], v[104:105], v[136:137]
	v_mov_b32_e32 v109, v133
	v_pk_mul_f32 v[100:101], v[100:101], v[138:139]
	v_mov_b32_e32 v110, v133
	v_pk_mul_f32 v[88:89], v[88:89], v[136:137]
	v_mov_b32_e32 v93, v133
	v_pk_mul_f32 v[84:85], v[84:85], v[138:139]
	v_mov_b32_e32 v94, v133
	v_cvt_pk_fp8_f32 v76, v78, v79 op_sel:[0,0,1]
	v_pk_mul_f32 v[72:73], v[72:73], v[136:137]
	v_mov_b32_e32 v77, v133
	v_pk_mul_f32 v[68:69], v[68:69], v[138:139]
	v_mov_b32_e32 v78, v133
	v_pk_mul_f32 v[64:65], v[64:65], v[136:137]
	v_mov_b32_e32 v79, v133
	v_cvt_pk_fp8_f32 v125, v120, v121
	v_cvt_pk_fp8_f32 v126, v116, v117
	v_cvt_pk_fp8_f32 v109, v104, v105
	v_cvt_pk_fp8_f32 v110, v100, v101
	v_cvt_pk_fp8_f32 v93, v88, v89
	v_cvt_pk_fp8_f32 v94, v84, v85
	v_cvt_pk_fp8_f32 v77, v72, v73
	v_cvt_pk_fp8_f32 v78, v68, v69
	v_cvt_pk_fp8_f32 v79, v64, v65
	v_pk_mul_f32 v[122:123], v[122:123], v[142:143]
	v_pk_mul_f32 v[118:119], v[118:119], v[140:141]
	v_pk_mul_f32 v[114:115], v[114:115], v[142:143]
	v_pk_mul_f32 v[106:107], v[106:107], v[142:143]
	v_pk_mul_f32 v[102:103], v[102:103], v[140:141]
	v_pk_mul_f32 v[90:91], v[90:91], v[142:143]
	v_pk_mul_f32 v[86:87], v[86:87], v[140:141]
	v_pk_mul_f32 v[82:83], v[82:83], v[142:143]
	v_pk_mul_f32 v[74:75], v[74:75], v[142:143]
	v_pk_mul_f32 v[70:71], v[70:71], v[140:141]
	v_pk_mul_f32 v[66:67], v[66:67], v[142:143]
	v_cvt_pk_fp8_f32 v125, v122, v123 op_sel:[0,0,1]
	v_cvt_pk_fp8_f32 v126, v118, v119 op_sel:[0,0,1]
	v_cvt_pk_fp8_f32 v127, v114, v115 op_sel:[0,0,1]
	v_cvt_pk_fp8_f32 v109, v106, v107 op_sel:[0,0,1]
	v_cvt_pk_fp8_f32 v110, v102, v103 op_sel:[0,0,1]
	v_add_co_u32_e32 v96, vcc, s2, v128
	v_cvt_pk_fp8_f32 v93, v90, v91 op_sel:[0,0,1]
	v_cvt_pk_fp8_f32 v94, v86, v87 op_sel:[0,0,1]
	v_cvt_pk_fp8_f32 v95, v82, v83 op_sel:[0,0,1]
	v_cvt_pk_fp8_f32 v77, v74, v75 op_sel:[0,0,1]
	v_cvt_pk_fp8_f32 v78, v70, v71 op_sel:[0,0,1]
	v_cvt_pk_fp8_f32 v79, v66, v67 op_sel:[0,0,1]
	v_addc_co_u32_e32 v97, vcc, 0, v129, vcc
	s_mov_b32 s2, 0x40000
	v_add_co_u32_e32 v64, vcc, s2, v128
	s_mov_b32 s2, 0x50000
	s_nop 0
	v_addc_co_u32_e32 v65, vcc, 0, v129, vcc
	v_permlane32_swap_b32_e32 v124, v126
	v_permlane32_swap_b32_e32 v125, v127
	v_permlane32_swap_b32_e32 v108, v110
	v_permlane32_swap_b32_e32 v109, v111
	v_permlane32_swap_b32_e32 v92, v94
	v_permlane32_swap_b32_e32 v93, v95
	v_permlane32_swap_b32_e32 v76, v78
	v_permlane32_swap_b32_e32 v77, v79
	v_add_co_u32_e32 v66, vcc, s2, v128
	v_permlane16_swap_b32_e32 v124, v125
	v_permlane16_swap_b32_e32 v126, v127
	v_permlane16_swap_b32_e32 v108, v109
	v_permlane16_swap_b32_e32 v110, v111
	v_permlane16_swap_b32_e32 v92, v93
	v_permlane16_swap_b32_e32 v94, v95
	v_permlane16_swap_b32_e32 v76, v77
	v_permlane16_swap_b32_e32 v78, v79
	v_addc_co_u32_e32 v67, vcc, 0, v129, vcc
	global_store_dwordx4 v[128:129], v[124:127], off
	global_store_dwordx4 v[96:97], v[108:111], off
	global_store_dwordx4 v[64:65], v[92:95], off
	global_store_dwordx4 v[66:67], v[76:79], off
	global_load_dwordx4 v[68:71], v[130:131], off offset:512
	s_and_b64 vcc, exec, s[4:5]
	global_load_dwordx4 v[76:79], v[130:131], off offset:576
	s_mov_b64 s[2:3], s[48:49]
	s_waitcnt vmcnt(0)
	v_pk_mul_f32 v[72:73], v[70:71], s[54:55] op_sel_hi:[1,0]
	v_pk_mul_f32 v[70:71], v[68:69], s[54:55] op_sel_hi:[1,0]
	v_pk_mul_f32 v[68:69], v[76:77], s[54:55] op_sel_hi:[1,0]
	v_pk_mul_f32 v[76:77], v[60:61], v[70:71]
	v_mov_b32_e32 v60, v133
	v_cvt_pk_fp8_f32 v60, v76, v77
	v_pk_mul_f32 v[62:63], v[62:63], v[72:73]
	v_pk_mul_f32 v[48:49], v[48:49], v[68:69]
	v_pk_mul_f32 v[46:47], v[46:47], v[72:73]
	v_cvt_pk_fp8_f32 v60, v62, v63 op_sel:[0,0,1]
	v_mov_b32_e32 v63, v133
	v_cvt_pk_fp8_f32 v63, v48, v49
	v_pk_mul_f32 v[48:49], v[44:45], v[70:71]
	v_mov_b32_e32 v44, v133
	v_cvt_pk_fp8_f32 v44, v48, v49
	v_pk_mul_f32 v[32:33], v[32:33], v[68:69]
	v_pk_mul_f32 v[30:31], v[30:31], v[72:73]
	v_pk_mul_f32 v[16:17], v[16:17], v[68:69]
	v_cvt_pk_fp8_f32 v44, v46, v47 op_sel:[0,0,1]
	v_mov_b32_e32 v47, v133
	v_cvt_pk_fp8_f32 v47, v32, v33
	v_pk_mul_f32 v[32:33], v[28:29], v[70:71]
	v_mov_b32_e32 v28, v133
	v_cvt_pk_fp8_f32 v28, v32, v33
	v_pk_mul_f32 v[56:57], v[56:57], v[68:69]
	v_mov_b32_e32 v61, v133
	v_pk_mul_f32 v[52:53], v[52:53], v[70:71]
	v_cvt_pk_fp8_f32 v28, v30, v31 op_sel:[0,0,1]
	v_mov_b32_e32 v31, v133
	v_cvt_pk_fp8_f32 v31, v16, v17
	v_pk_mul_f32 v[16:17], v[12:13], v[70:71]
	v_mov_b32_e32 v12, v133
	v_cvt_pk_fp8_f32 v12, v16, v17
	v_mov_b32_e32 v62, v133
	v_pk_mul_f32 v[24:25], v[24:25], v[68:69]
	v_mov_b32_e32 v29, v133
	v_pk_mul_f32 v[20:21], v[20:21], v[70:71]
	v_mov_b32_e32 v30, v133
	v_pk_mul_f32 v[14:15], v[14:15], v[72:73]
	v_cvt_pk_fp8_f32 v61, v56, v57
	v_cvt_pk_fp8_f32 v62, v52, v53
	v_pk_mul_f32 v[40:41], v[40:41], v[68:69]
	v_mov_b32_e32 v45, v133
	v_pk_mul_f32 v[36:37], v[36:37], v[70:71]
	v_mov_b32_e32 v46, v133
	v_cvt_pk_fp8_f32 v29, v24, v25
	v_cvt_pk_fp8_f32 v30, v20, v21
	v_cvt_pk_fp8_f32 v12, v14, v15 op_sel:[0,0,1]
	v_pk_mul_f32 v[8:9], v[8:9], v[68:69]
	v_mov_b32_e32 v13, v133
	v_pk_mul_f32 v[4:5], v[4:5], v[70:71]
	v_mov_b32_e32 v14, v133
	v_pk_mul_f32 v[0:1], v[0:1], v[68:69]
	v_mov_b32_e32 v15, v133
	v_cvt_pk_fp8_f32 v45, v40, v41
	v_cvt_pk_fp8_f32 v46, v36, v37
	v_cvt_pk_fp8_f32 v13, v8, v9
	v_cvt_pk_fp8_f32 v14, v4, v5
	v_cvt_pk_fp8_f32 v15, v0, v1
	v_pk_mul_f32 v[74:75], v[78:79], s[54:55] op_sel_hi:[1,0]
	v_pk_mul_f32 v[54:55], v[54:55], v[72:73]
	v_pk_mul_f32 v[58:59], v[58:59], v[74:75]
	v_pk_mul_f32 v[50:51], v[50:51], v[74:75]
	v_pk_mul_f32 v[26:27], v[26:27], v[74:75]
	v_pk_mul_f32 v[22:23], v[22:23], v[72:73]
	v_pk_mul_f32 v[18:19], v[18:19], v[74:75]
	v_cvt_pk_fp8_f32 v61, v58, v59 op_sel:[0,0,1]
	v_cvt_pk_fp8_f32 v62, v54, v55 op_sel:[0,0,1]
	v_cvt_pk_fp8_f32 v63, v50, v51 op_sel:[0,0,1]
	v_pk_mul_f32 v[42:43], v[42:43], v[74:75]
	v_pk_mul_f32 v[38:39], v[38:39], v[72:73]
	v_pk_mul_f32 v[34:35], v[34:35], v[74:75]
	v_cvt_pk_fp8_f32 v29, v26, v27 op_sel:[0,0,1]
	v_cvt_pk_fp8_f32 v30, v22, v23 op_sel:[0,0,1]
	v_cvt_pk_fp8_f32 v31, v18, v19 op_sel:[0,0,1]
	v_pk_mul_f32 v[10:11], v[10:11], v[74:75]
	v_pk_mul_f32 v[6:7], v[6:7], v[72:73]
	v_pk_mul_f32 v[2:3], v[2:3], v[74:75]
	v_cvt_pk_fp8_f32 v45, v42, v43 op_sel:[0,0,1]
	v_cvt_pk_fp8_f32 v46, v38, v39 op_sel:[0,0,1]
	v_cvt_pk_fp8_f32 v47, v34, v35 op_sel:[0,0,1]
	v_cvt_pk_fp8_f32 v13, v10, v11 op_sel:[0,0,1]
	v_cvt_pk_fp8_f32 v14, v6, v7 op_sel:[0,0,1]
	v_cvt_pk_fp8_f32 v15, v2, v3 op_sel:[0,0,1]
	v_permlane32_swap_b32_e32 v60, v62
	v_permlane32_swap_b32_e32 v61, v63
	v_permlane32_swap_b32_e32 v28, v30
	v_permlane32_swap_b32_e32 v29, v31
	v_permlane16_swap_b32_e32 v60, v61
	v_permlane16_swap_b32_e32 v62, v63
	v_permlane32_swap_b32_e32 v44, v46
	v_permlane32_swap_b32_e32 v45, v47
	v_permlane16_swap_b32_e32 v28, v29
	v_permlane16_swap_b32_e32 v30, v31
	v_permlane32_swap_b32_e32 v12, v14
	v_permlane32_swap_b32_e32 v13, v15
	v_permlane16_swap_b32_e32 v44, v45
	v_permlane16_swap_b32_e32 v46, v47
	global_store_dwordx4 v[128:129], v[60:63], off offset:128
	global_store_dwordx4 v[96:97], v[44:47], off offset:128
	v_permlane16_swap_b32_e32 v12, v13
	v_permlane16_swap_b32_e32 v14, v15
	global_store_dwordx4 v[64:65], v[28:31], off offset:128
	global_store_dwordx4 v[66:67], v[12:15], off offset:128
	s_cbranch_vccz .LBB0_1496
	v_readlane_b32 s0, v252, 18
	s_waitcnt vmcnt(0)
	v_readlane_b32 s1, v252, 19
	s_andn2_b64 vcc, exec, s[0:1]
	s_cbranch_vccnz .LBB0_1227
	s_barrier
	s_branch .LBB0_1227

.LBB0_2382:
	ds_read_b128 v[140:143], v134
	ds_read_b128 v[144:147], v134 offset:1024
	ds_read_b128 v[148:151], v134 offset:2048
	ds_read_b128 v[152:155], v134 offset:3072
	s_add_u32 s18, s16, 0xfffd0080
	s_addc_u32 s19, s17, -1
	s_cmp_eq_u32 s54, 8
	s_cselect_b32 s21, s15, s19
	s_cselect_b32 s20, s14, s18
	s_cselect_b32 s19, s13, s53
	s_cselect_b32 s18, s12, s52
	v_mov_b32_e32 v128, v132
	ds_read_b128 v[156:159], v135
	ds_read_b128 v[160:163], v135 offset:1024
	ds_read_b128 v[164:167], v135 offset:2048
	ds_read_b128 v[168:171], v135 offset:3072
	ds_read_b128 v[172:175], v135 offset:4096
	ds_read_b128 v[176:179], v135 offset:5120
	ds_read_b128 v[180:183], v135 offset:6144
	ds_read_b128 v[184:187], v135 offset:7168
	s_nop 0
	v_mov_b32_e32 v128, v133
	s_nop 0
	s_waitcnt lgkmcnt(8)
	s_barrier
	s_waitcnt lgkmcnt(0)
	s_setprio 1
	s_waitcnt lgkmcnt(0)
	v_mfma_scale_f32_16x16x128_f8f6f4 v[124:127], v[140:147], v[156:163], v[124:127], v136, v136 op_sel_hi:[0,0,0]
	s_mov_b32 m0, s39
	v_mfma_scale_f32_16x16x128_f8f6f4 v[120:123], v[148:155], v[156:163], v[120:123], v136, v136 op_sel_hi:[0,0,0]
	global_load_lds_dwordx4 v132, s[16:17]
	v_mfma_scale_f32_16x16x128_f8f6f4 v[116:119], v[140:147], v[164:171], v[116:119], v136, v136 op_sel_hi:[0,0,0]
	s_mov_b32 m0, s40
	v_mfma_scale_f32_16x16x128_f8f6f4 v[112:115], v[148:155], v[164:171], v[112:115], v136, v136 op_sel_hi:[0,0,0]
	global_load_lds_dwordx4 v133, s[16:17]
	v_mfma_scale_f32_16x16x128_f8f6f4 v[188:191], v[140:147], v[172:179], v[108:111], v136, v136 op_sel_hi:[0,0,0]
	v_mfma_scale_f32_16x16x128_f8f6f4 v[192:195], v[148:155], v[172:179], v[104:107], v136, v136 op_sel_hi:[0,0,0]
	v_mfma_scale_f32_16x16x128_f8f6f4 v[196:199], v[140:147], v[180:187], v[100:103], v136, v136 op_sel_hi:[0,0,0]
	v_mfma_scale_f32_16x16x128_f8f6f4 v[200:203], v[148:155], v[180:187], v[96:99], v136, v136 op_sel_hi:[0,0,0]
	s_setprio 0
	s_barrier
	v_mov_b32_e32 v128, v132
	s_nop 2
	ds_read_b128 v[96:99], v137
	ds_read_b128 v[100:103], v137 offset:1024
	ds_read_b128 v[104:107], v137 offset:2048
	ds_read_b128 v[108:111], v137 offset:3072
	s_nop 0
	v_mov_b32_e32 v128, v133
	s_nop 0
	s_barrier
	s_waitcnt lgkmcnt(0)
	s_setprio 1
	s_waitcnt lgkmcnt(0)
	v_mfma_scale_f32_16x16x128_f8f6f4 v[204:207], v[96:103], v[156:163], v[92:95], v136, v136 op_sel_hi:[0,0,0]
	s_mov_b32 m0, s41
	v_mfma_scale_f32_16x16x128_f8f6f4 v[156:159], v[104:111], v[156:163], v[88:91], v136, v136 op_sel_hi:[0,0,0]
	global_load_lds_dwordx4 v132, s[18:19]
	v_mfma_scale_f32_16x16x128_f8f6f4 v[160:163], v[96:103], v[164:171], v[84:87], v136, v136 op_sel_hi:[0,0,0]
	s_mov_b32 m0, s42
	v_mfma_scale_f32_16x16x128_f8f6f4 v[164:167], v[104:111], v[164:171], v[80:83], v136, v136 op_sel_hi:[0,0,0]
	global_load_lds_dwordx4 v133, s[18:19]
	v_mfma_scale_f32_16x16x128_f8f6f4 v[168:171], v[96:103], v[172:179], v[76:79], v136, v136 op_sel_hi:[0,0,0]
	v_mfma_scale_f32_16x16x128_f8f6f4 v[172:175], v[104:111], v[172:179], v[72:75], v136, v136 op_sel_hi:[0,0,0]
	v_mfma_scale_f32_16x16x128_f8f6f4 v[176:179], v[96:103], v[180:187], v[68:71], v136, v136 op_sel_hi:[0,0,0]
	v_mfma_scale_f32_16x16x128_f8f6f4 v[180:183], v[104:111], v[180:187], v[64:67], v136, v136 op_sel_hi:[0,0,0]
	s_setprio 0
	v_mov_b32_e32 v128, v132
	s_barrier
	s_nop 2
	ds_read_b128 v[64:67], v135 offset:16384
	ds_read_b128 v[68:71], v135 offset:17408
	ds_read_b128 v[72:75], v135 offset:18432
	ds_read_b128 v[76:79], v135 offset:19456
	ds_read_b128 v[80:83], v135 offset:20480
	ds_read_b128 v[84:87], v135 offset:21504
	ds_read_b128 v[88:91], v135 offset:22528
	ds_read_b128 v[92:95], v135 offset:23552
	s_nop 0
	v_mov_b32_e32 v128, v133
	s_nop 0
	s_barrier
	s_waitcnt lgkmcnt(0)
	s_setprio 1
	s_waitcnt lgkmcnt(0)
	v_mfma_scale_f32_16x16x128_f8f6f4 v[60:63], v[140:147], v[64:71], v[60:63], v136, v136 op_sel_hi:[0,0,0]
	s_mov_b32 m0, s25
	v_mfma_scale_f32_16x16x128_f8f6f4 v[56:59], v[148:155], v[64:71], v[56:59], v136, v136 op_sel_hi:[0,0,0]
	global_load_lds_dwordx4 v132, s[20:21]
	v_mfma_scale_f32_16x16x128_f8f6f4 v[52:55], v[140:147], v[72:79], v[52:55], v136, v136 op_sel_hi:[0,0,0]
	s_mov_b32 m0, s26
	v_mfma_scale_f32_16x16x128_f8f6f4 v[48:51], v[148:155], v[72:79], v[48:51], v136, v136 op_sel_hi:[0,0,0]
	global_load_lds_dwordx4 v133, s[20:21]
	v_mfma_scale_f32_16x16x128_f8f6f4 v[184:187], v[140:147], v[80:87], v[44:47], v136, v136 op_sel_hi:[0,0,0]
	v_mfma_scale_f32_16x16x128_f8f6f4 v[208:211], v[148:155], v[80:87], v[40:43], v136, v136 op_sel_hi:[0,0,0]
	v_mfma_scale_f32_16x16x128_f8f6f4 v[212:215], v[140:147], v[88:95], v[36:39], v136, v136 op_sel_hi:[0,0,0]
	v_mfma_scale_f32_16x16x128_f8f6f4 v[216:219], v[148:155], v[88:95], v[32:35], v136, v136 op_sel_hi:[0,0,0]
	s_setprio 0
	s_barrier
	s_add_u32 s56, s18, 0x30000
	s_nop 3
	v_mov_b32_e32 v32, v132
	s_addc_u32 s57, s19, 0
	s_nop 0
	v_mov_b32_e32 v32, v133
	s_nop 0
	s_waitcnt vmcnt(4)
	s_barrier
	s_setprio 1
	v_mfma_scale_f32_16x16x128_f8f6f4 v[220:223], v[96:103], v[64:71], v[28:31], v136, v136 op_sel_hi:[0,0,0]
	s_mov_b32 m0, s43
	v_mfma_scale_f32_16x16x128_f8f6f4 v[224:227], v[104:111], v[64:71], v[24:27], v136, v136 op_sel_hi:[0,0,0]
	global_load_lds_dwordx4 v132, s[56:57]
	v_mfma_scale_f32_16x16x128_f8f6f4 v[228:231], v[96:103], v[72:79], v[20:23], v136, v136 op_sel_hi:[0,0,0]
	s_mov_b32 m0, s44
	v_mfma_scale_f32_16x16x128_f8f6f4 v[232:235], v[104:111], v[72:79], v[16:19], v136, v136 op_sel_hi:[0,0,0]
	global_load_lds_dwordx4 v133, s[56:57]
	v_mfma_scale_f32_16x16x128_f8f6f4 v[236:239], v[96:103], v[80:87], v[12:15], v136, v136 op_sel_hi:[0,0,0]
	v_mfma_scale_f32_16x16x128_f8f6f4 v[240:243], v[104:111], v[80:87], v[8:11], v136, v136 op_sel_hi:[0,0,0]
	v_mfma_scale_f32_16x16x128_f8f6f4 v[244:247], v[96:103], v[88:95], v[4:7], v136, v136 op_sel_hi:[0,0,0]
	v_mfma_scale_f32_16x16x128_f8f6f4 v[248:251], v[104:111], v[88:95], v[0:3], v136, v136 op_sel_hi:[0,0,0]
	s_setprio 0
	s_barrier
	s_nop 4
	ds_read_b128 v[0:3], v138
	ds_read_b128 v[4:7], v138 offset:1024
	ds_read_b128 v[8:11], v138 offset:2048
	ds_read_b128 v[12:15], v138 offset:3072
	s_add_u32 s56, s20, 0x30000
	v_mov_b32_e32 v64, v132
	ds_read_b128 v[16:19], v135 offset:32768
	ds_read_b128 v[20:23], v135 offset:33792
	ds_read_b128 v[24:27], v135 offset:34816
	ds_read_b128 v[28:31], v135 offset:35840
	ds_read_b128 v[32:35], v135 offset:36864
	ds_read_b128 v[36:39], v135 offset:37888
	ds_read_b128 v[40:43], v135 offset:38912
	ds_read_b128 v[44:47], v135 offset:39936
	s_addc_u32 s57, s21, 0
	s_nop 0
	v_mov_b32_e32 v64, v133
	s_nop 0
	s_waitcnt lgkmcnt(8)
	s_barrier
	s_waitcnt lgkmcnt(0)
	s_setprio 1
	s_waitcnt lgkmcnt(0)
	v_mfma_scale_f32_16x16x128_f8f6f4 v[124:127], v[0:7], v[16:23], v[124:127], v136, v136 op_sel_hi:[0,0,0]
	s_mov_b32 m0, s27
	v_mfma_scale_f32_16x16x128_f8f6f4 v[120:123], v[8:15], v[16:23], v[120:123], v136, v136 op_sel_hi:[0,0,0]
	global_load_lds_dwordx4 v132, s[56:57]
	v_mfma_scale_f32_16x16x128_f8f6f4 v[116:119], v[0:7], v[24:31], v[116:119], v136, v136 op_sel_hi:[0,0,0]
	s_mov_b32 m0, s28
	v_mfma_scale_f32_16x16x128_f8f6f4 v[112:115], v[8:15], v[24:31], v[112:115], v136, v136 op_sel_hi:[0,0,0]
	global_load_lds_dwordx4 v133, s[56:57]
	v_mfma_scale_f32_16x16x128_f8f6f4 v[108:111], v[0:7], v[32:39], v[188:191], v136, v136 op_sel_hi:[0,0,0]
	v_mfma_scale_f32_16x16x128_f8f6f4 v[104:107], v[8:15], v[32:39], v[192:195], v136, v136 op_sel_hi:[0,0,0]
	v_mfma_scale_f32_16x16x128_f8f6f4 v[100:103], v[0:7], v[40:47], v[196:199], v136, v136 op_sel_hi:[0,0,0]
	v_mfma_scale_f32_16x16x128_f8f6f4 v[96:99], v[8:15], v[40:47], v[200:203], v136, v136 op_sel_hi:[0,0,0]
	s_setprio 0
	s_barrier
	v_mov_b32_e32 v128, v132
	ds_read_b128 v[140:143], v139
	ds_read_b128 v[144:147], v139 offset:1024
	ds_read_b128 v[148:151], v139 offset:2048
	ds_read_b128 v[152:155], v139 offset:3072
	v_lshl_add_u64 v[64:65], s[18:19], 0, v[128:129]
	v_lshl_add_u64 v[64:65], v[64:65], 0, s[4:5]
	v_mov_b32_e32 v128, v133
	v_lshl_add_u64 v[64:65], s[18:19], 0, v[128:129]
	v_lshl_add_u64 v[64:65], v[64:65], 0, s[4:5]
	s_barrier
	s_waitcnt lgkmcnt(0)
	s_setprio 1
	s_waitcnt lgkmcnt(0)
	v_mfma_scale_f32_16x16x128_f8f6f4 v[92:95], v[140:147], v[16:23], v[204:207], v136, v136 op_sel_hi:[0,0,0]
	s_add_u32 s98, s18, s4
	s_addc_u32 s99, s19, s5
	s_mov_b32 m0, s46
	v_mfma_scale_f32_16x16x128_f8f6f4 v[88:91], v[148:155], v[16:23], v[156:159], v136, v136 op_sel_hi:[0,0,0]
	global_load_lds_dwordx4 v132, s[98:99]
	v_mfma_scale_f32_16x16x128_f8f6f4 v[84:87], v[140:147], v[24:31], v[160:163], v136, v136 op_sel_hi:[0,0,0]
	s_mov_b32 m0, s47
	v_mfma_scale_f32_16x16x128_f8f6f4 v[80:83], v[148:155], v[24:31], v[164:167], v136, v136 op_sel_hi:[0,0,0]
	global_load_lds_dwordx4 v133, s[98:99]
	v_mfma_scale_f32_16x16x128_f8f6f4 v[76:79], v[140:147], v[32:39], v[168:171], v136, v136 op_sel_hi:[0,0,0]
	v_mfma_scale_f32_16x16x128_f8f6f4 v[72:75], v[148:155], v[32:39], v[172:175], v136, v136 op_sel_hi:[0,0,0]
	v_mfma_scale_f32_16x16x128_f8f6f4 v[68:71], v[140:147], v[40:47], v[176:179], v136, v136 op_sel_hi:[0,0,0]
	v_mfma_scale_f32_16x16x128_f8f6f4 v[64:67], v[148:155], v[40:47], v[180:183], v136, v136 op_sel_hi:[0,0,0]
	s_setprio 0
	v_mov_b32_e32 v128, v132
	s_barrier
	ds_read_b128 v[16:19], v135 offset:49152
	ds_read_b128 v[20:23], v135 offset:50176
	ds_read_b128 v[156:159], v135 offset:51200
	ds_read_b128 v[160:163], v135 offset:52224
	ds_read_b128 v[164:167], v135 offset:53248
	ds_read_b128 v[168:171], v135 offset:54272
	ds_read_b128 v[172:175], v135 offset:55296
	ds_read_b128 v[176:179], v135 offset:56320
	v_lshl_add_u64 v[24:25], s[20:21], 0, v[128:129]
	v_lshl_add_u64 v[24:25], v[24:25], 0, s[4:5]
	v_mov_b32_e32 v128, v133
	v_lshl_add_u64 v[24:25], s[20:21], 0, v[128:129]
	v_lshl_add_u64 v[24:25], v[24:25], 0, s[4:5]
	s_barrier
	s_waitcnt lgkmcnt(0)
	s_setprio 1
	s_waitcnt lgkmcnt(0)
	v_mfma_scale_f32_16x16x128_f8f6f4 v[60:63], v[0:7], v[16:23], v[60:63], v136, v136 op_sel_hi:[0,0,0]
	s_add_u32 s98, s20, s4
	s_addc_u32 s99, s21, s5
	s_mov_b32 m0, s36
	v_mfma_scale_f32_16x16x128_f8f6f4 v[56:59], v[8:15], v[16:23], v[56:59], v136, v136 op_sel_hi:[0,0,0]
	global_load_lds_dwordx4 v132, s[98:99]
	v_mfma_scale_f32_16x16x128_f8f6f4 v[52:55], v[0:7], v[156:163], v[52:55], v136, v136 op_sel_hi:[0,0,0]
	s_mov_b32 m0, s37
	v_mfma_scale_f32_16x16x128_f8f6f4 v[48:51], v[8:15], v[156:163], v[48:51], v136, v136 op_sel_hi:[0,0,0]
	global_load_lds_dwordx4 v133, s[98:99]
	v_mfma_scale_f32_16x16x128_f8f6f4 v[44:47], v[0:7], v[164:171], v[184:187], v136, v136 op_sel_hi:[0,0,0]
	v_mfma_scale_f32_16x16x128_f8f6f4 v[40:43], v[8:15], v[164:171], v[208:211], v136, v136 op_sel_hi:[0,0,0]
	v_mfma_scale_f32_16x16x128_f8f6f4 v[36:39], v[0:7], v[172:179], v[212:215], v136, v136 op_sel_hi:[0,0,0]
	v_mfma_scale_f32_16x16x128_f8f6f4 v[32:35], v[8:15], v[172:179], v[216:219], v136, v136 op_sel_hi:[0,0,0]
	s_setprio 0
	s_barrier
	s_add_u32 s18, s18, 0x30080
	s_addc_u32 s19, s19, 0
	v_mov_b32_e32 v0, v132
	s_add_i32 s20, s45, s24
	s_nop 0
	v_mov_b32_e32 v0, v133
	s_nop 0
	s_waitcnt vmcnt(4)
	s_barrier
	s_setprio 1
	v_mfma_scale_f32_16x16x128_f8f6f4 v[28:31], v[140:147], v[16:23], v[220:223], v136, v136 op_sel_hi:[0,0,0]
	s_mov_b32 m0, s20
	v_mfma_scale_f32_16x16x128_f8f6f4 v[24:27], v[148:155], v[16:23], v[224:227], v136, v136 op_sel_hi:[0,0,0]
	global_load_lds_dwordx4 v132, s[18:19]
	v_mfma_scale_f32_16x16x128_f8f6f4 v[20:23], v[140:147], v[156:163], v[228:231], v136, v136 op_sel_hi:[0,0,0]
	s_add_i32 m0, s20, 0x2000
	v_mfma_scale_f32_16x16x128_f8f6f4 v[16:19], v[148:155], v[156:163], v[232:235], v136, v136 op_sel_hi:[0,0,0]
	global_load_lds_dwordx4 v133, s[18:19]
	v_mfma_scale_f32_16x16x128_f8f6f4 v[12:15], v[140:147], v[164:171], v[236:239], v136, v136 op_sel_hi:[0,0,0]
	v_mfma_scale_f32_16x16x128_f8f6f4 v[8:11], v[148:155], v[164:171], v[240:243], v136, v136 op_sel_hi:[0,0,0]
	v_mfma_scale_f32_16x16x128_f8f6f4 v[4:7], v[140:147], v[172:179], v[244:247], v136, v136 op_sel_hi:[0,0,0]
	v_mfma_scale_f32_16x16x128_f8f6f4 v[0:3], v[148:155], v[172:179], v[248:251], v136, v136 op_sel_hi:[0,0,0]
	s_setprio 0
	s_add_i32 s54, s54, 2
	s_add_u32 s16, s16, 0x100
	s_addc_u32 s17, s17, 0
	s_add_u32 s52, s52, 0x100
	s_addc_u32 s53, s53, 0
	s_cmp_gt_u32 s54, 9
	s_barrier
	s_cbranch_scc0 .LBB0_2382
	v_pk_mul_f32 v[140:141], v[124:125], s[8:9] op_sel_hi:[1,0]
	v_pk_mul_f32 v[120:121], v[120:121], s[8:9] op_sel_hi:[1,0]
	v_mov_b32_e32 v125, v129
	v_cvt_pk_fp8_f32 v125, v120, v121
	v_pk_mul_f32 v[120:121], v[126:127], s[8:9] op_sel_hi:[1,0]
	v_pk_mul_f32 v[116:117], v[116:117], s[8:9] op_sel_hi:[1,0]
	v_mov_b32_e32 v126, v129
	v_cvt_pk_fp8_f32 v126, v116, v117
	v_pk_mul_f32 v[112:113], v[112:113], s[8:9] op_sel_hi:[1,0]
	v_mov_b32_e32 v127, v129
	v_cvt_pk_fp8_f32 v127, v112, v113
	v_pk_mul_f32 v[112:113], v[118:119], s[8:9] op_sel_hi:[1,0]
	v_pk_mul_f32 v[104:105], v[104:105], s[8:9] op_sel_hi:[1,0]
	v_cvt_pk_fp8_f32 v126, v112, v113 op_sel:[0,0,1]
	v_pk_mul_f32 v[112:113], v[114:115], s[8:9] op_sel_hi:[1,0]
	v_pk_mul_f32 v[100:101], v[100:101], s[8:9] op_sel_hi:[1,0]
	v_cvt_pk_fp8_f32 v127, v112, v113 op_sel:[0,0,1]
	v_pk_mul_f32 v[112:113], v[108:109], s[8:9] op_sel_hi:[1,0]
	v_mov_b32_e32 v109, v129
	v_cvt_pk_fp8_f32 v109, v104, v105
	v_pk_mul_f32 v[104:105], v[110:111], s[8:9] op_sel_hi:[1,0]
	v_mov_b32_e32 v110, v129
	v_cvt_pk_fp8_f32 v110, v100, v101
	v_pk_mul_f32 v[100:101], v[92:93], s[8:9] op_sel_hi:[1,0]
	v_pk_mul_f32 v[88:89], v[88:89], s[8:9] op_sel_hi:[1,0]
	v_mov_b32_e32 v93, v129
	v_cvt_pk_fp8_f32 v93, v88, v89
	v_pk_mul_f32 v[88:89], v[94:95], s[8:9] op_sel_hi:[1,0]
	v_pk_mul_f32 v[84:85], v[84:85], s[8:9] op_sel_hi:[1,0]
	v_mov_b32_e32 v94, v129
	v_cvt_pk_fp8_f32 v94, v84, v85
	v_pk_mul_f32 v[80:81], v[80:81], s[8:9] op_sel_hi:[1,0]
	v_mov_b32_e32 v95, v129
	v_cvt_pk_fp8_f32 v95, v80, v81
	v_pk_mul_f32 v[80:81], v[86:87], s[8:9] op_sel_hi:[1,0]
	v_pk_mul_f32 v[72:73], v[72:73], s[8:9] op_sel_hi:[1,0]
	v_cvt_pk_fp8_f32 v94, v80, v81 op_sel:[0,0,1]
	v_pk_mul_f32 v[80:81], v[82:83], s[8:9] op_sel_hi:[1,0]
	v_pk_mul_f32 v[68:69], v[68:69], s[8:9] op_sel_hi:[1,0]
	v_cvt_pk_fp8_f32 v95, v80, v81 op_sel:[0,0,1]
	v_pk_mul_f32 v[80:81], v[76:77], s[8:9] op_sel_hi:[1,0]
	v_mov_b32_e32 v77, v129
	v_cvt_pk_fp8_f32 v77, v72, v73
	v_pk_mul_f32 v[72:73], v[78:79], s[8:9] op_sel_hi:[1,0]
	v_mov_b32_e32 v78, v129
	v_cvt_pk_fp8_f32 v78, v68, v69
	v_pk_mul_f32 v[64:65], v[64:65], s[8:9] op_sel_hi:[1,0]
	v_mov_b32_e32 v79, v129
	v_cvt_pk_fp8_f32 v79, v64, v65
	v_pk_mul_f32 v[64:65], v[70:71], s[8:9] op_sel_hi:[1,0]
	v_pk_mul_f32 v[56:57], v[56:57], s[8:9] op_sel_hi:[1,0]
	v_cvt_pk_fp8_f32 v78, v64, v65 op_sel:[0,0,1]
	v_pk_mul_f32 v[64:65], v[66:67], s[8:9] op_sel_hi:[1,0]
	v_pk_mul_f32 v[52:53], v[52:53], s[8:9] op_sel_hi:[1,0]
	v_cvt_pk_fp8_f32 v79, v64, v65 op_sel:[0,0,1]
	v_pk_mul_f32 v[64:65], v[60:61], s[8:9] op_sel_hi:[1,0]
	v_mov_b32_e32 v61, v129
	v_cvt_pk_fp8_f32 v61, v56, v57
	v_pk_mul_f32 v[56:57], v[62:63], s[8:9] op_sel_hi:[1,0]
	v_mov_b32_e32 v62, v129
	v_cvt_pk_fp8_f32 v62, v52, v53
	v_pk_mul_f32 v[48:49], v[48:49], s[8:9] op_sel_hi:[1,0]
	v_mov_b32_e32 v63, v129
	v_cvt_pk_fp8_f32 v63, v48, v49
	s_lshl_b32 s16, s50, 8
	v_pk_mul_f32 v[48:49], v[54:55], s[8:9] op_sel_hi:[1,0]
	s_add_i32 s16, s16, s34
	v_cvt_pk_fp8_f32 v62, v48, v49 op_sel:[0,0,1]
	v_pk_mul_f32 v[48:49], v[50:51], s[8:9] op_sel_hi:[1,0]
	s_lshl_b32 s18, s51, 8
	s_ashr_i32 s17, s16, 31
	v_cvt_pk_fp8_f32 v63, v48, v49 op_sel:[0,0,1]
	v_pk_mul_f32 v[48:49], v[44:45], s[8:9] op_sel_hi:[1,0]
	v_pk_mul_f32 v[40:41], v[40:41], s[8:9] op_sel_hi:[1,0]
	v_mov_b32_e32 v45, v129
	s_ashr_i32 s19, s18, 31
	s_lshl_b64 s[20:21], s[16:17], 11
	v_cvt_pk_fp8_f32 v45, v40, v41
	v_pk_mul_f32 v[40:41], v[46:47], s[8:9] op_sel_hi:[1,0]
	v_pk_mul_f32 v[36:37], v[36:37], s[8:9] op_sel_hi:[1,0]
	v_mov_b32_e32 v46, v129
	s_add_u32 s17, s31, s20
	v_cvt_pk_fp8_f32 v46, v36, v37
	v_pk_mul_f32 v[36:37], v[28:29], s[8:9] op_sel_hi:[1,0]
	v_pk_mul_f32 v[24:25], v[24:25], s[8:9] op_sel_hi:[1,0]
	v_mov_b32_e32 v29, v129
	s_addc_u32 s20, s33, s21
	v_cvt_pk_fp8_f32 v29, v24, v25
	v_pk_mul_f32 v[24:25], v[30:31], s[8:9] op_sel_hi:[1,0]
	v_pk_mul_f32 v[20:21], v[20:21], s[8:9] op_sel_hi:[1,0]
	v_mov_b32_e32 v30, v129
	s_add_u32 s17, s17, s18
	v_cvt_pk_fp8_f32 v30, v20, v21
	v_pk_mul_f32 v[16:17], v[16:17], s[8:9] op_sel_hi:[1,0]
	v_mov_b32_e32 v31, v129
	s_addc_u32 s21, s20, s19
	v_cvt_pk_fp8_f32 v31, v16, v17
	s_add_u32 s20, s17, s35
	s_addc_u32 s21, s21, 0
	s_addk_i32 s16, 0x80
	v_pk_mul_f32 v[16:17], v[22:23], s[8:9] op_sel_hi:[1,0]
	s_ashr_i32 s17, s16, 31
	v_cvt_pk_fp8_f32 v30, v16, v17 op_sel:[0,0,1]
	v_pk_mul_f32 v[16:17], v[18:19], s[8:9] op_sel_hi:[1,0]
	v_mov_b32_e32 v124, v129
	v_mov_b32_e32 v108, v129
	v_pk_mul_f32 v[96:97], v[96:97], s[8:9] op_sel_hi:[1,0]
	v_mov_b32_e32 v111, v129
	v_mov_b32_e32 v92, v129
	s_lshl_b64 s[16:17], s[16:17], 11
	v_mov_b32_e32 v60, v129
	v_mov_b32_e32 v44, v129
	v_mov_b32_e32 v28, v129
	v_cvt_pk_fp8_f32 v31, v16, v17 op_sel:[0,0,1]
	v_pk_mul_f32 v[16:17], v[12:13], s[8:9] op_sel_hi:[1,0]
	v_pk_mul_f32 v[8:9], v[8:9], s[8:9] op_sel_hi:[1,0]
	v_mov_b32_e32 v13, v129
	v_mbcnt_lo_u32_b32 v128, -1, 0
	v_mbcnt_hi_u32_b32 v128, -1, v128
	v_cvt_pk_fp8_f32 v124, v140, v141
	v_ashrrev_i32_e32 v130, 1, v128
	v_cvt_pk_fp8_f32 v108, v112, v113
	v_cvt_pk_fp8_f32 v111, v96, v97
	v_cvt_pk_fp8_f32 v92, v100, v101
	v_mov_b32_e32 v76, v129
	v_cvt_pk_fp8_f32 v60, v64, v65
	v_cvt_pk_fp8_f32 v44, v48, v49
	v_pk_mul_f32 v[32:33], v[32:33], s[8:9] op_sel_hi:[1,0]
	v_mov_b32_e32 v47, v129
	s_add_u32 s16, s31, s16
	v_cvt_pk_fp8_f32 v28, v36, v37
	v_mov_b32_e32 v12, v129
	v_cvt_pk_fp8_f32 v13, v8, v9
	v_pk_mul_f32 v[8:9], v[14:15], s[8:9] op_sel_hi:[1,0]
	v_pk_mul_f32 v[4:5], v[4:5], s[8:9] op_sel_hi:[1,0]
	v_mov_b32_e32 v14, v129
	v_bfi_b32 v130, -16, v130, v128
	v_cvt_pk_fp8_f32 v76, v80, v81
	v_cvt_pk_fp8_f32 v47, v32, v33
	s_addc_u32 s17, s33, s17
	v_cvt_pk_fp8_f32 v12, v16, v17
	v_cvt_pk_fp8_f32 v14, v4, v5
	v_pk_mul_f32 v[0:1], v[0:1], s[8:9] op_sel_hi:[1,0]
	v_mov_b32_e32 v15, v129
	v_ashrrev_i32_e32 v131, 31, v130
	v_pk_mul_f32 v[96:97], v[102:103], s[8:9] op_sel_hi:[1,0]
	s_add_u32 s16, s16, s18
	v_cvt_pk_fp8_f32 v15, v0, v1
	v_lshlrev_b64 v[130:131], 11, v[130:131]
	v_cvt_pk_fp8_f32 v110, v96, v97 op_sel:[0,0,1]
	v_pk_mul_f32 v[96:97], v[98:99], s[8:9] op_sel_hi:[1,0]
	v_pk_mul_f32 v[32:33], v[38:39], s[8:9] op_sel_hi:[1,0]
	s_addc_u32 s17, s17, s19
	v_and_b32_e32 v128, 16, v128
	v_cvt_pk_fp8_f32 v124, v120, v121 op_sel:[0,0,1]
	v_pk_mul_f32 v[120:121], v[122:123], s[8:9] op_sel_hi:[1,0]
	v_cvt_pk_fp8_f32 v108, v104, v105 op_sel:[0,0,1]
	v_pk_mul_f32 v[104:105], v[106:107], s[8:9] op_sel_hi:[1,0]
	v_cvt_pk_fp8_f32 v111, v96, v97 op_sel:[0,0,1]
	v_lshl_add_u64 v[96:97], s[20:21], 0, v[130:131]
	v_cvt_pk_fp8_f32 v92, v88, v89 op_sel:[0,0,1]
	v_pk_mul_f32 v[88:89], v[90:91], s[8:9] op_sel_hi:[1,0]
	v_cvt_pk_fp8_f32 v60, v56, v57 op_sel:[0,0,1]
	v_pk_mul_f32 v[56:57], v[58:59], s[8:9] op_sel_hi:[1,0]
	v_cvt_pk_fp8_f32 v44, v40, v41 op_sel:[0,0,1]
	v_pk_mul_f32 v[40:41], v[42:43], s[8:9] op_sel_hi:[1,0]
	v_cvt_pk_fp8_f32 v46, v32, v33 op_sel:[0,0,1]
	v_pk_mul_f32 v[32:33], v[34:35], s[8:9] op_sel_hi:[1,0]
	s_add_u32 s16, s16, s35
	v_cvt_pk_fp8_f32 v28, v24, v25 op_sel:[0,0,1]
	v_pk_mul_f32 v[24:25], v[26:27], s[8:9] op_sel_hi:[1,0]
	v_pk_mul_f32 v[0:1], v[6:7], s[8:9] op_sel_hi:[1,0]
	v_cvt_pk_fp8_f32 v125, v120, v121 op_sel:[0,0,1]
	v_cvt_pk_fp8_f32 v109, v104, v105 op_sel:[0,0,1]
	v_lshl_add_u64 v[96:97], v[96:97], 0, v[128:129]
	v_cvt_pk_fp8_f32 v93, v88, v89 op_sel:[0,0,1]
	v_cvt_pk_fp8_f32 v76, v72, v73 op_sel:[0,0,1]
	v_pk_mul_f32 v[72:73], v[74:75], s[8:9] op_sel_hi:[1,0]
	v_cvt_pk_fp8_f32 v61, v56, v57 op_sel:[0,0,1]
	v_cvt_pk_fp8_f32 v45, v40, v41 op_sel:[0,0,1]
	v_cvt_pk_fp8_f32 v47, v32, v33 op_sel:[0,0,1]
	s_addc_u32 s17, s17, 0
	v_cvt_pk_fp8_f32 v29, v24, v25 op_sel:[0,0,1]
	v_cvt_pk_fp8_f32 v12, v8, v9 op_sel:[0,0,1]
	v_pk_mul_f32 v[8:9], v[10:11], s[8:9] op_sel_hi:[1,0]
	v_cvt_pk_fp8_f32 v14, v0, v1 op_sel:[0,0,1]
	v_pk_mul_f32 v[0:1], v[2:3], s[8:9] op_sel_hi:[1,0]
	v_add_co_u32_e32 v98, vcc, s30, v96
	v_cvt_pk_fp8_f32 v77, v72, v73 op_sel:[0,0,1]
	v_lshl_add_u64 v[32:33], s[16:17], 0, v[130:131]
	v_cvt_pk_fp8_f32 v13, v8, v9 op_sel:[0,0,1]
	v_cvt_pk_fp8_f32 v15, v0, v1 op_sel:[0,0,1]
	v_addc_co_u32_e32 v99, vcc, 0, v97, vcc
	v_lshl_add_u64 v[32:33], v[32:33], 0, v[128:129]
	v_add_co_u32_e32 v34, vcc, s30, v32
	v_permlane32_swap_b32_e32 v124, v126
	v_permlane32_swap_b32_e32 v125, v127
	v_permlane32_swap_b32_e32 v108, v110
	v_permlane32_swap_b32_e32 v109, v111
	v_permlane32_swap_b32_e32 v92, v94
	v_permlane32_swap_b32_e32 v93, v95
	v_permlane32_swap_b32_e32 v60, v62
	v_permlane32_swap_b32_e32 v61, v63
	v_permlane32_swap_b32_e32 v44, v46
	v_permlane32_swap_b32_e32 v45, v47
	v_addc_co_u32_e32 v35, vcc, 0, v33, vcc
	v_permlane32_swap_b32_e32 v28, v30
	v_permlane32_swap_b32_e32 v29, v31
	v_permlane16_swap_b32_e32 v124, v125
	v_permlane16_swap_b32_e32 v126, v127
	v_permlane16_swap_b32_e32 v108, v109
	v_permlane16_swap_b32_e32 v110, v111
	v_permlane16_swap_b32_e32 v92, v93
	v_permlane16_swap_b32_e32 v94, v95
	v_permlane32_swap_b32_e32 v76, v78
	v_permlane32_swap_b32_e32 v77, v79
	v_permlane16_swap_b32_e32 v60, v61
	v_permlane16_swap_b32_e32 v62, v63
	v_permlane16_swap_b32_e32 v44, v45
	v_permlane16_swap_b32_e32 v46, v47
	v_permlane16_swap_b32_e32 v28, v29
	v_permlane16_swap_b32_e32 v30, v31
	v_permlane32_swap_b32_e32 v12, v14
	v_permlane32_swap_b32_e32 v13, v15
	s_and_b64 vcc, exec, s[10:11]
	s_mov_b32 s51, s49
	s_mov_b32 s50, s48
	s_mov_b64 s[18:19], s[12:13]
	s_mov_b64 s[16:17], s[14:15]
	global_store_dwordx4 v[96:97], v[124:127], off
	global_store_dwordx4 v[98:99], v[108:111], off
	v_permlane16_swap_b32_e32 v76, v77
	v_permlane16_swap_b32_e32 v78, v79
	global_store_dwordx4 v[96:97], v[92:95], off offset:128
	global_store_dwordx4 v[98:99], v[76:79], off offset:128
	global_store_dwordx4 v[32:33], v[60:63], off
	global_store_dwordx4 v[34:35], v[44:47], off
	v_permlane16_swap_b32_e32 v12, v13
	v_permlane16_swap_b32_e32 v14, v15
	global_store_dwordx4 v[32:33], v[28:31], off offset:128
	global_store_dwordx4 v[34:35], v[12:15], off offset:128
	s_cbranch_vccz .LBB0_2377
	s_waitcnt vmcnt(0)
	v_readlane_b32 s0, v252, 2
	s_cmpk_gt_u32 s0, 0xff
	s_cbranch_scc1 .LBB0_2386
	s_barrier

.LBB0_3995:
	s_add_i32 s34, s6, 2
	s_add_u32 s8, s4, 0xfffe0080
	s_addc_u32 s7, s5, -1
	s_add_i32 s30, 0, 0x10000
	v_add_u32_e32 v140, s30, v200
	ds_read_b128 v[128:131], v140
	ds_read_b128 v[132:135], v140 offset:1024
	ds_read_b128 v[136:139], v140 offset:2048
	ds_read_b128 v[140:143], v140 offset:3072
	s_cmp_eq_u32 s12, s6
	s_cselect_b32 s6, s52, s8
	s_cselect_b32 s7, s53, s7
	s_cselect_b32 s9, s55, s27
	s_cselect_b32 s8, s54, s25
	v_mov_b32_e32 v168, v169
	ds_read_b128 v[144:147], v182
	ds_read_b128 v[148:151], v182 offset:1024
	ds_read_b128 v[152:155], v182 offset:2048
	ds_read_b128 v[156:159], v182 offset:3072
	ds_read_b128 v[160:163], v182 offset:4096
	ds_read_b128 v[164:167], v182 offset:5120
	ds_read_b128 v[184:187], v182 offset:6144
	ds_read_b128 v[188:191], v182 offset:7168
	s_nop 0
	v_mov_b32_e32 v168, v181
	s_nop 0
	s_waitcnt lgkmcnt(8)
	s_barrier
	s_waitcnt lgkmcnt(0)
	s_setprio 1
	s_waitcnt lgkmcnt(0)
	v_mfma_scale_f32_16x16x128_f8f6f4 v[120:123], v[128:135], v[144:151], v[120:123], v183, v183 op_sel_hi:[0,0,0]
	s_add_i32 m0, s3, 0xc000
	v_mov_b32_e32 v170, v200
	v_mfma_scale_f32_16x16x128_f8f6f4 v[124:127], v[136:143], v[144:151], v[124:127], v183, v183 op_sel_hi:[0,0,0]
	global_load_lds_dwordx4 v169, s[4:5]
	v_mfma_scale_f32_16x16x128_f8f6f4 v[200:203], v[136:143], v[160:167], v[88:91], v183, v183 op_sel_hi:[0,0,0]
	s_add_i32 m0, s3, 0xe000
	v_mfma_scale_f32_16x16x128_f8f6f4 v[176:179], v[128:135], v[152:159], v[108:111], v183, v183 op_sel_hi:[0,0,0]
	global_load_lds_dwordx4 v181, s[4:5]
	v_mfma_scale_f32_16x16x128_f8f6f4 v[192:195], v[136:143], v[152:159], v[104:107], v183, v183 op_sel_hi:[0,0,0]
	v_mfma_scale_f32_16x16x128_f8f6f4 v[196:199], v[128:135], v[160:167], v[92:95], v183, v183 op_sel_hi:[0,0,0]
	v_mfma_scale_f32_16x16x128_f8f6f4 v[204:207], v[128:135], v[184:191], v[76:79], v183, v183 op_sel_hi:[0,0,0]
	v_mfma_scale_f32_16x16x128_f8f6f4 v[208:211], v[136:143], v[184:191], v[72:75], v183, v183 op_sel_hi:[0,0,0]
	s_setprio 0
	s_barrier
	s_add_i32 s35, 0, 0x14000
	s_nop 1
	v_add_u32_e32 v92, s35, v170
	v_mov_b32_e32 v104, v180
	s_add_i32 s30, s30, s33
	ds_read_b128 v[72:75], v92
	ds_read_b128 v[76:79], v92 offset:1024
	ds_read_b128 v[88:91], v92 offset:2048
	ds_read_b128 v[92:95], v92 offset:3072
	s_mov_b32 m0, s30
	s_nop 0
	global_load_lds_dwordx4 v104, s[8:9]
	v_mov_b32_e32 v104, v212
	s_add_i32 m0, s30, 0x2000
	s_nop 0
	global_load_lds_dwordx4 v104, s[8:9]
	s_barrier
	s_waitcnt lgkmcnt(0)
	s_setprio 1
	s_waitcnt lgkmcnt(0)
	v_mfma_scale_f32_16x16x128_f8f6f4 v[116:119], v[144:151], v[72:79], v[116:119], v183, v183 op_sel_hi:[0,0,0]
	v_mov_b32_e32 v168, v212
	v_mfma_scale_f32_16x16x128_f8f6f4 v[112:115], v[144:151], v[88:95], v[112:115], v183, v183 op_sel_hi:[0,0,0]
	v_mfma_scale_f32_16x16x128_f8f6f4 v[212:215], v[152:159], v[72:79], v[100:103], v183, v183 op_sel_hi:[0,0,0]
	v_mfma_scale_f32_16x16x128_f8f6f4 v[216:219], v[152:159], v[88:95], v[96:99], v183, v183 op_sel_hi:[0,0,0]
	v_mfma_scale_f32_16x16x128_f8f6f4 v[220:223], v[160:167], v[72:79], v[84:87], v183, v183 op_sel_hi:[0,0,0]
	v_mfma_scale_f32_16x16x128_f8f6f4 v[160:163], v[160:167], v[88:95], v[80:83], v183, v183 op_sel_hi:[0,0,0]
	v_mfma_scale_f32_16x16x128_f8f6f4 v[164:167], v[184:191], v[72:79], v[68:71], v183, v183 op_sel_hi:[0,0,0]
	v_mfma_scale_f32_16x16x128_f8f6f4 v[184:187], v[184:191], v[88:95], v[64:67], v183, v183 op_sel_hi:[0,0,0]
	s_setprio 0
	v_mov_b32_e32 v144, v169
	s_barrier
	s_nop 2
	ds_read_b128 v[64:67], v182 offset:16384
	ds_read_b128 v[68:71], v182 offset:17408
	ds_read_b128 v[80:83], v182 offset:18432
	ds_read_b128 v[84:87], v182 offset:19456
	ds_read_b128 v[96:99], v182 offset:20480
	ds_read_b128 v[100:103], v182 offset:21504
	ds_read_b128 v[104:107], v182 offset:22528
	ds_read_b128 v[108:111], v182 offset:23552
	s_nop 0
	v_mov_b32_e32 v144, v181
	s_nop 0
	s_barrier
	s_waitcnt lgkmcnt(0)
	s_setprio 1
	s_waitcnt lgkmcnt(0)
	v_mfma_scale_f32_16x16x128_f8f6f4 v[224:227], v[128:135], v[64:71], v[60:63], v183, v183 op_sel_hi:[0,0,0]
	s_mov_b32 m0, s3
	v_mfma_scale_f32_16x16x128_f8f6f4 v[228:231], v[136:143], v[64:71], v[56:59], v183, v183 op_sel_hi:[0,0,0]
	global_load_lds_dwordx4 v169, s[6:7]
	v_mfma_scale_f32_16x16x128_f8f6f4 v[232:235], v[128:135], v[80:87], v[44:47], v183, v183 op_sel_hi:[0,0,0]
	s_mov_b32 m0, s11
	v_mfma_scale_f32_16x16x128_f8f6f4 v[236:239], v[136:143], v[80:87], v[40:43], v183, v183 op_sel_hi:[0,0,0]
	global_load_lds_dwordx4 v181, s[6:7]
	v_mfma_scale_f32_16x16x128_f8f6f4 v[240:243], v[128:135], v[96:103], v[28:31], v183, v183 op_sel_hi:[0,0,0]
	v_mfma_scale_f32_16x16x128_f8f6f4 v[244:247], v[136:143], v[96:103], v[24:27], v183, v183 op_sel_hi:[0,0,0]
	v_mfma_scale_f32_16x16x128_f8f6f4 v[248:251], v[128:135], v[104:111], v[12:15], v183, v183 op_sel_hi:[0,0,0]
	v_mfma_scale_f32_16x16x128_f8f6f4 v[172:175], v[136:143], v[104:111], v[8:11], v183, v183 op_sel_hi:[0,0,0]
	s_setprio 0
	s_barrier
	s_add_u32 s30, s8, s20
	s_addc_u32 s31, s9, s21
	s_nop 2
	v_mov_b32_e32 v8, v180
	s_add_i32 s35, s35, s33
	s_mov_b32 s100, s35
	s_nop 0
	v_mov_b32_e32 v8, v168
	s_add_i32 s101, s35, 0x2000
	s_nop 0
	s_waitcnt vmcnt(4)
	s_barrier
	s_setprio 1
	v_mfma_scale_f32_16x16x128_f8f6f4 v[52:55], v[64:71], v[72:79], v[52:55], v183, v183 op_sel_hi:[0,0,0]
	s_mov_b32 m0, s100
	v_mfma_scale_f32_16x16x128_f8f6f4 v[48:51], v[64:71], v[88:95], v[48:51], v183, v183 op_sel_hi:[0,0,0]
	global_load_lds_dwordx4 v180, s[30:31]
	v_mfma_scale_f32_16x16x128_f8f6f4 v[36:39], v[80:87], v[72:79], v[36:39], v183, v183 op_sel_hi:[0,0,0]
	s_mov_b32 m0, s101
	v_mfma_scale_f32_16x16x128_f8f6f4 v[32:35], v[80:87], v[88:95], v[32:35], v183, v183 op_sel_hi:[0,0,0]
	global_load_lds_dwordx4 v168, s[30:31]
	v_mfma_scale_f32_16x16x128_f8f6f4 v[20:23], v[96:103], v[72:79], v[20:23], v183, v183 op_sel_hi:[0,0,0]
	v_mfma_scale_f32_16x16x128_f8f6f4 v[16:19], v[96:103], v[88:95], v[16:19], v183, v183 op_sel_hi:[0,0,0]
	v_mfma_scale_f32_16x16x128_f8f6f4 v[4:7], v[104:111], v[72:79], v[4:7], v183, v183 op_sel_hi:[0,0,0]
	v_mfma_scale_f32_16x16x128_f8f6f4 v[0:3], v[104:111], v[88:95], v[0:3], v183, v183 op_sel_hi:[0,0,0]
	s_setprio 0
	s_add_i32 s35, 0, 0x18000
	v_add_u32_e32 v24, s35, v170
	s_barrier
	ds_read_b128 v[8:11], v24
	ds_read_b128 v[12:15], v24 offset:1024
	ds_read_b128 v[128:131], v24 offset:2048
	ds_read_b128 v[132:135], v24 offset:3072
	s_add_u32 s36, s6, 0x20000
	v_mov_b32_e32 v64, v169
	ds_read_b128 v[24:27], v182 offset:32768
	ds_read_b128 v[28:31], v182 offset:33792
	ds_read_b128 v[40:43], v182 offset:34816
	ds_read_b128 v[44:47], v182 offset:35840
	ds_read_b128 v[56:59], v182 offset:36864
	ds_read_b128 v[60:63], v182 offset:37888
	ds_read_b128 v[136:139], v182 offset:38912
	ds_read_b128 v[140:143], v182 offset:39936
	s_addc_u32 s37, s7, 0
	s_nop 0
	v_mov_b32_e32 v64, v181
	s_nop 0
	s_waitcnt lgkmcnt(8)
	s_barrier
	s_waitcnt lgkmcnt(0)
	s_setprio 1
	s_waitcnt lgkmcnt(0)
	v_mfma_scale_f32_16x16x128_f8f6f4 v[120:123], v[8:15], v[24:31], v[120:123], v183, v183 op_sel_hi:[0,0,0]
	s_mov_b32 m0, s14
	v_mfma_scale_f32_16x16x128_f8f6f4 v[124:127], v[128:135], v[24:31], v[124:127], v183, v183 op_sel_hi:[0,0,0]
	global_load_lds_dwordx4 v169, s[36:37]
	v_mfma_scale_f32_16x16x128_f8f6f4 v[108:111], v[8:15], v[40:47], v[176:179], v183, v183 op_sel_hi:[0,0,0]
	s_mov_b32 m0, s15
	v_mfma_scale_f32_16x16x128_f8f6f4 v[104:107], v[128:135], v[40:47], v[192:195], v183, v183 op_sel_hi:[0,0,0]
	global_load_lds_dwordx4 v181, s[36:37]
	v_mfma_scale_f32_16x16x128_f8f6f4 v[92:95], v[8:15], v[56:63], v[196:199], v183, v183 op_sel_hi:[0,0,0]
	v_mfma_scale_f32_16x16x128_f8f6f4 v[88:91], v[128:135], v[56:63], v[200:203], v183, v183 op_sel_hi:[0,0,0]
	v_mfma_scale_f32_16x16x128_f8f6f4 v[76:79], v[8:15], v[136:143], v[204:207], v183, v183 op_sel_hi:[0,0,0]
	s_nop 5
	v_mov_b32_e32 v200, v170
	v_mfma_scale_f32_16x16x128_f8f6f4 v[72:75], v[128:135], v[136:143], v[208:211], v183, v183 op_sel_hi:[0,0,0]
	s_setprio 0
	s_barrier
	s_add_i32 s36, 0, 0x1c000
	v_add_u32_e32 v64, s36, v200
	v_mov_b32_e32 v170, v180
	ds_read_b128 v[144:147], v64
	ds_read_b128 v[148:151], v64 offset:1024
	ds_read_b128 v[152:155], v64 offset:2048
	ds_read_b128 v[156:159], v64 offset:3072
	s_add_i32 s35, s35, s33
	v_lshl_add_u64 v[64:65], s[8:9], 0, v[170:171]
	v_lshl_add_u64 v[64:65], v[64:65], 0, s[62:63]
	v_mov_b32_e32 v170, v168
	v_lshl_add_u64 v[64:65], s[8:9], 0, v[170:171]
	v_lshl_add_u64 v[64:65], v[64:65], 0, s[62:63]
	s_barrier
	s_waitcnt lgkmcnt(0)
	s_setprio 1
	s_waitcnt lgkmcnt(0)
	v_mfma_scale_f32_16x16x128_f8f6f4 v[116:119], v[24:31], v[144:151], v[116:119], v183, v183 op_sel_hi:[0,0,0]
	s_add_u32 s98, s8, s62
	s_addc_u32 s99, s9, s63
	s_mov_b32 m0, s35
	v_mfma_scale_f32_16x16x128_f8f6f4 v[112:115], v[24:31], v[152:159], v[112:115], v183, v183 op_sel_hi:[0,0,0]
	global_load_lds_dwordx4 v180, s[98:99]
	v_mfma_scale_f32_16x16x128_f8f6f4 v[100:103], v[40:47], v[144:151], v[212:215], v183, v183 op_sel_hi:[0,0,0]
	s_add_i32 m0, s35, 0x2000
	v_mfma_scale_f32_16x16x128_f8f6f4 v[96:99], v[40:47], v[152:159], v[216:219], v183, v183 op_sel_hi:[0,0,0]
	global_load_lds_dwordx4 v168, s[98:99]
	s_nop 5
	v_mov_b32_e32 v212, v168
	v_mfma_scale_f32_16x16x128_f8f6f4 v[84:87], v[56:63], v[144:151], v[220:223], v183, v183 op_sel_hi:[0,0,0]
	v_mfma_scale_f32_16x16x128_f8f6f4 v[80:83], v[56:63], v[152:159], v[160:163], v183, v183 op_sel_hi:[0,0,0]
	v_mfma_scale_f32_16x16x128_f8f6f4 v[68:71], v[136:143], v[144:151], v[164:167], v183, v183 op_sel_hi:[0,0,0]
	v_mfma_scale_f32_16x16x128_f8f6f4 v[64:67], v[136:143], v[152:159], v[184:187], v183, v183 op_sel_hi:[0,0,0]
	s_setprio 0
	v_mov_b32_e32 v170, v169
	s_barrier
	ds_read_b128 v[136:139], v182 offset:49152
	ds_read_b128 v[140:143], v182 offset:50176
	ds_read_b128 v[160:163], v182 offset:51200
	ds_read_b128 v[164:167], v182 offset:52224
	ds_read_b128 v[184:187], v182 offset:53248
	ds_read_b128 v[188:191], v182 offset:54272
	ds_read_b128 v[192:195], v182 offset:55296
	ds_read_b128 v[196:199], v182 offset:56320
	v_lshl_add_u64 v[24:25], s[6:7], 0, v[170:171]
	v_lshl_add_u64 v[24:25], v[24:25], 0, s[62:63]
	v_mov_b32_e32 v170, v181
	v_lshl_add_u64 v[24:25], s[6:7], 0, v[170:171]
	v_lshl_add_u64 v[24:25], v[24:25], 0, s[62:63]
	s_barrier
	s_waitcnt lgkmcnt(0)
	s_setprio 1
	s_waitcnt lgkmcnt(0)
	v_mfma_scale_f32_16x16x128_f8f6f4 v[60:63], v[8:15], v[136:143], v[224:227], v183, v183 op_sel_hi:[0,0,0]
	s_add_u32 s98, s6, s62
	s_addc_u32 s99, s7, s63
	s_mov_b32 m0, s16
	v_mfma_scale_f32_16x16x128_f8f6f4 v[56:59], v[128:135], v[136:143], v[228:231], v183, v183 op_sel_hi:[0,0,0]
	global_load_lds_dwordx4 v169, s[98:99]
	v_mfma_scale_f32_16x16x128_f8f6f4 v[44:47], v[8:15], v[160:167], v[232:235], v183, v183 op_sel_hi:[0,0,0]
	s_mov_b32 m0, s17
	v_mfma_scale_f32_16x16x128_f8f6f4 v[40:43], v[128:135], v[160:167], v[236:239], v183, v183 op_sel_hi:[0,0,0]
	global_load_lds_dwordx4 v181, s[98:99]
	v_mfma_scale_f32_16x16x128_f8f6f4 v[28:31], v[8:15], v[184:191], v[240:243], v183, v183 op_sel_hi:[0,0,0]
	v_mfma_scale_f32_16x16x128_f8f6f4 v[24:27], v[128:135], v[184:191], v[244:247], v183, v183 op_sel_hi:[0,0,0]
	v_mfma_scale_f32_16x16x128_f8f6f4 v[12:15], v[8:15], v[192:199], v[248:251], v183, v183 op_sel_hi:[0,0,0]
	v_mfma_scale_f32_16x16x128_f8f6f4 v[8:11], v[128:135], v[192:199], v[172:175], v183, v183 op_sel_hi:[0,0,0]
	s_setprio 0
	s_barrier
	v_mov_b32_e32 v170, v180
	s_add_i32 s6, s36, s33
	v_lshl_add_u64 v[128:129], s[30:31], 0, v[170:171]
	v_lshl_add_u64 v[128:129], v[128:129], 0, s[62:63]
	s_mov_b32 s100, s6
	v_mov_b32_e32 v170, v168
	s_add_i32 s101, s6, 0x2000
	v_lshl_add_u64 v[128:129], s[30:31], 0, v[170:171]
	v_lshl_add_u64 v[128:129], v[128:129], 0, s[62:63]
	s_waitcnt vmcnt(4)
	s_barrier
	s_setprio 1
	v_mfma_scale_f32_16x16x128_f8f6f4 v[52:55], v[136:143], v[144:151], v[52:55], v183, v183 op_sel_hi:[0,0,0]
	s_add_u32 s98, s30, s62
	s_addc_u32 s99, s31, s63
	s_mov_b32 m0, s100
	v_mfma_scale_f32_16x16x128_f8f6f4 v[48:51], v[136:143], v[152:159], v[48:51], v183, v183 op_sel_hi:[0,0,0]
	global_load_lds_dwordx4 v180, s[98:99]
	v_mfma_scale_f32_16x16x128_f8f6f4 v[36:39], v[160:167], v[144:151], v[36:39], v183, v183 op_sel_hi:[0,0,0]
	s_mov_b32 m0, s101
	v_mfma_scale_f32_16x16x128_f8f6f4 v[32:35], v[160:167], v[152:159], v[32:35], v183, v183 op_sel_hi:[0,0,0]
	global_load_lds_dwordx4 v168, s[98:99]
	v_mfma_scale_f32_16x16x128_f8f6f4 v[20:23], v[184:191], v[144:151], v[20:23], v183, v183 op_sel_hi:[0,0,0]
	v_mfma_scale_f32_16x16x128_f8f6f4 v[16:19], v[184:191], v[152:159], v[16:19], v183, v183 op_sel_hi:[0,0,0]
	v_mfma_scale_f32_16x16x128_f8f6f4 v[4:7], v[192:199], v[144:151], v[4:7], v183, v183 op_sel_hi:[0,0,0]
	v_mfma_scale_f32_16x16x128_f8f6f4 v[0:3], v[192:199], v[152:159], v[0:3], v183, v183 op_sel_hi:[0,0,0]
	s_setprio 0
	s_add_u32 s4, s4, 0x100
	s_addc_u32 s5, s5, 0
	s_add_u32 s25, s25, 0x100
	s_addc_u32 s27, s27, 0
	s_cmp_ge_i32 s34, s13
	s_mov_b32 s6, s34
	s_barrier
	s_cbranch_scc0 .LBB0_3995

.LBB0_4066:
	s_add_i32 s34, s6, 2
	s_add_u32 s8, s4, 0xfffe0080
	s_addc_u32 s7, s5, -1
	s_add_i32 s30, 0, 0x10000
	v_add_u32_e32 v140, s30, v181
	ds_read_b128 v[128:131], v140
	ds_read_b128 v[132:135], v140 offset:1024
	ds_read_b128 v[136:139], v140 offset:2048
	ds_read_b128 v[140:143], v140 offset:3072
	s_cmp_eq_u32 s12, s6
	s_cselect_b32 s6, s52, s8
	s_cselect_b32 s7, s53, s7
	s_cselect_b32 s9, s55, s27
	s_cselect_b32 s8, s54, s25
	v_mov_b32_e32 v168, v169
	ds_read_b128 v[144:147], v182
	ds_read_b128 v[148:151], v182 offset:1024
	ds_read_b128 v[152:155], v182 offset:2048
	ds_read_b128 v[156:159], v182 offset:3072
	ds_read_b128 v[160:163], v182 offset:4096
	ds_read_b128 v[164:167], v182 offset:5120
	ds_read_b128 v[184:187], v182 offset:6144
	ds_read_b128 v[188:191], v182 offset:7168
	s_add_i32 m0, s3, 0xc000
	s_nop 0
	global_load_lds_dwordx4 v168, s[4:5]
	v_mov_b32_e32 v168, v200
	s_add_i32 m0, s3, 0xe000
	s_nop 0
	global_load_lds_dwordx4 v168, s[4:5]
	s_waitcnt lgkmcnt(8)
	s_barrier
	s_waitcnt lgkmcnt(0)
	s_setprio 1
	s_waitcnt lgkmcnt(0)
	v_mfma_scale_f32_16x16x128_f8f6f4 v[120:123], v[128:135], v[144:151], v[120:123], v183, v183 op_sel_hi:[0,0,0]
	v_mov_b32_e32 v170, v200
	v_mfma_scale_f32_16x16x128_f8f6f4 v[124:127], v[136:143], v[144:151], v[124:127], v183, v183 op_sel_hi:[0,0,0]
	v_mfma_scale_f32_16x16x128_f8f6f4 v[200:203], v[128:135], v[160:167], v[92:95], v183, v183 op_sel_hi:[0,0,0]
	v_mfma_scale_f32_16x16x128_f8f6f4 v[192:195], v[128:135], v[152:159], v[108:111], v183, v183 op_sel_hi:[0,0,0]
	v_mfma_scale_f32_16x16x128_f8f6f4 v[196:199], v[136:143], v[152:159], v[104:107], v183, v183 op_sel_hi:[0,0,0]
	v_mfma_scale_f32_16x16x128_f8f6f4 v[204:207], v[136:143], v[160:167], v[88:91], v183, v183 op_sel_hi:[0,0,0]
	v_mfma_scale_f32_16x16x128_f8f6f4 v[208:211], v[128:135], v[184:191], v[76:79], v183, v183 op_sel_hi:[0,0,0]
	v_mfma_scale_f32_16x16x128_f8f6f4 v[212:215], v[136:143], v[184:191], v[72:75], v183, v183 op_sel_hi:[0,0,0]
	s_setprio 0
	s_barrier
	s_add_i32 s35, 0, 0x14000
	v_add_u32_e32 v92, s35, v181
	v_mov_b32_e32 v104, v216
	s_add_i32 s30, s30, s33
	s_nop 0
	ds_read_b128 v[72:75], v92
	ds_read_b128 v[76:79], v92 offset:1024
	ds_read_b128 v[88:91], v92 offset:2048
	ds_read_b128 v[92:95], v92 offset:3072
	s_nop 0
	v_mov_b32_e32 v104, v180
	s_nop 0
	s_barrier
	s_waitcnt lgkmcnt(0)
	s_setprio 1
	s_waitcnt lgkmcnt(0)
	v_mfma_scale_f32_16x16x128_f8f6f4 v[116:119], v[72:79], v[144:151], v[116:119], v183, v183 op_sel_hi:[0,0,0]
	s_mov_b32 m0, s30
	v_mov_b32_e32 v168, v216
	v_mfma_scale_f32_16x16x128_f8f6f4 v[112:115], v[88:95], v[144:151], v[112:115], v183, v183 op_sel_hi:[0,0,0]
	global_load_lds_dwordx4 v216, s[8:9]
	v_mfma_scale_f32_16x16x128_f8f6f4 v[216:219], v[72:79], v[152:159], v[100:103], v183, v183 op_sel_hi:[0,0,0]
	s_add_i32 m0, s30, 0x2000
	v_mfma_scale_f32_16x16x128_f8f6f4 v[220:223], v[88:95], v[152:159], v[96:99], v183, v183 op_sel_hi:[0,0,0]
	global_load_lds_dwordx4 v180, s[8:9]
	v_mfma_scale_f32_16x16x128_f8f6f4 v[224:227], v[72:79], v[160:167], v[84:87], v183, v183 op_sel_hi:[0,0,0]
	v_mfma_scale_f32_16x16x128_f8f6f4 v[160:163], v[88:95], v[160:167], v[80:83], v183, v183 op_sel_hi:[0,0,0]
	v_mfma_scale_f32_16x16x128_f8f6f4 v[164:167], v[72:79], v[184:191], v[68:71], v183, v183 op_sel_hi:[0,0,0]
	v_mfma_scale_f32_16x16x128_f8f6f4 v[184:187], v[88:95], v[184:191], v[64:67], v183, v183 op_sel_hi:[0,0,0]
	s_setprio 0
	v_mov_b32_e32 v144, v169
	s_barrier
	s_nop 2
	ds_read_b128 v[64:67], v182 offset:16384
	ds_read_b128 v[68:71], v182 offset:17408
	ds_read_b128 v[80:83], v182 offset:18432
	ds_read_b128 v[84:87], v182 offset:19456
	ds_read_b128 v[96:99], v182 offset:20480
	ds_read_b128 v[100:103], v182 offset:21504
	ds_read_b128 v[104:107], v182 offset:22528
	ds_read_b128 v[108:111], v182 offset:23552
	s_nop 0
	v_mov_b32_e32 v144, v170
	s_nop 0
	s_barrier
	s_waitcnt lgkmcnt(0)
	s_setprio 1
	s_waitcnt lgkmcnt(0)
	v_mfma_scale_f32_16x16x128_f8f6f4 v[228:231], v[128:135], v[64:71], v[60:63], v183, v183 op_sel_hi:[0,0,0]
	s_mov_b32 m0, s3
	v_mfma_scale_f32_16x16x128_f8f6f4 v[232:235], v[136:143], v[64:71], v[56:59], v183, v183 op_sel_hi:[0,0,0]
	global_load_lds_dwordx4 v169, s[6:7]
	v_mfma_scale_f32_16x16x128_f8f6f4 v[236:239], v[128:135], v[80:87], v[44:47], v183, v183 op_sel_hi:[0,0,0]
	s_mov_b32 m0, s11
	v_mfma_scale_f32_16x16x128_f8f6f4 v[240:243], v[136:143], v[80:87], v[40:43], v183, v183 op_sel_hi:[0,0,0]
	global_load_lds_dwordx4 v170, s[6:7]
	v_mfma_scale_f32_16x16x128_f8f6f4 v[244:247], v[128:135], v[96:103], v[28:31], v183, v183 op_sel_hi:[0,0,0]
	v_mfma_scale_f32_16x16x128_f8f6f4 v[248:251], v[136:143], v[96:103], v[24:27], v183, v183 op_sel_hi:[0,0,0]
	v_mfma_scale_f32_16x16x128_f8f6f4 v[172:175], v[128:135], v[104:111], v[12:15], v183, v183 op_sel_hi:[0,0,0]
	v_mfma_scale_f32_16x16x128_f8f6f4 v[176:179], v[136:143], v[104:111], v[8:11], v183, v183 op_sel_hi:[0,0,0]
	s_setprio 0
	s_barrier
	s_add_u32 s30, s8, s20
	s_addc_u32 s31, s9, s21
	s_nop 2
	v_mov_b32_e32 v8, v168
	s_add_i32 s35, s35, s33
	s_mov_b32 s100, s35
	s_nop 0
	v_mov_b32_e32 v8, v180
	s_add_i32 s101, s35, 0x2000
	s_nop 0
	s_waitcnt vmcnt(4)
	s_barrier
	s_setprio 1
	v_mfma_scale_f32_16x16x128_f8f6f4 v[52:55], v[72:79], v[64:71], v[52:55], v183, v183 op_sel_hi:[0,0,0]
	s_mov_b32 m0, s100
	v_mfma_scale_f32_16x16x128_f8f6f4 v[48:51], v[88:95], v[64:71], v[48:51], v183, v183 op_sel_hi:[0,0,0]
	global_load_lds_dwordx4 v168, s[30:31]
	v_mfma_scale_f32_16x16x128_f8f6f4 v[36:39], v[72:79], v[80:87], v[36:39], v183, v183 op_sel_hi:[0,0,0]
	s_mov_b32 m0, s101
	v_mfma_scale_f32_16x16x128_f8f6f4 v[32:35], v[88:95], v[80:87], v[32:35], v183, v183 op_sel_hi:[0,0,0]
	global_load_lds_dwordx4 v180, s[30:31]
	v_mfma_scale_f32_16x16x128_f8f6f4 v[20:23], v[72:79], v[96:103], v[20:23], v183, v183 op_sel_hi:[0,0,0]
	v_mfma_scale_f32_16x16x128_f8f6f4 v[16:19], v[88:95], v[96:103], v[16:19], v183, v183 op_sel_hi:[0,0,0]
	v_mfma_scale_f32_16x16x128_f8f6f4 v[4:7], v[72:79], v[104:111], v[4:7], v183, v183 op_sel_hi:[0,0,0]
	v_mfma_scale_f32_16x16x128_f8f6f4 v[0:3], v[88:95], v[104:111], v[0:3], v183, v183 op_sel_hi:[0,0,0]
	s_setprio 0
	s_add_i32 s35, 0, 0x18000
	v_add_u32_e32 v24, s35, v181
	s_barrier
	ds_read_b128 v[8:11], v24
	ds_read_b128 v[12:15], v24 offset:1024
	ds_read_b128 v[128:131], v24 offset:2048
	ds_read_b128 v[132:135], v24 offset:3072
	s_add_u32 s36, s6, 0x20000
	v_mov_b32_e32 v64, v169
	ds_read_b128 v[24:27], v182 offset:32768
	ds_read_b128 v[28:31], v182 offset:33792
	ds_read_b128 v[40:43], v182 offset:34816
	ds_read_b128 v[44:47], v182 offset:35840
	ds_read_b128 v[56:59], v182 offset:36864
	ds_read_b128 v[60:63], v182 offset:37888
	ds_read_b128 v[136:139], v182 offset:38912
	ds_read_b128 v[140:143], v182 offset:39936
	s_addc_u32 s37, s7, 0
	s_nop 0
	v_mov_b32_e32 v64, v170
	s_nop 0
	s_waitcnt lgkmcnt(8)
	s_barrier
	s_waitcnt lgkmcnt(0)
	s_setprio 1
	s_waitcnt lgkmcnt(0)
	v_mfma_scale_f32_16x16x128_f8f6f4 v[120:123], v[8:15], v[24:31], v[120:123], v183, v183 op_sel_hi:[0,0,0]
	s_mov_b32 m0, s14
	v_mfma_scale_f32_16x16x128_f8f6f4 v[124:127], v[128:135], v[24:31], v[124:127], v183, v183 op_sel_hi:[0,0,0]
	global_load_lds_dwordx4 v169, s[36:37]
	v_mfma_scale_f32_16x16x128_f8f6f4 v[108:111], v[8:15], v[40:47], v[192:195], v183, v183 op_sel_hi:[0,0,0]
	s_mov_b32 m0, s15
	v_mfma_scale_f32_16x16x128_f8f6f4 v[104:107], v[128:135], v[40:47], v[196:199], v183, v183 op_sel_hi:[0,0,0]
	global_load_lds_dwordx4 v170, s[36:37]
	v_mfma_scale_f32_16x16x128_f8f6f4 v[92:95], v[8:15], v[56:63], v[200:203], v183, v183 op_sel_hi:[0,0,0]
	v_mfma_scale_f32_16x16x128_f8f6f4 v[88:91], v[128:135], v[56:63], v[204:207], v183, v183 op_sel_hi:[0,0,0]
	s_nop 5
	v_mov_b32_e32 v200, v170
	v_mfma_scale_f32_16x16x128_f8f6f4 v[76:79], v[8:15], v[136:143], v[208:211], v183, v183 op_sel_hi:[0,0,0]
	v_mfma_scale_f32_16x16x128_f8f6f4 v[72:75], v[128:135], v[136:143], v[212:215], v183, v183 op_sel_hi:[0,0,0]
	s_setprio 0
	s_barrier
	s_add_i32 s36, 0, 0x1c000
	v_add_u32_e32 v64, s36, v181
	v_mov_b32_e32 v170, v168
	ds_read_b128 v[144:147], v64
	ds_read_b128 v[148:151], v64 offset:1024
	ds_read_b128 v[152:155], v64 offset:2048
	ds_read_b128 v[156:159], v64 offset:3072
	s_add_i32 s35, s35, s33
	v_lshl_add_u64 v[64:65], s[8:9], 0, v[170:171]
	v_lshl_add_u64 v[64:65], v[64:65], 0, s[62:63]
	v_mov_b32_e32 v170, v180
	v_lshl_add_u64 v[64:65], s[8:9], 0, v[170:171]
	v_lshl_add_u64 v[64:65], v[64:65], 0, s[62:63]
	s_barrier
	s_waitcnt lgkmcnt(0)
	s_setprio 1
	s_waitcnt lgkmcnt(0)
	v_mfma_scale_f32_16x16x128_f8f6f4 v[116:119], v[144:151], v[24:31], v[116:119], v183, v183 op_sel_hi:[0,0,0]
	s_add_u32 s98, s8, s62
	s_addc_u32 s99, s9, s63
	s_mov_b32 m0, s35
	v_mfma_scale_f32_16x16x128_f8f6f4 v[112:115], v[152:159], v[24:31], v[112:115], v183, v183 op_sel_hi:[0,0,0]
	global_load_lds_dwordx4 v168, s[98:99]
	v_mfma_scale_f32_16x16x128_f8f6f4 v[100:103], v[144:151], v[40:47], v[216:219], v183, v183 op_sel_hi:[0,0,0]
	s_add_i32 m0, s35, 0x2000
	v_mfma_scale_f32_16x16x128_f8f6f4 v[96:99], v[152:159], v[40:47], v[220:223], v183, v183 op_sel_hi:[0,0,0]
	global_load_lds_dwordx4 v180, s[98:99]
	s_nop 5
	v_mov_b32_e32 v216, v168
	v_mfma_scale_f32_16x16x128_f8f6f4 v[84:87], v[144:151], v[56:63], v[224:227], v183, v183 op_sel_hi:[0,0,0]
	v_mfma_scale_f32_16x16x128_f8f6f4 v[80:83], v[152:159], v[56:63], v[160:163], v183, v183 op_sel_hi:[0,0,0]
	v_mfma_scale_f32_16x16x128_f8f6f4 v[68:71], v[144:151], v[136:143], v[164:167], v183, v183 op_sel_hi:[0,0,0]
	v_mfma_scale_f32_16x16x128_f8f6f4 v[64:67], v[152:159], v[136:143], v[184:187], v183, v183 op_sel_hi:[0,0,0]
	s_setprio 0
	v_mov_b32_e32 v170, v169
	s_barrier
	ds_read_b128 v[136:139], v182 offset:49152
	ds_read_b128 v[140:143], v182 offset:50176
	ds_read_b128 v[160:163], v182 offset:51200
	ds_read_b128 v[164:167], v182 offset:52224
	ds_read_b128 v[184:187], v182 offset:53248
	ds_read_b128 v[188:191], v182 offset:54272
	ds_read_b128 v[192:195], v182 offset:55296
	ds_read_b128 v[196:199], v182 offset:56320
	v_lshl_add_u64 v[24:25], s[6:7], 0, v[170:171]
	v_lshl_add_u64 v[24:25], v[24:25], 0, s[62:63]
	v_mov_b32_e32 v170, v200
	v_lshl_add_u64 v[24:25], s[6:7], 0, v[170:171]
	v_lshl_add_u64 v[24:25], v[24:25], 0, s[62:63]
	s_barrier
	s_waitcnt lgkmcnt(0)
	s_setprio 1
	s_waitcnt lgkmcnt(0)
	v_mfma_scale_f32_16x16x128_f8f6f4 v[60:63], v[8:15], v[136:143], v[228:231], v183, v183 op_sel_hi:[0,0,0]
	s_add_u32 s98, s6, s62
	s_addc_u32 s99, s7, s63
	s_mov_b32 m0, s16
	v_mfma_scale_f32_16x16x128_f8f6f4 v[56:59], v[128:135], v[136:143], v[232:235], v183, v183 op_sel_hi:[0,0,0]
	global_load_lds_dwordx4 v169, s[98:99]
	v_mfma_scale_f32_16x16x128_f8f6f4 v[44:47], v[8:15], v[160:167], v[236:239], v183, v183 op_sel_hi:[0,0,0]
	s_mov_b32 m0, s17
	v_mfma_scale_f32_16x16x128_f8f6f4 v[40:43], v[128:135], v[160:167], v[240:243], v183, v183 op_sel_hi:[0,0,0]
	global_load_lds_dwordx4 v200, s[98:99]
	v_mfma_scale_f32_16x16x128_f8f6f4 v[28:31], v[8:15], v[184:191], v[244:247], v183, v183 op_sel_hi:[0,0,0]
	v_mfma_scale_f32_16x16x128_f8f6f4 v[24:27], v[128:135], v[184:191], v[248:251], v183, v183 op_sel_hi:[0,0,0]
	v_mfma_scale_f32_16x16x128_f8f6f4 v[12:15], v[8:15], v[192:199], v[172:175], v183, v183 op_sel_hi:[0,0,0]
	v_mfma_scale_f32_16x16x128_f8f6f4 v[8:11], v[128:135], v[192:199], v[176:179], v183, v183 op_sel_hi:[0,0,0]
	s_setprio 0
	s_barrier
	v_mov_b32_e32 v170, v168
	s_add_i32 s6, s36, s33
	v_lshl_add_u64 v[128:129], s[30:31], 0, v[170:171]
	v_lshl_add_u64 v[128:129], v[128:129], 0, s[62:63]
	s_mov_b32 s100, s6
	v_mov_b32_e32 v170, v180
	s_add_i32 s101, s6, 0x2000
	v_lshl_add_u64 v[128:129], s[30:31], 0, v[170:171]
	v_lshl_add_u64 v[128:129], v[128:129], 0, s[62:63]
	s_waitcnt vmcnt(4)
	s_barrier
	s_setprio 1
	v_mfma_scale_f32_16x16x128_f8f6f4 v[52:55], v[144:151], v[136:143], v[52:55], v183, v183 op_sel_hi:[0,0,0]
	s_add_u32 s98, s30, s62
	s_addc_u32 s99, s31, s63
	s_mov_b32 m0, s100
	v_mfma_scale_f32_16x16x128_f8f6f4 v[48:51], v[152:159], v[136:143], v[48:51], v183, v183 op_sel_hi:[0,0,0]
	global_load_lds_dwordx4 v168, s[98:99]
	v_mfma_scale_f32_16x16x128_f8f6f4 v[36:39], v[144:151], v[160:167], v[36:39], v183, v183 op_sel_hi:[0,0,0]
	s_mov_b32 m0, s101
	v_mfma_scale_f32_16x16x128_f8f6f4 v[32:35], v[152:159], v[160:167], v[32:35], v183, v183 op_sel_hi:[0,0,0]
	global_load_lds_dwordx4 v180, s[98:99]
	v_mfma_scale_f32_16x16x128_f8f6f4 v[20:23], v[144:151], v[184:191], v[20:23], v183, v183 op_sel_hi:[0,0,0]
	v_mfma_scale_f32_16x16x128_f8f6f4 v[16:19], v[152:159], v[184:191], v[16:19], v183, v183 op_sel_hi:[0,0,0]
	v_mfma_scale_f32_16x16x128_f8f6f4 v[4:7], v[144:151], v[192:199], v[4:7], v183, v183 op_sel_hi:[0,0,0]
	v_mfma_scale_f32_16x16x128_f8f6f4 v[0:3], v[152:159], v[192:199], v[0:3], v183, v183 op_sel_hi:[0,0,0]
	s_setprio 0
	s_add_u32 s4, s4, 0x100
	s_addc_u32 s5, s5, 0
	s_add_u32 s25, s25, 0x100
	s_addc_u32 s27, s27, 0
	s_cmp_ge_i32 s34, s13
	s_mov_b32 s6, s34
	s_barrier
	s_cbranch_scc0 .LBB0_4066

.LBB0_4932:
	ds_read_b128 v[146:149], v141
	ds_read_b128 v[150:153], v141 offset:1024
	ds_read_b128 v[154:157], v141 offset:2048
	ds_read_b128 v[158:161], v141 offset:3072
	s_add_u32 s22, s20, 0xfffc0080
	s_addc_u32 s23, s21, -1
	s_cmp_eq_u32 s50, 12
	s_cselect_b32 s25, s15, s23
	s_cselect_b32 s24, s14, s22
	s_cselect_b32 s23, s17, s13
	s_cselect_b32 s22, s16, s11
	v_mov_b32_e32 v128, v138
	ds_read_b128 v[162:165], v142
	ds_read_b128 v[166:169], v142 offset:1024
	ds_read_b128 v[170:173], v142 offset:2048
	ds_read_b128 v[174:177], v142 offset:3072
	ds_read_b128 v[178:181], v142 offset:4096
	ds_read_b128 v[182:185], v142 offset:5120
	ds_read_b128 v[186:189], v142 offset:6144
	ds_read_b128 v[190:193], v142 offset:7168
	s_nop 0
	v_mov_b32_e32 v128, v139
	s_nop 0
	s_waitcnt lgkmcnt(8)
	s_barrier
	s_waitcnt lgkmcnt(0)
	s_setprio 1
	s_waitcnt lgkmcnt(0)
	v_mfma_scale_f32_16x16x128_f8f6f4 v[124:127], v[146:153], v[162:169], v[124:127], v143, v143 op_sel_hi:[0,0,0]
	s_add_i32 m0, s19, 0xc000
	v_mfma_scale_f32_16x16x128_f8f6f4 v[120:123], v[154:161], v[162:169], v[120:123], v143, v143 op_sel_hi:[0,0,0]
	global_load_lds_dwordx4 v138, s[20:21]
	v_mfma_scale_f32_16x16x128_f8f6f4 v[116:119], v[146:153], v[170:177], v[116:119], v143, v143 op_sel_hi:[0,0,0]
	s_add_i32 m0, s19, 0xe000
	v_mfma_scale_f32_16x16x128_f8f6f4 v[112:115], v[154:161], v[170:177], v[112:115], v143, v143 op_sel_hi:[0,0,0]
	global_load_lds_dwordx4 v139, s[20:21]
	v_mfma_scale_f32_16x16x128_f8f6f4 v[132:135], v[146:153], v[178:185], v[108:111], v143, v143 op_sel_hi:[0,0,0]
	v_mfma_scale_f32_16x16x128_f8f6f4 v[194:197], v[154:161], v[178:185], v[104:107], v143, v143 op_sel_hi:[0,0,0]
	v_mfma_scale_f32_16x16x128_f8f6f4 v[198:201], v[146:153], v[186:193], v[100:103], v143, v143 op_sel_hi:[0,0,0]
	v_mfma_scale_f32_16x16x128_f8f6f4 v[202:205], v[154:161], v[186:193], v[96:99], v143, v143 op_sel_hi:[0,0,0]
	s_setprio 0
	s_barrier
	v_mov_b32_e32 v128, v138
	s_add_i32 s51, s44, s28
	s_nop 2
	ds_read_b128 v[96:99], v144
	ds_read_b128 v[100:103], v144 offset:1024
	ds_read_b128 v[104:107], v144 offset:2048
	ds_read_b128 v[108:111], v144 offset:3072
	s_nop 0
	v_mov_b32_e32 v128, v139
	s_nop 0
	s_barrier
	s_waitcnt lgkmcnt(0)
	s_setprio 1
	s_waitcnt lgkmcnt(0)
	v_mfma_scale_f32_16x16x128_f8f6f4 v[206:209], v[96:103], v[162:169], v[60:63], v143, v143 op_sel_hi:[0,0,0]
	s_mov_b32 m0, s51
	v_mfma_scale_f32_16x16x128_f8f6f4 v[162:165], v[104:111], v[162:169], v[56:59], v143, v143 op_sel_hi:[0,0,0]
	global_load_lds_dwordx4 v138, s[22:23]
	v_mfma_scale_f32_16x16x128_f8f6f4 v[166:169], v[96:103], v[170:177], v[52:55], v143, v143 op_sel_hi:[0,0,0]
	s_add_i32 m0, s51, 0x2000
	v_mfma_scale_f32_16x16x128_f8f6f4 v[170:173], v[104:111], v[170:177], v[48:51], v143, v143 op_sel_hi:[0,0,0]
	global_load_lds_dwordx4 v139, s[22:23]
	v_mfma_scale_f32_16x16x128_f8f6f4 v[174:177], v[96:103], v[178:185], v[44:47], v143, v143 op_sel_hi:[0,0,0]
	v_mfma_scale_f32_16x16x128_f8f6f4 v[178:181], v[104:111], v[178:185], v[40:43], v143, v143 op_sel_hi:[0,0,0]
	v_mfma_scale_f32_16x16x128_f8f6f4 v[182:185], v[96:103], v[186:193], v[36:39], v143, v143 op_sel_hi:[0,0,0]
	v_mfma_scale_f32_16x16x128_f8f6f4 v[186:189], v[104:111], v[186:193], v[32:35], v143, v143 op_sel_hi:[0,0,0]
	s_setprio 0
	v_mov_b32_e32 v128, v138
	s_barrier
	s_nop 2
	ds_read_b128 v[32:35], v142 offset:16384
	ds_read_b128 v[36:39], v142 offset:17408
	ds_read_b128 v[40:43], v142 offset:18432
	ds_read_b128 v[44:47], v142 offset:19456
	ds_read_b128 v[48:51], v142 offset:20480
	ds_read_b128 v[52:55], v142 offset:21504
	ds_read_b128 v[56:59], v142 offset:22528
	ds_read_b128 v[60:63], v142 offset:23552
	s_nop 0
	v_mov_b32_e32 v128, v139
	s_nop 0
	s_barrier
	s_waitcnt lgkmcnt(0)
	s_setprio 1
	s_waitcnt lgkmcnt(0)
	v_mfma_scale_f32_16x16x128_f8f6f4 v[92:95], v[146:153], v[32:39], v[92:95], v143, v143 op_sel_hi:[0,0,0]
	s_mov_b32 m0, s19
	v_mfma_scale_f32_16x16x128_f8f6f4 v[88:91], v[154:161], v[32:39], v[88:91], v143, v143 op_sel_hi:[0,0,0]
	global_load_lds_dwordx4 v138, s[24:25]
	v_mfma_scale_f32_16x16x128_f8f6f4 v[84:87], v[146:153], v[40:47], v[84:87], v143, v143 op_sel_hi:[0,0,0]
	s_mov_b32 m0, s29
	v_mfma_scale_f32_16x16x128_f8f6f4 v[80:83], v[154:161], v[40:47], v[80:83], v143, v143 op_sel_hi:[0,0,0]
	global_load_lds_dwordx4 v139, s[24:25]
	v_mfma_scale_f32_16x16x128_f8f6f4 v[76:79], v[146:153], v[48:55], v[76:79], v143, v143 op_sel_hi:[0,0,0]
	v_mfma_scale_f32_16x16x128_f8f6f4 v[72:75], v[154:161], v[48:55], v[72:75], v143, v143 op_sel_hi:[0,0,0]
	v_mfma_scale_f32_16x16x128_f8f6f4 v[190:193], v[146:153], v[56:63], v[68:71], v143, v143 op_sel_hi:[0,0,0]
	v_mfma_scale_f32_16x16x128_f8f6f4 v[210:213], v[154:161], v[56:63], v[64:67], v143, v143 op_sel_hi:[0,0,0]
	s_setprio 0
	s_barrier
	s_add_u32 s52, s22, 0x40000
	s_addc_u32 s53, s23, 0
	s_nop 2
	v_mov_b32_e32 v64, v138
	s_add_i32 s51, s45, s28
	s_mov_b32 s100, s51
	s_nop 0
	v_mov_b32_e32 v64, v139
	s_add_i32 s101, s51, 0x2000
	s_nop 0
	s_waitcnt vmcnt(4)
	s_barrier
	s_setprio 1
	v_mfma_scale_f32_16x16x128_f8f6f4 v[214:217], v[96:103], v[32:39], v[28:31], v143, v143 op_sel_hi:[0,0,0]
	s_mov_b32 m0, s100
	v_mfma_scale_f32_16x16x128_f8f6f4 v[218:221], v[104:111], v[32:39], v[24:27], v143, v143 op_sel_hi:[0,0,0]
	global_load_lds_dwordx4 v138, s[52:53]
	v_mfma_scale_f32_16x16x128_f8f6f4 v[222:225], v[96:103], v[40:47], v[20:23], v143, v143 op_sel_hi:[0,0,0]
	s_mov_b32 m0, s101
	v_mfma_scale_f32_16x16x128_f8f6f4 v[226:229], v[104:111], v[40:47], v[16:19], v143, v143 op_sel_hi:[0,0,0]
	global_load_lds_dwordx4 v139, s[52:53]
	v_mfma_scale_f32_16x16x128_f8f6f4 v[230:233], v[96:103], v[48:55], v[12:15], v143, v143 op_sel_hi:[0,0,0]
	v_mfma_scale_f32_16x16x128_f8f6f4 v[234:237], v[104:111], v[48:55], v[8:11], v143, v143 op_sel_hi:[0,0,0]
	v_mfma_scale_f32_16x16x128_f8f6f4 v[238:241], v[96:103], v[56:63], v[4:7], v143, v143 op_sel_hi:[0,0,0]
	v_mfma_scale_f32_16x16x128_f8f6f4 v[242:245], v[104:111], v[56:63], v[0:3], v143, v143 op_sel_hi:[0,0,0]
	s_setprio 0
	s_add_i32 s51, 0, 0x18000
	s_nop 1
	v_add_u32_e32 v12, s51, v140
	s_barrier
	s_nop 0
	ds_read_b128 v[0:3], v12
	ds_read_b128 v[4:7], v12 offset:1024
	ds_read_b128 v[8:11], v12 offset:2048
	ds_read_b128 v[12:15], v12 offset:3072
	s_add_u32 s52, s24, 0x40000
	v_mov_b32_e32 v40, v138
	ds_read_b128 v[16:19], v142 offset:32768
	ds_read_b128 v[20:23], v142 offset:33792
	ds_read_b128 v[24:27], v142 offset:34816
	ds_read_b128 v[28:31], v142 offset:35840
	ds_read_b128 v[32:35], v142 offset:36864
	ds_read_b128 v[36:39], v142 offset:37888
	ds_read_b128 v[64:67], v142 offset:38912
	ds_read_b128 v[68:71], v142 offset:39936
	s_addc_u32 s53, s25, 0
	s_nop 0
	v_mov_b32_e32 v40, v139
	s_nop 0
	s_waitcnt lgkmcnt(8)
	s_barrier
	s_waitcnt lgkmcnt(0)
	s_setprio 1
	s_waitcnt lgkmcnt(0)
	v_mfma_scale_f32_16x16x128_f8f6f4 v[124:127], v[0:7], v[16:23], v[124:127], v143, v143 op_sel_hi:[0,0,0]
	s_mov_b32 m0, s30
	v_mfma_scale_f32_16x16x128_f8f6f4 v[120:123], v[8:15], v[16:23], v[120:123], v143, v143 op_sel_hi:[0,0,0]
	global_load_lds_dwordx4 v138, s[52:53]
	v_mfma_scale_f32_16x16x128_f8f6f4 v[116:119], v[0:7], v[24:31], v[116:119], v143, v143 op_sel_hi:[0,0,0]
	s_mov_b32 m0, s31
	v_mfma_scale_f32_16x16x128_f8f6f4 v[112:115], v[8:15], v[24:31], v[112:115], v143, v143 op_sel_hi:[0,0,0]
	global_load_lds_dwordx4 v139, s[52:53]
	v_mfma_scale_f32_16x16x128_f8f6f4 v[108:111], v[0:7], v[32:39], v[132:135], v143, v143 op_sel_hi:[0,0,0]
	v_mfma_scale_f32_16x16x128_f8f6f4 v[104:107], v[8:15], v[32:39], v[194:197], v143, v143 op_sel_hi:[0,0,0]
	v_mfma_scale_f32_16x16x128_f8f6f4 v[100:103], v[0:7], v[64:71], v[198:201], v143, v143 op_sel_hi:[0,0,0]
	v_mfma_scale_f32_16x16x128_f8f6f4 v[96:99], v[8:15], v[64:71], v[202:205], v143, v143 op_sel_hi:[0,0,0]
	s_setprio 0
	s_barrier
	s_add_i32 s52, 0, 0x1c000
	v_add_u32_e32 v40, s52, v140
	v_mov_b32_e32 v128, v138
	ds_read_b128 v[146:149], v40
	ds_read_b128 v[150:153], v40 offset:1024
	ds_read_b128 v[154:157], v40 offset:2048
	ds_read_b128 v[158:161], v40 offset:3072
	s_add_i32 s51, s51, s28
	v_lshl_add_u64 v[40:41], s[22:23], 0, v[128:129]
	v_lshl_add_u64 v[40:41], v[40:41], 0, s[6:7]
	v_mov_b32_e32 v128, v139
	v_lshl_add_u64 v[40:41], s[22:23], 0, v[128:129]
	v_lshl_add_u64 v[40:41], v[40:41], 0, s[6:7]
	s_barrier
	s_waitcnt lgkmcnt(0)
	s_setprio 1
	s_waitcnt lgkmcnt(0)
	v_mfma_scale_f32_16x16x128_f8f6f4 v[60:63], v[146:153], v[16:23], v[206:209], v143, v143 op_sel_hi:[0,0,0]
	s_add_u32 s98, s22, s6
	s_addc_u32 s99, s23, s7
	s_mov_b32 m0, s51
	v_mfma_scale_f32_16x16x128_f8f6f4 v[56:59], v[154:161], v[16:23], v[162:165], v143, v143 op_sel_hi:[0,0,0]
	global_load_lds_dwordx4 v138, s[98:99]
	v_mfma_scale_f32_16x16x128_f8f6f4 v[52:55], v[146:153], v[24:31], v[166:169], v143, v143 op_sel_hi:[0,0,0]
	s_add_i32 m0, s51, 0x2000
	v_mfma_scale_f32_16x16x128_f8f6f4 v[48:51], v[154:161], v[24:31], v[170:173], v143, v143 op_sel_hi:[0,0,0]
	global_load_lds_dwordx4 v139, s[98:99]
	v_mfma_scale_f32_16x16x128_f8f6f4 v[44:47], v[146:153], v[32:39], v[174:177], v143, v143 op_sel_hi:[0,0,0]
	v_mfma_scale_f32_16x16x128_f8f6f4 v[40:43], v[154:161], v[32:39], v[178:181], v143, v143 op_sel_hi:[0,0,0]
	v_mfma_scale_f32_16x16x128_f8f6f4 v[36:39], v[146:153], v[64:71], v[182:185], v143, v143 op_sel_hi:[0,0,0]
	v_mfma_scale_f32_16x16x128_f8f6f4 v[32:35], v[154:161], v[64:71], v[186:189], v143, v143 op_sel_hi:[0,0,0]
	s_setprio 0
	v_mov_b32_e32 v128, v138
	s_barrier
	ds_read_b128 v[16:19], v142 offset:49152
	ds_read_b128 v[20:23], v142 offset:50176
	ds_read_b128 v[162:165], v142 offset:51200
	ds_read_b128 v[166:169], v142 offset:52224
	ds_read_b128 v[170:173], v142 offset:53248
	ds_read_b128 v[174:177], v142 offset:54272
	ds_read_b128 v[178:181], v142 offset:55296
	ds_read_b128 v[182:185], v142 offset:56320
	v_lshl_add_u64 v[24:25], s[24:25], 0, v[128:129]
	v_lshl_add_u64 v[24:25], v[24:25], 0, s[6:7]
	v_mov_b32_e32 v128, v139
	v_lshl_add_u64 v[24:25], s[24:25], 0, v[128:129]
	v_lshl_add_u64 v[24:25], v[24:25], 0, s[6:7]
	s_barrier
	s_waitcnt lgkmcnt(0)
	s_setprio 1
	s_waitcnt lgkmcnt(0)
	v_mfma_scale_f32_16x16x128_f8f6f4 v[92:95], v[0:7], v[16:23], v[92:95], v143, v143 op_sel_hi:[0,0,0]
	s_add_u32 s98, s24, s6
	s_addc_u32 s99, s25, s7
	s_mov_b32 m0, s41
	v_mfma_scale_f32_16x16x128_f8f6f4 v[88:91], v[8:15], v[16:23], v[88:91], v143, v143 op_sel_hi:[0,0,0]
	global_load_lds_dwordx4 v138, s[98:99]
	v_mfma_scale_f32_16x16x128_f8f6f4 v[84:87], v[0:7], v[162:169], v[84:87], v143, v143 op_sel_hi:[0,0,0]
	s_mov_b32 m0, s42
	v_mfma_scale_f32_16x16x128_f8f6f4 v[80:83], v[8:15], v[162:169], v[80:83], v143, v143 op_sel_hi:[0,0,0]
	global_load_lds_dwordx4 v139, s[98:99]
	v_mfma_scale_f32_16x16x128_f8f6f4 v[76:79], v[0:7], v[170:177], v[76:79], v143, v143 op_sel_hi:[0,0,0]
	v_mfma_scale_f32_16x16x128_f8f6f4 v[72:75], v[8:15], v[170:177], v[72:75], v143, v143 op_sel_hi:[0,0,0]
	v_mfma_scale_f32_16x16x128_f8f6f4 v[68:71], v[0:7], v[178:185], v[190:193], v143, v143 op_sel_hi:[0,0,0]
	v_mfma_scale_f32_16x16x128_f8f6f4 v[64:67], v[8:15], v[178:185], v[210:213], v143, v143 op_sel_hi:[0,0,0]
	s_setprio 0
	s_barrier
	s_add_u32 s22, s22, 0x40080
	s_addc_u32 s23, s23, 0
	v_mov_b32_e32 v0, v138
	s_add_i32 s24, s52, s28
	s_nop 0
	v_mov_b32_e32 v0, v139
	s_nop 0
	s_waitcnt vmcnt(4)
	s_barrier
	s_setprio 1
	v_mfma_scale_f32_16x16x128_f8f6f4 v[28:31], v[146:153], v[16:23], v[214:217], v143, v143 op_sel_hi:[0,0,0]
	s_mov_b32 m0, s24
	v_mfma_scale_f32_16x16x128_f8f6f4 v[24:27], v[154:161], v[16:23], v[218:221], v143, v143 op_sel_hi:[0,0,0]
	global_load_lds_dwordx4 v138, s[22:23]
	v_mfma_scale_f32_16x16x128_f8f6f4 v[20:23], v[146:153], v[162:169], v[222:225], v143, v143 op_sel_hi:[0,0,0]
	s_add_i32 m0, s24, 0x2000
	v_mfma_scale_f32_16x16x128_f8f6f4 v[16:19], v[154:161], v[162:169], v[226:229], v143, v143 op_sel_hi:[0,0,0]
	global_load_lds_dwordx4 v139, s[22:23]
	v_mfma_scale_f32_16x16x128_f8f6f4 v[12:15], v[146:153], v[170:177], v[230:233], v143, v143 op_sel_hi:[0,0,0]
	v_mfma_scale_f32_16x16x128_f8f6f4 v[8:11], v[154:161], v[170:177], v[234:237], v143, v143 op_sel_hi:[0,0,0]
	v_mfma_scale_f32_16x16x128_f8f6f4 v[4:7], v[146:153], v[178:185], v[238:241], v143, v143 op_sel_hi:[0,0,0]
	v_mfma_scale_f32_16x16x128_f8f6f4 v[0:3], v[154:161], v[178:185], v[242:245], v143, v143 op_sel_hi:[0,0,0]
	s_setprio 0
	s_add_i32 s50, s50, 2
	s_add_u32 s20, s20, 0x100
	s_addc_u32 s21, s21, 0
	s_add_u32 s11, s11, 0x100
	s_addc_u32 s13, s13, 0
	s_cmp_gt_u32 s50, 13
	s_barrier
	s_cbranch_scc0 .LBB0_4932
	s_ashr_i32 s11, s18, 4
	s_mul_hi_i32 s13, s11, 0xc000
	s_mul_i32 s11, s11, 0xc000
	s_add_u32 s11, s37, s11
	s_addc_u32 s13, s38, s13
	s_lshl_b32 s20, s49, 8
	s_ashr_i32 s21, s20, 31
	s_lshl_b64 s[22:23], s[20:21], 2
	s_add_u32 s11, s11, s22
	v_mbcnt_lo_u32_b32 v134, -1, 0
	v_mbcnt_hi_u32_b32 v134, -1, v134
	s_addc_u32 s13, s13, s23
	v_ashrrev_i32_e32 v135, 4, v134
	s_add_u32 s22, s11, s46
	v_lshlrev_b32_e32 v132, 2, v135
	s_addc_u32 s23, s13, 0
	v_ashrrev_i32_e32 v133, 31, v132
	v_lshl_add_u64 v[132:133], v[132:133], 2, s[22:23]
	global_load_dwordx4 v[146:149], v[132:133], off
	global_load_dwordx4 v[150:153], v[132:133], off offset:64
	v_mov_b32_e32 v164, v129
	s_lshl_b32 s11, s18, 8
	v_mov_b32_e32 v165, v129
	s_add_i32 s22, s11, s39
	s_ashr_i32 s23, s22, 31
	s_lshl_b64 s[22:23], s[22:23], 11
	s_add_u32 s11, s35, s22
	s_addc_u32 s13, s36, s23
	v_mov_b32_e32 v162, v129
	v_lshlrev_b32_e32 v135, 3, v135
	s_add_u32 s11, s11, s20
	v_mov_b32_e32 v154, v129
	v_mov_b32_e32 v155, v129
	v_mov_b32_e32 v156, v129
	v_mov_b32_e32 v157, v129
	v_and_b32_e32 v128, 16, v134
	v_bfi_b32 v134, -16, v135, v134
	s_addc_u32 s13, s13, s21
	v_mov_b32_e32 v163, v129
	v_mov_b32_e32 v158, v129
	v_mov_b32_e32 v159, v129
	v_mov_b32_e32 v160, v129
	v_mov_b32_e32 v161, v129
	v_ashrrev_i32_e32 v135, 31, v134
	s_add_u32 s20, s11, s40
	v_lshlrev_b64 v[134:135], 11, v[134:135]
	s_addc_u32 s21, s13, 0
	v_lshl_add_u64 v[134:135], s[20:21], 0, v[134:135]
	v_lshl_add_u64 v[134:135], v[134:135], 0, v[128:129]
	v_add_co_u32_e32 v136, vcc, s34, v134
	s_mov_b32 s18, s12
	s_nop 0
	v_addc_co_u32_e32 v137, vcc, 0, v135, vcc
	s_mov_b32 s49, s10
	s_mov_b64 s[22:23], s[16:17]
	s_mov_b64 s[20:21], s[14:15]
	s_waitcnt vmcnt(0)
	v_pk_mul_f32 v[146:147], v[146:147], s[8:9] op_sel_hi:[1,0]
	v_pk_mul_f32 v[150:151], v[150:151], s[8:9] op_sel_hi:[1,0]
	v_pk_mul_f32 v[84:85], v[84:85], v[146:147]
	v_pk_mul_f32 v[80:81], v[80:81], v[150:151]
	v_cvt_pk_fp8_f32 v164, v84, v85
	v_cvt_pk_fp8_f32 v165, v80, v81
	v_pk_mul_f32 v[148:149], v[148:149], s[8:9] op_sel_hi:[1,0]
	v_pk_mul_f32 v[152:153], v[152:153], s[8:9] op_sel_hi:[1,0]
	v_pk_mul_f32 v[80:81], v[86:87], v[148:149]
	v_pk_mul_f32 v[72:73], v[72:73], v[150:151]
	v_cvt_pk_fp8_f32 v164, v80, v81 op_sel:[0,0,1]
	v_pk_mul_f32 v[80:81], v[82:83], v[152:153]
	v_pk_mul_f32 v[92:93], v[92:93], v[146:147]
	v_cvt_pk_fp8_f32 v165, v80, v81 op_sel:[0,0,1]
	v_pk_mul_f32 v[80:81], v[76:77], v[146:147]
	v_mov_b32_e32 v77, v129
	v_mov_b32_e32 v76, v129
	v_cvt_pk_fp8_f32 v77, v72, v73
	v_pk_mul_f32 v[72:73], v[78:79], v[148:149]
	v_pk_mul_f32 v[68:69], v[68:69], v[146:147]
	v_mov_b32_e32 v78, v129
	v_pk_mul_f32 v[124:125], v[124:125], v[146:147]
	v_pk_mul_f32 v[120:121], v[120:121], v[150:151]
	v_pk_mul_f32 v[116:117], v[116:117], v[146:147]
	v_pk_mul_f32 v[112:113], v[112:113], v[150:151]
	v_cvt_pk_fp8_f32 v162, v92, v93
	v_pk_mul_f32 v[88:89], v[88:89], v[150:151]
	v_cvt_pk_fp8_f32 v76, v80, v81
	v_cvt_pk_fp8_f32 v78, v68, v69
	v_pk_mul_f32 v[64:65], v[64:65], v[150:151]
	v_mov_b32_e32 v79, v129
	v_pk_mul_f32 v[108:109], v[108:109], v[146:147]
	v_pk_mul_f32 v[104:105], v[104:105], v[150:151]
	v_pk_mul_f32 v[100:101], v[100:101], v[146:147]
	v_pk_mul_f32 v[96:97], v[96:97], v[150:151]
	v_cvt_pk_fp8_f32 v154, v124, v125
	v_cvt_pk_fp8_f32 v155, v120, v121
	v_cvt_pk_fp8_f32 v156, v116, v117
	v_cvt_pk_fp8_f32 v157, v112, v113
	v_cvt_pk_fp8_f32 v163, v88, v89
	v_cvt_pk_fp8_f32 v79, v64, v65
	v_cvt_pk_fp8_f32 v158, v108, v109
	v_cvt_pk_fp8_f32 v159, v104, v105
	v_cvt_pk_fp8_f32 v160, v100, v101
	v_cvt_pk_fp8_f32 v161, v96, v97
	v_pk_mul_f32 v[88:89], v[94:95], v[148:149]
	v_pk_mul_f32 v[64:65], v[70:71], v[148:149]
	v_pk_mul_f32 v[126:127], v[126:127], v[148:149]
	v_pk_mul_f32 v[122:123], v[122:123], v[152:153]
	v_pk_mul_f32 v[118:119], v[118:119], v[148:149]
	v_pk_mul_f32 v[114:115], v[114:115], v[152:153]
	v_cvt_pk_fp8_f32 v162, v88, v89 op_sel:[0,0,1]
	v_pk_mul_f32 v[88:89], v[90:91], v[152:153]
	v_cvt_pk_fp8_f32 v76, v72, v73 op_sel:[0,0,1]
	v_pk_mul_f32 v[72:73], v[74:75], v[152:153]
	v_cvt_pk_fp8_f32 v78, v64, v65 op_sel:[0,0,1]
	v_pk_mul_f32 v[64:65], v[66:67], v[152:153]
	v_pk_mul_f32 v[110:111], v[110:111], v[148:149]
	v_pk_mul_f32 v[106:107], v[106:107], v[152:153]
	v_pk_mul_f32 v[102:103], v[102:103], v[148:149]
	v_pk_mul_f32 v[98:99], v[98:99], v[152:153]
	v_cvt_pk_fp8_f32 v154, v126, v127 op_sel:[0,0,1]
	v_cvt_pk_fp8_f32 v155, v122, v123 op_sel:[0,0,1]
	v_cvt_pk_fp8_f32 v156, v118, v119 op_sel:[0,0,1]
	v_cvt_pk_fp8_f32 v157, v114, v115 op_sel:[0,0,1]
	v_cvt_pk_fp8_f32 v163, v88, v89 op_sel:[0,0,1]
	v_cvt_pk_fp8_f32 v77, v72, v73 op_sel:[0,0,1]
	v_cvt_pk_fp8_f32 v79, v64, v65 op_sel:[0,0,1]
	v_cvt_pk_fp8_f32 v158, v110, v111 op_sel:[0,0,1]
	v_cvt_pk_fp8_f32 v159, v106, v107 op_sel:[0,0,1]
	v_cvt_pk_fp8_f32 v160, v102, v103 op_sel:[0,0,1]
	v_cvt_pk_fp8_f32 v161, v98, v99 op_sel:[0,0,1]
	v_add_co_u32_e32 v80, vcc, s47, v134
	v_permlane32_swap_b32_e32 v154, v156
	s_nop 0
	v_addc_co_u32_e32 v81, vcc, 0, v135, vcc
	v_permlane32_swap_b32_e32 v155, v157
	v_permlane32_swap_b32_e32 v162, v164
	v_permlane32_swap_b32_e32 v163, v165
	v_permlane32_swap_b32_e32 v76, v78
	v_permlane32_swap_b32_e32 v77, v79
	v_add_co_u32_e32 v82, vcc, s48, v134
	v_permlane32_swap_b32_e32 v158, v160
	v_permlane32_swap_b32_e32 v159, v161
	v_permlane16_swap_b32_e32 v154, v155
	v_permlane16_swap_b32_e32 v156, v157
	v_permlane16_swap_b32_e32 v162, v163
	v_permlane16_swap_b32_e32 v164, v165
	v_permlane16_swap_b32_e32 v76, v77
	v_permlane16_swap_b32_e32 v78, v79
	v_addc_co_u32_e32 v83, vcc, 0, v135, vcc
	v_permlane16_swap_b32_e32 v158, v159
	v_permlane16_swap_b32_e32 v160, v161
	global_store_dwordx4 v[134:135], v[154:157], off
	global_store_dwordx4 v[136:137], v[158:161], off
	global_store_dwordx4 v[80:81], v[162:165], off
	global_store_dwordx4 v[82:83], v[76:79], off
	global_load_dwordx4 v[64:67], v[132:133], off offset:512
	global_load_dwordx4 v[68:71], v[132:133], off offset:576
	v_mov_b32_e32 v75, v129
	v_mov_b32_e32 v72, v129
	v_mov_b32_e32 v73, v129
	v_mov_b32_e32 v74, v129
	s_and_b64 vcc, exec, s[4:5]
	s_waitcnt vmcnt(0)
	v_pk_mul_f32 v[64:65], v[64:65], s[8:9] op_sel_hi:[1,0]
	v_pk_mul_f32 v[68:69], v[68:69], s[8:9] op_sel_hi:[1,0]
	v_pk_mul_f32 v[70:71], v[70:71], s[8:9] op_sel_hi:[1,0]
	v_pk_mul_f32 v[48:49], v[48:49], v[68:69]
	v_pk_mul_f32 v[66:67], v[66:67], s[8:9] op_sel_hi:[1,0]
	v_cvt_pk_fp8_f32 v75, v48, v49
	v_pk_mul_f32 v[48:49], v[50:51], v[70:71]
	v_pk_mul_f32 v[40:41], v[40:41], v[68:69]
	v_pk_mul_f32 v[36:37], v[36:37], v[64:65]
	v_cvt_pk_fp8_f32 v75, v48, v49 op_sel:[0,0,1]
	v_pk_mul_f32 v[48:49], v[44:45], v[64:65]
	v_mov_b32_e32 v45, v129
	v_cvt_pk_fp8_f32 v45, v40, v41
	v_pk_mul_f32 v[40:41], v[46:47], v[66:67]
	v_mov_b32_e32 v46, v129
	v_cvt_pk_fp8_f32 v46, v36, v37
	v_pk_mul_f32 v[32:33], v[32:33], v[68:69]
	v_mov_b32_e32 v47, v129
	v_cvt_pk_fp8_f32 v47, v32, v33
	v_pk_mul_f32 v[32:33], v[38:39], v[66:67]
	v_pk_mul_f32 v[24:25], v[24:25], v[68:69]
	v_cvt_pk_fp8_f32 v46, v32, v33 op_sel:[0,0,1]
	v_pk_mul_f32 v[32:33], v[34:35], v[70:71]
	v_pk_mul_f32 v[20:21], v[20:21], v[64:65]
	v_cvt_pk_fp8_f32 v47, v32, v33 op_sel:[0,0,1]
	v_pk_mul_f32 v[32:33], v[28:29], v[64:65]
	v_mov_b32_e32 v29, v129
	v_cvt_pk_fp8_f32 v29, v24, v25
	v_pk_mul_f32 v[24:25], v[30:31], v[66:67]
	v_mov_b32_e32 v30, v129
	v_cvt_pk_fp8_f32 v30, v20, v21
	v_pk_mul_f32 v[16:17], v[16:17], v[68:69]
	v_mov_b32_e32 v31, v129
	v_cvt_pk_fp8_f32 v31, v16, v17
	v_pk_mul_f32 v[16:17], v[22:23], v[66:67]
	v_mov_b32_e32 v28, v129
	v_cvt_pk_fp8_f32 v30, v16, v17 op_sel:[0,0,1]
	v_pk_mul_f32 v[16:17], v[18:19], v[70:71]
	v_pk_mul_f32 v[8:9], v[8:9], v[68:69]
	v_cvt_pk_fp8_f32 v31, v16, v17 op_sel:[0,0,1]
	v_pk_mul_f32 v[16:17], v[12:13], v[64:65]
	v_mov_b32_e32 v13, v129
	v_pk_mul_f32 v[60:61], v[60:61], v[64:65]
	v_pk_mul_f32 v[56:57], v[56:57], v[68:69]
	v_pk_mul_f32 v[52:53], v[52:53], v[64:65]
	v_mov_b32_e32 v44, v129
	v_cvt_pk_fp8_f32 v28, v32, v33
	v_mov_b32_e32 v12, v129
	v_cvt_pk_fp8_f32 v13, v8, v9
	v_pk_mul_f32 v[8:9], v[14:15], v[66:67]
	v_pk_mul_f32 v[4:5], v[4:5], v[64:65]
	v_mov_b32_e32 v14, v129
	v_cvt_pk_fp8_f32 v72, v60, v61
	v_cvt_pk_fp8_f32 v73, v56, v57
	v_cvt_pk_fp8_f32 v74, v52, v53
	v_cvt_pk_fp8_f32 v44, v48, v49
	v_cvt_pk_fp8_f32 v12, v16, v17
	v_cvt_pk_fp8_f32 v14, v4, v5
	v_pk_mul_f32 v[0:1], v[0:1], v[68:69]
	v_mov_b32_e32 v15, v129
	v_cvt_pk_fp8_f32 v15, v0, v1
	v_pk_mul_f32 v[62:63], v[62:63], v[66:67]
	v_pk_mul_f32 v[58:59], v[58:59], v[70:71]
	v_pk_mul_f32 v[54:55], v[54:55], v[66:67]
	v_cvt_pk_fp8_f32 v28, v24, v25 op_sel:[0,0,1]
	v_pk_mul_f32 v[24:25], v[26:27], v[70:71]
	v_pk_mul_f32 v[0:1], v[6:7], v[66:67]
	v_cvt_pk_fp8_f32 v72, v62, v63 op_sel:[0,0,1]
	v_cvt_pk_fp8_f32 v73, v58, v59 op_sel:[0,0,1]
	v_cvt_pk_fp8_f32 v74, v54, v55 op_sel:[0,0,1]
	v_cvt_pk_fp8_f32 v44, v40, v41 op_sel:[0,0,1]
	v_pk_mul_f32 v[40:41], v[42:43], v[70:71]
	v_cvt_pk_fp8_f32 v29, v24, v25 op_sel:[0,0,1]
	v_cvt_pk_fp8_f32 v12, v8, v9 op_sel:[0,0,1]
	v_pk_mul_f32 v[8:9], v[10:11], v[70:71]
	v_cvt_pk_fp8_f32 v14, v0, v1 op_sel:[0,0,1]
	v_pk_mul_f32 v[0:1], v[2:3], v[70:71]
	v_cvt_pk_fp8_f32 v45, v40, v41 op_sel:[0,0,1]
	v_cvt_pk_fp8_f32 v13, v8, v9 op_sel:[0,0,1]
	v_cvt_pk_fp8_f32 v15, v0, v1 op_sel:[0,0,1]
	v_permlane32_swap_b32_e32 v72, v74
	v_permlane32_swap_b32_e32 v73, v75
	v_permlane32_swap_b32_e32 v28, v30
	v_permlane32_swap_b32_e32 v29, v31
	v_permlane16_swap_b32_e32 v72, v73
	v_permlane16_swap_b32_e32 v74, v75
	v_permlane32_swap_b32_e32 v44, v46
	v_permlane32_swap_b32_e32 v45, v47
	v_permlane16_swap_b32_e32 v28, v29
	v_permlane16_swap_b32_e32 v30, v31
	v_permlane32_swap_b32_e32 v12, v14
	v_permlane32_swap_b32_e32 v13, v15
	v_permlane16_swap_b32_e32 v44, v45
	v_permlane16_swap_b32_e32 v46, v47
	global_store_dwordx4 v[134:135], v[72:75], off offset:128
	global_store_dwordx4 v[136:137], v[44:47], off offset:128
	v_permlane16_swap_b32_e32 v12, v13
	v_permlane16_swap_b32_e32 v14, v15
	global_store_dwordx4 v[80:81], v[28:31], off offset:128
	global_store_dwordx4 v[82:83], v[12:15], off offset:128
	s_cbranch_vccz .LBB0_4925
	s_waitcnt vmcnt(0)
	v_readlane_b32 s0, v252, 2
	s_cmpk_gt_u32 s0, 0xff
	s_cbranch_scc1 .LBB0_4936
	s_barrier

.LBB0_5813:
	ds_read_b128 v[140:143], v134
	ds_read_b128 v[144:147], v134 offset:1024
	ds_read_b128 v[148:151], v134 offset:2048
	ds_read_b128 v[152:155], v134 offset:3072
	s_add_u32 s16, s14, 0xfffd0080
	s_addc_u32 s17, s15, -1
	s_cmp_eq_u32 s53, 8
	s_cselect_b32 s19, s13, s17
	s_cselect_b32 s18, s12, s16
	s_cselect_b32 s17, s11, s52
	s_cselect_b32 s16, s10, s51
	v_mov_b32_e32 v128, v132
	ds_read_b128 v[156:159], v135
	ds_read_b128 v[160:163], v135 offset:1024
	ds_read_b128 v[164:167], v135 offset:2048
	ds_read_b128 v[168:171], v135 offset:3072
	ds_read_b128 v[172:175], v135 offset:4096
	ds_read_b128 v[176:179], v135 offset:5120
	ds_read_b128 v[180:183], v135 offset:6144
	ds_read_b128 v[184:187], v135 offset:7168
	s_nop 0
	v_mov_b32_e32 v128, v133
	s_nop 0
	s_waitcnt lgkmcnt(8)
	s_barrier
	s_waitcnt lgkmcnt(0)
	s_setprio 1
	s_waitcnt lgkmcnt(0)
	v_mfma_scale_f32_16x16x128_f8f6f4 v[124:127], v[140:147], v[156:163], v[124:127], v136, v136 op_sel_hi:[0,0,0]
	s_mov_b32 m0, s38
	v_mfma_scale_f32_16x16x128_f8f6f4 v[120:123], v[148:155], v[156:163], v[120:123], v136, v136 op_sel_hi:[0,0,0]
	global_load_lds_dwordx4 v132, s[14:15]
	v_mfma_scale_f32_16x16x128_f8f6f4 v[116:119], v[140:147], v[164:171], v[116:119], v136, v136 op_sel_hi:[0,0,0]
	s_mov_b32 m0, s39
	v_mfma_scale_f32_16x16x128_f8f6f4 v[112:115], v[148:155], v[164:171], v[112:115], v136, v136 op_sel_hi:[0,0,0]
	global_load_lds_dwordx4 v133, s[14:15]
	v_mfma_scale_f32_16x16x128_f8f6f4 v[188:191], v[140:147], v[172:179], v[108:111], v136, v136 op_sel_hi:[0,0,0]
	v_mfma_scale_f32_16x16x128_f8f6f4 v[192:195], v[148:155], v[172:179], v[104:107], v136, v136 op_sel_hi:[0,0,0]
	v_mfma_scale_f32_16x16x128_f8f6f4 v[196:199], v[140:147], v[180:187], v[100:103], v136, v136 op_sel_hi:[0,0,0]
	v_mfma_scale_f32_16x16x128_f8f6f4 v[200:203], v[148:155], v[180:187], v[96:99], v136, v136 op_sel_hi:[0,0,0]
	s_setprio 0
	s_barrier
	v_mov_b32_e32 v128, v132
	s_nop 2
	ds_read_b128 v[96:99], v137
	ds_read_b128 v[100:103], v137 offset:1024
	ds_read_b128 v[104:107], v137 offset:2048
	ds_read_b128 v[108:111], v137 offset:3072
	s_nop 0
	v_mov_b32_e32 v128, v133
	s_nop 0
	s_barrier
	s_waitcnt lgkmcnt(0)
	s_setprio 1
	s_waitcnt lgkmcnt(0)
	v_mfma_scale_f32_16x16x128_f8f6f4 v[204:207], v[96:103], v[156:163], v[92:95], v136, v136 op_sel_hi:[0,0,0]
	s_mov_b32 m0, s40
	v_mfma_scale_f32_16x16x128_f8f6f4 v[156:159], v[104:111], v[156:163], v[88:91], v136, v136 op_sel_hi:[0,0,0]
	global_load_lds_dwordx4 v132, s[16:17]
	v_mfma_scale_f32_16x16x128_f8f6f4 v[160:163], v[96:103], v[164:171], v[84:87], v136, v136 op_sel_hi:[0,0,0]
	s_mov_b32 m0, s41
	v_mfma_scale_f32_16x16x128_f8f6f4 v[164:167], v[104:111], v[164:171], v[80:83], v136, v136 op_sel_hi:[0,0,0]
	global_load_lds_dwordx4 v133, s[16:17]
	v_mfma_scale_f32_16x16x128_f8f6f4 v[168:171], v[96:103], v[172:179], v[76:79], v136, v136 op_sel_hi:[0,0,0]
	v_mfma_scale_f32_16x16x128_f8f6f4 v[172:175], v[104:111], v[172:179], v[72:75], v136, v136 op_sel_hi:[0,0,0]
	v_mfma_scale_f32_16x16x128_f8f6f4 v[176:179], v[96:103], v[180:187], v[68:71], v136, v136 op_sel_hi:[0,0,0]
	v_mfma_scale_f32_16x16x128_f8f6f4 v[180:183], v[104:111], v[180:187], v[64:67], v136, v136 op_sel_hi:[0,0,0]
	s_setprio 0
	v_mov_b32_e32 v128, v132
	s_barrier
	s_nop 2
	ds_read_b128 v[64:67], v135 offset:16384
	ds_read_b128 v[68:71], v135 offset:17408
	ds_read_b128 v[72:75], v135 offset:18432
	ds_read_b128 v[76:79], v135 offset:19456
	ds_read_b128 v[80:83], v135 offset:20480
	ds_read_b128 v[84:87], v135 offset:21504
	ds_read_b128 v[88:91], v135 offset:22528
	ds_read_b128 v[92:95], v135 offset:23552
	s_nop 0
	v_mov_b32_e32 v128, v133
	s_nop 0
	s_barrier
	s_waitcnt lgkmcnt(0)
	s_setprio 1
	s_waitcnt lgkmcnt(0)
	v_mfma_scale_f32_16x16x128_f8f6f4 v[60:63], v[140:147], v[64:71], v[60:63], v136, v136 op_sel_hi:[0,0,0]
	s_mov_b32 m0, s24
	v_mfma_scale_f32_16x16x128_f8f6f4 v[56:59], v[148:155], v[64:71], v[56:59], v136, v136 op_sel_hi:[0,0,0]
	global_load_lds_dwordx4 v132, s[18:19]
	v_mfma_scale_f32_16x16x128_f8f6f4 v[52:55], v[140:147], v[72:79], v[52:55], v136, v136 op_sel_hi:[0,0,0]
	s_mov_b32 m0, s25
	v_mfma_scale_f32_16x16x128_f8f6f4 v[48:51], v[148:155], v[72:79], v[48:51], v136, v136 op_sel_hi:[0,0,0]
	global_load_lds_dwordx4 v133, s[18:19]
	v_mfma_scale_f32_16x16x128_f8f6f4 v[184:187], v[140:147], v[80:87], v[44:47], v136, v136 op_sel_hi:[0,0,0]
	v_mfma_scale_f32_16x16x128_f8f6f4 v[208:211], v[148:155], v[80:87], v[40:43], v136, v136 op_sel_hi:[0,0,0]
	v_mfma_scale_f32_16x16x128_f8f6f4 v[212:215], v[140:147], v[88:95], v[36:39], v136, v136 op_sel_hi:[0,0,0]
	v_mfma_scale_f32_16x16x128_f8f6f4 v[216:219], v[148:155], v[88:95], v[32:35], v136, v136 op_sel_hi:[0,0,0]
	s_setprio 0
	s_barrier
	s_add_u32 s54, s16, 0x30000
	s_nop 3
	v_mov_b32_e32 v32, v132
	s_addc_u32 s55, s17, 0
	s_nop 0
	v_mov_b32_e32 v32, v133
	s_nop 0
	s_waitcnt vmcnt(4)
	s_barrier
	s_setprio 1
	v_mfma_scale_f32_16x16x128_f8f6f4 v[220:223], v[96:103], v[64:71], v[28:31], v136, v136 op_sel_hi:[0,0,0]
	s_mov_b32 m0, s42
	v_mfma_scale_f32_16x16x128_f8f6f4 v[224:227], v[104:111], v[64:71], v[24:27], v136, v136 op_sel_hi:[0,0,0]
	global_load_lds_dwordx4 v132, s[54:55]
	v_mfma_scale_f32_16x16x128_f8f6f4 v[228:231], v[96:103], v[72:79], v[20:23], v136, v136 op_sel_hi:[0,0,0]
	s_mov_b32 m0, s43
	v_mfma_scale_f32_16x16x128_f8f6f4 v[232:235], v[104:111], v[72:79], v[16:19], v136, v136 op_sel_hi:[0,0,0]
	global_load_lds_dwordx4 v133, s[54:55]
	v_mfma_scale_f32_16x16x128_f8f6f4 v[236:239], v[96:103], v[80:87], v[12:15], v136, v136 op_sel_hi:[0,0,0]
	v_mfma_scale_f32_16x16x128_f8f6f4 v[240:243], v[104:111], v[80:87], v[8:11], v136, v136 op_sel_hi:[0,0,0]
	v_mfma_scale_f32_16x16x128_f8f6f4 v[244:247], v[96:103], v[88:95], v[4:7], v136, v136 op_sel_hi:[0,0,0]
	v_mfma_scale_f32_16x16x128_f8f6f4 v[248:251], v[104:111], v[88:95], v[0:3], v136, v136 op_sel_hi:[0,0,0]
	s_setprio 0
	s_barrier
	s_nop 4
	ds_read_b128 v[0:3], v138
	ds_read_b128 v[4:7], v138 offset:1024
	ds_read_b128 v[8:11], v138 offset:2048
	ds_read_b128 v[12:15], v138 offset:3072
	s_add_u32 s54, s18, 0x30000
	v_mov_b32_e32 v64, v132
	ds_read_b128 v[16:19], v135 offset:32768
	ds_read_b128 v[20:23], v135 offset:33792
	ds_read_b128 v[24:27], v135 offset:34816
	ds_read_b128 v[28:31], v135 offset:35840
	ds_read_b128 v[32:35], v135 offset:36864
	ds_read_b128 v[36:39], v135 offset:37888
	ds_read_b128 v[40:43], v135 offset:38912
	ds_read_b128 v[44:47], v135 offset:39936
	s_addc_u32 s55, s19, 0
	s_nop 0
	v_mov_b32_e32 v64, v133
	s_nop 0
	s_waitcnt lgkmcnt(8)
	s_barrier
	s_waitcnt lgkmcnt(0)
	s_setprio 1
	s_waitcnt lgkmcnt(0)
	v_mfma_scale_f32_16x16x128_f8f6f4 v[124:127], v[0:7], v[16:23], v[124:127], v136, v136 op_sel_hi:[0,0,0]
	s_mov_b32 m0, s26
	v_mfma_scale_f32_16x16x128_f8f6f4 v[120:123], v[8:15], v[16:23], v[120:123], v136, v136 op_sel_hi:[0,0,0]
	global_load_lds_dwordx4 v132, s[54:55]
	v_mfma_scale_f32_16x16x128_f8f6f4 v[116:119], v[0:7], v[24:31], v[116:119], v136, v136 op_sel_hi:[0,0,0]
	s_mov_b32 m0, s27
	v_mfma_scale_f32_16x16x128_f8f6f4 v[112:115], v[8:15], v[24:31], v[112:115], v136, v136 op_sel_hi:[0,0,0]
	global_load_lds_dwordx4 v133, s[54:55]
	v_mfma_scale_f32_16x16x128_f8f6f4 v[108:111], v[0:7], v[32:39], v[188:191], v136, v136 op_sel_hi:[0,0,0]
	v_mfma_scale_f32_16x16x128_f8f6f4 v[104:107], v[8:15], v[32:39], v[192:195], v136, v136 op_sel_hi:[0,0,0]
	v_mfma_scale_f32_16x16x128_f8f6f4 v[100:103], v[0:7], v[40:47], v[196:199], v136, v136 op_sel_hi:[0,0,0]
	v_mfma_scale_f32_16x16x128_f8f6f4 v[96:99], v[8:15], v[40:47], v[200:203], v136, v136 op_sel_hi:[0,0,0]
	s_setprio 0
	s_barrier
	v_mov_b32_e32 v128, v132
	ds_read_b128 v[140:143], v139
	ds_read_b128 v[144:147], v139 offset:1024
	ds_read_b128 v[148:151], v139 offset:2048
	ds_read_b128 v[152:155], v139 offset:3072
	v_lshl_add_u64 v[64:65], s[16:17], 0, v[128:129]
	v_lshl_add_u64 v[64:65], v[64:65], 0, s[4:5]
	v_mov_b32_e32 v128, v133
	v_lshl_add_u64 v[64:65], s[16:17], 0, v[128:129]
	v_lshl_add_u64 v[64:65], v[64:65], 0, s[4:5]
	s_barrier
	s_waitcnt lgkmcnt(0)
	s_setprio 1
	s_waitcnt lgkmcnt(0)
	v_mfma_scale_f32_16x16x128_f8f6f4 v[92:95], v[140:147], v[16:23], v[204:207], v136, v136 op_sel_hi:[0,0,0]
	s_add_u32 s98, s16, s4
	s_addc_u32 s99, s17, s5
	s_mov_b32 m0, s45
	v_mfma_scale_f32_16x16x128_f8f6f4 v[88:91], v[148:155], v[16:23], v[156:159], v136, v136 op_sel_hi:[0,0,0]
	global_load_lds_dwordx4 v132, s[98:99]
	v_mfma_scale_f32_16x16x128_f8f6f4 v[84:87], v[140:147], v[24:31], v[160:163], v136, v136 op_sel_hi:[0,0,0]
	s_mov_b32 m0, s46
	v_mfma_scale_f32_16x16x128_f8f6f4 v[80:83], v[148:155], v[24:31], v[164:167], v136, v136 op_sel_hi:[0,0,0]
	global_load_lds_dwordx4 v133, s[98:99]
	v_mfma_scale_f32_16x16x128_f8f6f4 v[76:79], v[140:147], v[32:39], v[168:171], v136, v136 op_sel_hi:[0,0,0]
	v_mfma_scale_f32_16x16x128_f8f6f4 v[72:75], v[148:155], v[32:39], v[172:175], v136, v136 op_sel_hi:[0,0,0]
	v_mfma_scale_f32_16x16x128_f8f6f4 v[68:71], v[140:147], v[40:47], v[176:179], v136, v136 op_sel_hi:[0,0,0]
	v_mfma_scale_f32_16x16x128_f8f6f4 v[64:67], v[148:155], v[40:47], v[180:183], v136, v136 op_sel_hi:[0,0,0]
	s_setprio 0
	v_mov_b32_e32 v128, v132
	s_barrier
	ds_read_b128 v[16:19], v135 offset:49152
	ds_read_b128 v[20:23], v135 offset:50176
	ds_read_b128 v[156:159], v135 offset:51200
	ds_read_b128 v[160:163], v135 offset:52224
	ds_read_b128 v[164:167], v135 offset:53248
	ds_read_b128 v[168:171], v135 offset:54272
	ds_read_b128 v[172:175], v135 offset:55296
	ds_read_b128 v[176:179], v135 offset:56320
	v_lshl_add_u64 v[24:25], s[18:19], 0, v[128:129]
	v_lshl_add_u64 v[24:25], v[24:25], 0, s[4:5]
	v_mov_b32_e32 v128, v133
	v_lshl_add_u64 v[24:25], s[18:19], 0, v[128:129]
	v_lshl_add_u64 v[24:25], v[24:25], 0, s[4:5]
	s_barrier
	s_waitcnt lgkmcnt(0)
	s_setprio 1
	s_waitcnt lgkmcnt(0)
	v_mfma_scale_f32_16x16x128_f8f6f4 v[60:63], v[0:7], v[16:23], v[60:63], v136, v136 op_sel_hi:[0,0,0]
	s_add_u32 s98, s18, s4
	s_addc_u32 s99, s19, s5
	s_mov_b32 m0, s35
	v_mfma_scale_f32_16x16x128_f8f6f4 v[56:59], v[8:15], v[16:23], v[56:59], v136, v136 op_sel_hi:[0,0,0]
	global_load_lds_dwordx4 v132, s[98:99]
	v_mfma_scale_f32_16x16x128_f8f6f4 v[52:55], v[0:7], v[156:163], v[52:55], v136, v136 op_sel_hi:[0,0,0]
	s_mov_b32 m0, s36
	v_mfma_scale_f32_16x16x128_f8f6f4 v[48:51], v[8:15], v[156:163], v[48:51], v136, v136 op_sel_hi:[0,0,0]
	global_load_lds_dwordx4 v133, s[98:99]
	v_mfma_scale_f32_16x16x128_f8f6f4 v[44:47], v[0:7], v[164:171], v[184:187], v136, v136 op_sel_hi:[0,0,0]
	v_mfma_scale_f32_16x16x128_f8f6f4 v[40:43], v[8:15], v[164:171], v[208:211], v136, v136 op_sel_hi:[0,0,0]
	v_mfma_scale_f32_16x16x128_f8f6f4 v[36:39], v[0:7], v[172:179], v[212:215], v136, v136 op_sel_hi:[0,0,0]
	v_mfma_scale_f32_16x16x128_f8f6f4 v[32:35], v[8:15], v[172:179], v[216:219], v136, v136 op_sel_hi:[0,0,0]
	s_setprio 0
	s_barrier
	s_add_u32 s16, s16, 0x30080
	s_addc_u32 s17, s17, 0
	v_mov_b32_e32 v0, v132
	s_add_i32 s18, s44, s23
	s_nop 0
	v_mov_b32_e32 v0, v133
	s_nop 0
	s_waitcnt vmcnt(4)
	s_barrier
	s_setprio 1
	v_mfma_scale_f32_16x16x128_f8f6f4 v[28:31], v[140:147], v[16:23], v[220:223], v136, v136 op_sel_hi:[0,0,0]
	s_mov_b32 m0, s18
	v_mfma_scale_f32_16x16x128_f8f6f4 v[24:27], v[148:155], v[16:23], v[224:227], v136, v136 op_sel_hi:[0,0,0]
	global_load_lds_dwordx4 v132, s[16:17]
	v_mfma_scale_f32_16x16x128_f8f6f4 v[20:23], v[140:147], v[156:163], v[228:231], v136, v136 op_sel_hi:[0,0,0]
	s_add_i32 m0, s18, 0x2000
	v_mfma_scale_f32_16x16x128_f8f6f4 v[16:19], v[148:155], v[156:163], v[232:235], v136, v136 op_sel_hi:[0,0,0]
	global_load_lds_dwordx4 v133, s[16:17]
	v_mfma_scale_f32_16x16x128_f8f6f4 v[12:15], v[140:147], v[164:171], v[236:239], v136, v136 op_sel_hi:[0,0,0]
	v_mfma_scale_f32_16x16x128_f8f6f4 v[8:11], v[148:155], v[164:171], v[240:243], v136, v136 op_sel_hi:[0,0,0]
	v_mfma_scale_f32_16x16x128_f8f6f4 v[4:7], v[140:147], v[172:179], v[244:247], v136, v136 op_sel_hi:[0,0,0]
	v_mfma_scale_f32_16x16x128_f8f6f4 v[0:3], v[148:155], v[172:179], v[248:251], v136, v136 op_sel_hi:[0,0,0]
	s_setprio 0
	s_add_i32 s53, s53, 2
	s_add_u32 s14, s14, 0x100
	s_addc_u32 s15, s15, 0
	s_add_u32 s51, s51, 0x100
	s_addc_u32 s52, s52, 0
	s_cmp_gt_u32 s53, 9
	s_barrier
	s_cbranch_scc0 .LBB0_5813
	v_pk_mul_f32 v[140:141], v[124:125], s[6:7] op_sel_hi:[1,0]
	v_pk_mul_f32 v[120:121], v[120:121], s[6:7] op_sel_hi:[1,0]
	v_mov_b32_e32 v125, v129
	v_cvt_pk_fp8_f32 v125, v120, v121
	v_pk_mul_f32 v[120:121], v[126:127], s[6:7] op_sel_hi:[1,0]
	v_pk_mul_f32 v[116:117], v[116:117], s[6:7] op_sel_hi:[1,0]
	v_mov_b32_e32 v126, v129
	v_cvt_pk_fp8_f32 v126, v116, v117
	v_pk_mul_f32 v[112:113], v[112:113], s[6:7] op_sel_hi:[1,0]
	v_mov_b32_e32 v127, v129
	v_cvt_pk_fp8_f32 v127, v112, v113
	v_pk_mul_f32 v[112:113], v[118:119], s[6:7] op_sel_hi:[1,0]
	v_pk_mul_f32 v[104:105], v[104:105], s[6:7] op_sel_hi:[1,0]
	v_cvt_pk_fp8_f32 v126, v112, v113 op_sel:[0,0,1]
	v_pk_mul_f32 v[112:113], v[114:115], s[6:7] op_sel_hi:[1,0]
	v_pk_mul_f32 v[100:101], v[100:101], s[6:7] op_sel_hi:[1,0]
	v_cvt_pk_fp8_f32 v127, v112, v113 op_sel:[0,0,1]
	v_pk_mul_f32 v[112:113], v[108:109], s[6:7] op_sel_hi:[1,0]
	v_mov_b32_e32 v109, v129
	v_cvt_pk_fp8_f32 v109, v104, v105
	v_pk_mul_f32 v[104:105], v[110:111], s[6:7] op_sel_hi:[1,0]
	v_mov_b32_e32 v110, v129
	v_cvt_pk_fp8_f32 v110, v100, v101
	v_pk_mul_f32 v[100:101], v[92:93], s[6:7] op_sel_hi:[1,0]
	v_pk_mul_f32 v[88:89], v[88:89], s[6:7] op_sel_hi:[1,0]
	v_mov_b32_e32 v93, v129
	v_cvt_pk_fp8_f32 v93, v88, v89
	v_pk_mul_f32 v[88:89], v[94:95], s[6:7] op_sel_hi:[1,0]
	v_pk_mul_f32 v[84:85], v[84:85], s[6:7] op_sel_hi:[1,0]
	v_mov_b32_e32 v94, v129
	v_cvt_pk_fp8_f32 v94, v84, v85
	v_pk_mul_f32 v[80:81], v[80:81], s[6:7] op_sel_hi:[1,0]
	v_mov_b32_e32 v95, v129
	v_cvt_pk_fp8_f32 v95, v80, v81
	v_pk_mul_f32 v[80:81], v[86:87], s[6:7] op_sel_hi:[1,0]
	v_pk_mul_f32 v[72:73], v[72:73], s[6:7] op_sel_hi:[1,0]
	v_cvt_pk_fp8_f32 v94, v80, v81 op_sel:[0,0,1]
	v_pk_mul_f32 v[80:81], v[82:83], s[6:7] op_sel_hi:[1,0]
	v_pk_mul_f32 v[68:69], v[68:69], s[6:7] op_sel_hi:[1,0]
	v_cvt_pk_fp8_f32 v95, v80, v81 op_sel:[0,0,1]
	v_pk_mul_f32 v[80:81], v[76:77], s[6:7] op_sel_hi:[1,0]
	v_mov_b32_e32 v77, v129
	v_cvt_pk_fp8_f32 v77, v72, v73
	v_pk_mul_f32 v[72:73], v[78:79], s[6:7] op_sel_hi:[1,0]
	v_mov_b32_e32 v78, v129
	v_cvt_pk_fp8_f32 v78, v68, v69
	v_pk_mul_f32 v[64:65], v[64:65], s[6:7] op_sel_hi:[1,0]
	v_mov_b32_e32 v79, v129
	v_cvt_pk_fp8_f32 v79, v64, v65
	v_pk_mul_f32 v[64:65], v[70:71], s[6:7] op_sel_hi:[1,0]
	v_pk_mul_f32 v[56:57], v[56:57], s[6:7] op_sel_hi:[1,0]
	v_cvt_pk_fp8_f32 v78, v64, v65 op_sel:[0,0,1]
	v_pk_mul_f32 v[64:65], v[66:67], s[6:7] op_sel_hi:[1,0]
	v_pk_mul_f32 v[52:53], v[52:53], s[6:7] op_sel_hi:[1,0]
	v_cvt_pk_fp8_f32 v79, v64, v65 op_sel:[0,0,1]
	v_pk_mul_f32 v[64:65], v[60:61], s[6:7] op_sel_hi:[1,0]
	v_mov_b32_e32 v61, v129
	v_cvt_pk_fp8_f32 v61, v56, v57
	v_pk_mul_f32 v[56:57], v[62:63], s[6:7] op_sel_hi:[1,0]
	v_mov_b32_e32 v62, v129
	v_cvt_pk_fp8_f32 v62, v52, v53
	v_pk_mul_f32 v[48:49], v[48:49], s[6:7] op_sel_hi:[1,0]
	v_mov_b32_e32 v63, v129
	v_cvt_pk_fp8_f32 v63, v48, v49
	s_lshl_b32 s14, s49, 8
	v_pk_mul_f32 v[48:49], v[54:55], s[6:7] op_sel_hi:[1,0]
	s_add_i32 s14, s14, s33
	v_cvt_pk_fp8_f32 v62, v48, v49 op_sel:[0,0,1]
	v_pk_mul_f32 v[48:49], v[50:51], s[6:7] op_sel_hi:[1,0]
	s_lshl_b32 s16, s50, 8
	s_ashr_i32 s15, s14, 31
	v_cvt_pk_fp8_f32 v63, v48, v49 op_sel:[0,0,1]
	v_pk_mul_f32 v[48:49], v[44:45], s[6:7] op_sel_hi:[1,0]
	v_pk_mul_f32 v[40:41], v[40:41], s[6:7] op_sel_hi:[1,0]
	v_mov_b32_e32 v45, v129
	s_ashr_i32 s17, s16, 31
	s_lshl_b64 s[18:19], s[14:15], 11
	v_cvt_pk_fp8_f32 v45, v40, v41
	v_pk_mul_f32 v[40:41], v[46:47], s[6:7] op_sel_hi:[1,0]
	v_pk_mul_f32 v[36:37], v[36:37], s[6:7] op_sel_hi:[1,0]
	v_mov_b32_e32 v46, v129
	s_add_u32 s15, s30, s18
	v_cvt_pk_fp8_f32 v46, v36, v37
	v_pk_mul_f32 v[36:37], v[28:29], s[6:7] op_sel_hi:[1,0]
	v_pk_mul_f32 v[24:25], v[24:25], s[6:7] op_sel_hi:[1,0]
	v_mov_b32_e32 v29, v129
	s_addc_u32 s18, s31, s19
	v_cvt_pk_fp8_f32 v29, v24, v25
	v_pk_mul_f32 v[24:25], v[30:31], s[6:7] op_sel_hi:[1,0]
	v_pk_mul_f32 v[20:21], v[20:21], s[6:7] op_sel_hi:[1,0]
	v_mov_b32_e32 v30, v129
	s_add_u32 s15, s15, s16
	v_cvt_pk_fp8_f32 v30, v20, v21
	v_pk_mul_f32 v[16:17], v[16:17], s[6:7] op_sel_hi:[1,0]
	v_mov_b32_e32 v31, v129
	s_addc_u32 s19, s18, s17
	v_cvt_pk_fp8_f32 v31, v16, v17
	s_add_u32 s18, s15, s34
	s_addc_u32 s19, s19, 0
	s_addk_i32 s14, 0x80
	v_pk_mul_f32 v[16:17], v[22:23], s[6:7] op_sel_hi:[1,0]
	s_ashr_i32 s15, s14, 31
	v_cvt_pk_fp8_f32 v30, v16, v17 op_sel:[0,0,1]
	v_pk_mul_f32 v[16:17], v[18:19], s[6:7] op_sel_hi:[1,0]
	v_mov_b32_e32 v124, v129
	v_mov_b32_e32 v108, v129
	v_pk_mul_f32 v[96:97], v[96:97], s[6:7] op_sel_hi:[1,0]
	v_mov_b32_e32 v111, v129
	v_mov_b32_e32 v92, v129
	s_lshl_b64 s[14:15], s[14:15], 11
	v_mov_b32_e32 v60, v129
	v_mov_b32_e32 v44, v129
	v_mov_b32_e32 v28, v129
	v_cvt_pk_fp8_f32 v31, v16, v17 op_sel:[0,0,1]
	v_pk_mul_f32 v[16:17], v[12:13], s[6:7] op_sel_hi:[1,0]
	v_pk_mul_f32 v[8:9], v[8:9], s[6:7] op_sel_hi:[1,0]
	v_mov_b32_e32 v13, v129
	v_mbcnt_lo_u32_b32 v128, -1, 0
	v_mbcnt_hi_u32_b32 v128, -1, v128
	v_cvt_pk_fp8_f32 v124, v140, v141
	v_ashrrev_i32_e32 v130, 1, v128
	v_cvt_pk_fp8_f32 v108, v112, v113
	v_cvt_pk_fp8_f32 v111, v96, v97
	v_cvt_pk_fp8_f32 v92, v100, v101
	v_mov_b32_e32 v76, v129
	v_cvt_pk_fp8_f32 v60, v64, v65
	v_cvt_pk_fp8_f32 v44, v48, v49
	v_pk_mul_f32 v[32:33], v[32:33], s[6:7] op_sel_hi:[1,0]
	v_mov_b32_e32 v47, v129
	s_add_u32 s14, s30, s14
	v_cvt_pk_fp8_f32 v28, v36, v37
	v_mov_b32_e32 v12, v129
	v_cvt_pk_fp8_f32 v13, v8, v9
	v_pk_mul_f32 v[8:9], v[14:15], s[6:7] op_sel_hi:[1,0]
	v_pk_mul_f32 v[4:5], v[4:5], s[6:7] op_sel_hi:[1,0]
	v_mov_b32_e32 v14, v129
	v_bfi_b32 v130, -16, v130, v128
	v_cvt_pk_fp8_f32 v76, v80, v81
	v_cvt_pk_fp8_f32 v47, v32, v33
	s_addc_u32 s15, s31, s15
	v_cvt_pk_fp8_f32 v12, v16, v17
	v_cvt_pk_fp8_f32 v14, v4, v5
	v_pk_mul_f32 v[0:1], v[0:1], s[6:7] op_sel_hi:[1,0]
	v_mov_b32_e32 v15, v129
	v_ashrrev_i32_e32 v131, 31, v130
	v_pk_mul_f32 v[96:97], v[102:103], s[6:7] op_sel_hi:[1,0]
	s_add_u32 s14, s14, s16
	v_cvt_pk_fp8_f32 v15, v0, v1
	v_lshlrev_b64 v[130:131], 11, v[130:131]
	v_cvt_pk_fp8_f32 v110, v96, v97 op_sel:[0,0,1]
	v_pk_mul_f32 v[96:97], v[98:99], s[6:7] op_sel_hi:[1,0]
	v_pk_mul_f32 v[32:33], v[38:39], s[6:7] op_sel_hi:[1,0]
	s_addc_u32 s15, s15, s17
	v_and_b32_e32 v128, 16, v128
	v_cvt_pk_fp8_f32 v124, v120, v121 op_sel:[0,0,1]
	v_pk_mul_f32 v[120:121], v[122:123], s[6:7] op_sel_hi:[1,0]
	v_cvt_pk_fp8_f32 v108, v104, v105 op_sel:[0,0,1]
	v_pk_mul_f32 v[104:105], v[106:107], s[6:7] op_sel_hi:[1,0]
	v_cvt_pk_fp8_f32 v111, v96, v97 op_sel:[0,0,1]
	v_lshl_add_u64 v[96:97], s[18:19], 0, v[130:131]
	v_cvt_pk_fp8_f32 v92, v88, v89 op_sel:[0,0,1]
	v_pk_mul_f32 v[88:89], v[90:91], s[6:7] op_sel_hi:[1,0]
	v_cvt_pk_fp8_f32 v60, v56, v57 op_sel:[0,0,1]
	v_pk_mul_f32 v[56:57], v[58:59], s[6:7] op_sel_hi:[1,0]
	v_cvt_pk_fp8_f32 v44, v40, v41 op_sel:[0,0,1]
	v_pk_mul_f32 v[40:41], v[42:43], s[6:7] op_sel_hi:[1,0]
	v_cvt_pk_fp8_f32 v46, v32, v33 op_sel:[0,0,1]
	v_pk_mul_f32 v[32:33], v[34:35], s[6:7] op_sel_hi:[1,0]
	s_add_u32 s14, s14, s34
	v_cvt_pk_fp8_f32 v28, v24, v25 op_sel:[0,0,1]
	v_pk_mul_f32 v[24:25], v[26:27], s[6:7] op_sel_hi:[1,0]
	v_pk_mul_f32 v[0:1], v[6:7], s[6:7] op_sel_hi:[1,0]
	v_cvt_pk_fp8_f32 v125, v120, v121 op_sel:[0,0,1]
	v_cvt_pk_fp8_f32 v109, v104, v105 op_sel:[0,0,1]
	v_lshl_add_u64 v[96:97], v[96:97], 0, v[128:129]
	v_cvt_pk_fp8_f32 v93, v88, v89 op_sel:[0,0,1]
	v_cvt_pk_fp8_f32 v76, v72, v73 op_sel:[0,0,1]
	v_pk_mul_f32 v[72:73], v[74:75], s[6:7] op_sel_hi:[1,0]
	v_cvt_pk_fp8_f32 v61, v56, v57 op_sel:[0,0,1]
	v_cvt_pk_fp8_f32 v45, v40, v41 op_sel:[0,0,1]
	v_cvt_pk_fp8_f32 v47, v32, v33 op_sel:[0,0,1]
	s_addc_u32 s15, s15, 0
	v_cvt_pk_fp8_f32 v29, v24, v25 op_sel:[0,0,1]
	v_cvt_pk_fp8_f32 v12, v8, v9 op_sel:[0,0,1]
	v_pk_mul_f32 v[8:9], v[10:11], s[6:7] op_sel_hi:[1,0]
	v_cvt_pk_fp8_f32 v14, v0, v1 op_sel:[0,0,1]
	v_pk_mul_f32 v[0:1], v[2:3], s[6:7] op_sel_hi:[1,0]
	v_add_co_u32_e32 v98, vcc, s29, v96
	v_cvt_pk_fp8_f32 v77, v72, v73 op_sel:[0,0,1]
	v_lshl_add_u64 v[32:33], s[14:15], 0, v[130:131]
	v_cvt_pk_fp8_f32 v13, v8, v9 op_sel:[0,0,1]
	v_cvt_pk_fp8_f32 v15, v0, v1 op_sel:[0,0,1]
	v_addc_co_u32_e32 v99, vcc, 0, v97, vcc
	v_lshl_add_u64 v[32:33], v[32:33], 0, v[128:129]
	v_add_co_u32_e32 v34, vcc, s29, v32
	v_permlane32_swap_b32_e32 v124, v126
	v_permlane32_swap_b32_e32 v125, v127
	v_permlane32_swap_b32_e32 v108, v110
	v_permlane32_swap_b32_e32 v109, v111
	v_permlane32_swap_b32_e32 v92, v94
	v_permlane32_swap_b32_e32 v93, v95
	v_permlane32_swap_b32_e32 v60, v62
	v_permlane32_swap_b32_e32 v61, v63
	v_permlane32_swap_b32_e32 v44, v46
	v_permlane32_swap_b32_e32 v45, v47
	v_addc_co_u32_e32 v35, vcc, 0, v33, vcc
	v_permlane32_swap_b32_e32 v28, v30
	v_permlane32_swap_b32_e32 v29, v31
	v_permlane16_swap_b32_e32 v124, v125
	v_permlane16_swap_b32_e32 v126, v127
	v_permlane16_swap_b32_e32 v108, v109
	v_permlane16_swap_b32_e32 v110, v111
	v_permlane16_swap_b32_e32 v92, v93
	v_permlane16_swap_b32_e32 v94, v95
	v_permlane32_swap_b32_e32 v76, v78
	v_permlane32_swap_b32_e32 v77, v79
	v_permlane16_swap_b32_e32 v60, v61
	v_permlane16_swap_b32_e32 v62, v63
	v_permlane16_swap_b32_e32 v44, v45
	v_permlane16_swap_b32_e32 v46, v47
	v_permlane16_swap_b32_e32 v28, v29
	v_permlane16_swap_b32_e32 v30, v31
	v_permlane32_swap_b32_e32 v12, v14
	v_permlane32_swap_b32_e32 v13, v15
	s_and_b64 vcc, exec, s[8:9]
	s_mov_b32 s50, s48
	s_mov_b32 s49, s47
	s_mov_b64 s[16:17], s[10:11]
	s_mov_b64 s[14:15], s[12:13]
	global_store_dwordx4 v[96:97], v[124:127], off
	global_store_dwordx4 v[98:99], v[108:111], off
	v_permlane16_swap_b32_e32 v76, v77
	v_permlane16_swap_b32_e32 v78, v79
	global_store_dwordx4 v[96:97], v[92:95], off offset:128
	global_store_dwordx4 v[98:99], v[76:79], off offset:128
	global_store_dwordx4 v[32:33], v[60:63], off
	global_store_dwordx4 v[34:35], v[44:47], off
	v_permlane16_swap_b32_e32 v12, v13
	v_permlane16_swap_b32_e32 v14, v15
	global_store_dwordx4 v[32:33], v[28:31], off offset:128
	global_store_dwordx4 v[34:35], v[12:15], off offset:128
	s_cbranch_vccz .LBB0_5808
	s_waitcnt vmcnt(0)
	v_readlane_b32 s0, v252, 2
	s_cmpk_gt_u32 s0, 0xff
	s_cbranch_scc1 .LBB0_5817
	s_barrier
